# v13 + load segments at s_setprio 3, compute segments at 0 in all GEMM K-loops
# baseline (speedup 1.0000x reference)
.LBB0_286:
	s_lshl_b32 s10, s51, 19
	s_add_u32 s10, s20, s10
	s_addc_u32 s11, s21, 0
	s_and_b64 s[16:17], s[4:5], exec
	s_cselect_b32 s54, s11, s31
	s_cselect_b32 s55, s10, s30
	s_lshl_b32 s14, s50, 19
	s_add_u32 s16, s15, s14
	s_addc_u32 s17, s26, 0
	s_and_b64 s[36:37], s[4:5], exec
	s_cselect_b32 s56, s17, s23
	s_cselect_b32 s57, s16, s22
	s_add_i32 s60, 0, 0x10000
	v_add_u32_e32 v198, s60, v196
	s_add_i32 s62, 0, 0x14000
	v_add_u32_e32 v199, s62, v196
	ds_read_b128 v[160:163], v198
	ds_read_b128 v[152:155], v198 offset:1024
	ds_read_b128 v[156:159], v198 offset:2048
	ds_read_b128 v[148:151], v198 offset:3072
	ds_read_b128 v[144:147], v199
	ds_read_b128 v[136:139], v199 offset:1024
	ds_read_b128 v[140:143], v199 offset:2048
	ds_read_b128 v[132:135], v199 offset:3072
	s_add_u32 s36, s30, 0x40080
	s_addc_u32 s37, s31, 0
	s_add_i32 s58, s41, 0xc000
	v_lshl_add_u64 v[174:175], s[36:37], 0, v[168:169]
	s_mov_b32 m0, s58
	s_add_i32 s59, s41, 0xe000
	ds_read_b128 v[178:181], v197
	ds_read_b128 v[182:185], v197 offset:1024
	ds_read_b128 v[190:193], v197 offset:2048
	ds_read_b128 v[200:203], v197 offset:3072
	ds_read_b128 v[204:207], v197 offset:4096
	ds_read_b128 v[208:211], v197 offset:5120
	ds_read_b128 v[212:215], v197 offset:6144
	ds_read_b128 v[216:219], v197 offset:7168
	global_load_lds_dwordx4 v[174:175], off
	v_lshl_add_u64 v[174:175], s[36:37], 0, v[166:167]
	s_mov_b32 m0, s59
	s_nop 0
	global_load_lds_dwordx4 v[174:175], off
	s_waitcnt vmcnt(8)
	s_waitcnt lgkmcnt(0)
	s_barrier
	s_setprio 0
	s_waitcnt lgkmcnt(0)
	v_mfma_f32_16x16x32_bf16 v[128:131], v[160:163], v[178:181], 0
	v_mfma_f32_16x16x32_bf16 v[124:127], v[156:159], v[178:181], 0
	v_mfma_f32_16x16x32_bf16 v[116:119], v[156:159], v[190:193], 0
	v_mfma_f32_16x16x32_bf16 v[120:123], v[160:163], v[190:193], 0
	v_mfma_f32_16x16x32_bf16 v[112:115], v[160:163], v[204:207], 0
	v_mfma_f32_16x16x32_bf16 v[108:111], v[156:159], v[204:207], 0
	v_mfma_f32_16x16x32_bf16 v[100:103], v[156:159], v[212:215], 0
	v_mfma_f32_16x16x32_bf16 v[104:107], v[160:163], v[212:215], 0
	s_nop 0
	v_mfma_f32_16x16x32_bf16 v[128:131], v[152:155], v[182:185], v[128:131]
	v_mfma_f32_16x16x32_bf16 v[124:127], v[148:151], v[182:185], v[124:127]
	v_mfma_f32_16x16x32_bf16 v[116:119], v[148:151], v[200:203], v[116:119]
	v_mfma_f32_16x16x32_bf16 v[120:123], v[152:155], v[200:203], v[120:123]
	v_mfma_f32_16x16x32_bf16 v[112:115], v[152:155], v[208:211], v[112:115]
	v_mfma_f32_16x16x32_bf16 v[108:111], v[148:151], v[208:211], v[108:111]
	v_mfma_f32_16x16x32_bf16 v[100:103], v[148:151], v[216:219], v[100:103]
	v_mfma_f32_16x16x32_bf16 v[104:107], v[152:155], v[216:219], v[104:107]
	s_setprio 3
	s_setprio 0
	v_mfma_f32_16x16x32_bf16 v[96:99], v[144:147], v[178:181], 0
	v_mfma_f32_16x16x32_bf16 v[92:95], v[140:143], v[178:181], 0
	v_mfma_f32_16x16x32_bf16 v[84:87], v[140:143], v[190:193], 0
	v_mfma_f32_16x16x32_bf16 v[88:91], v[144:147], v[190:193], 0
	v_mfma_f32_16x16x32_bf16 v[80:83], v[144:147], v[204:207], 0
	v_mfma_f32_16x16x32_bf16 v[76:79], v[140:143], v[204:207], 0
	v_mfma_f32_16x16x32_bf16 v[68:71], v[140:143], v[212:215], 0
	v_mfma_f32_16x16x32_bf16 v[72:75], v[144:147], v[212:215], 0
	s_nop 0
	v_mfma_f32_16x16x32_bf16 v[96:99], v[136:139], v[182:185], v[96:99]
	v_mfma_f32_16x16x32_bf16 v[92:95], v[132:135], v[182:185], v[92:95]
	v_mfma_f32_16x16x32_bf16 v[84:87], v[132:135], v[200:203], v[84:87]
	v_mfma_f32_16x16x32_bf16 v[88:91], v[136:139], v[200:203], v[88:91]
	v_mfma_f32_16x16x32_bf16 v[80:83], v[136:139], v[208:211], v[80:83]
	v_mfma_f32_16x16x32_bf16 v[76:79], v[132:135], v[208:211], v[76:79]
	v_mfma_f32_16x16x32_bf16 v[68:71], v[132:135], v[216:219], v[68:71]
	v_mfma_f32_16x16x32_bf16 v[72:75], v[136:139], v[216:219], v[72:75]
	s_setprio 3
	s_barrier
	v_lshl_add_u64 v[174:175], s[22:23], 0, v[34:35]
	s_add_i32 s60, s60, s40
	v_lshl_add_u64 v[190:191], v[174:175], 0, s[28:29]
	s_mov_b32 m0, s60
	s_add_i32 s61, s60, 0x2000
	ds_read_b128 v[178:181], v197 offset:16384
	ds_read_b128 v[182:185], v197 offset:17408
	ds_read_b128 v[200:203], v197 offset:18432
	ds_read_b128 v[204:207], v197 offset:19456
	ds_read_b128 v[208:211], v197 offset:20480
	ds_read_b128 v[212:215], v197 offset:21504
	ds_read_b128 v[216:219], v197 offset:22528
	ds_read_b128 v[222:225], v197 offset:23552
	global_load_lds_dwordx4 v[190:191], off
	v_lshl_add_u64 v[190:191], s[22:23], 0, v[164:165]
	s_add_u32 s36, s22, 0x40100
	v_lshl_add_u64 v[192:193], v[190:191], 0, s[28:29]
	s_mov_b32 m0, s61
	s_addc_u32 s37, s23, 0
	s_add_i32 s62, s62, s40
	global_load_lds_dwordx4 v[192:193], off
	v_lshl_add_u64 v[192:193], s[36:37], 0, v[34:35]
	s_mov_b32 m0, s62
	s_add_i32 s63, s62, 0x2000
	global_load_lds_dwordx4 v[192:193], off
	v_lshl_add_u64 v[192:193], s[36:37], 0, v[164:165]
	s_mov_b32 m0, s63
	s_nop 0
	global_load_lds_dwordx4 v[192:193], off
	v_lshl_add_u64 v[192:193], s[30:31], 0, v[168:169]
	v_lshl_add_u64 v[194:195], v[192:193], 0, s[28:29]
	s_mov_b32 m0, s41
	s_nop 0
	global_load_lds_dwordx4 v[194:195], off
	v_lshl_add_u64 v[194:195], s[30:31], 0, v[166:167]
	v_lshl_add_u64 v[226:227], v[194:195], 0, s[28:29]
	s_mov_b32 m0, s42
	s_nop 0
	global_load_lds_dwordx4 v[226:227], off
	s_waitcnt vmcnt(8)
	s_waitcnt lgkmcnt(0)
	s_barrier
	s_setprio 0
	s_waitcnt lgkmcnt(0)
	v_mfma_f32_16x16x32_bf16 v[64:67], v[160:163], v[178:181], 0
	v_mfma_f32_16x16x32_bf16 v[60:63], v[156:159], v[178:181], 0
	v_mfma_f32_16x16x32_bf16 v[52:55], v[156:159], v[200:203], 0
	v_mfma_f32_16x16x32_bf16 v[56:59], v[160:163], v[200:203], 0
	v_mfma_f32_16x16x32_bf16 v[48:51], v[160:163], v[208:211], 0
	v_mfma_f32_16x16x32_bf16 v[44:47], v[156:159], v[208:211], 0
	v_mfma_f32_16x16x32_bf16 v[36:39], v[156:159], v[216:219], 0
	v_mfma_f32_16x16x32_bf16 v[40:43], v[160:163], v[216:219], 0
	s_nop 0
	v_mfma_f32_16x16x32_bf16 v[64:67], v[152:155], v[182:185], v[64:67]
	v_mfma_f32_16x16x32_bf16 v[60:63], v[148:151], v[182:185], v[60:63]
	v_mfma_f32_16x16x32_bf16 v[52:55], v[148:151], v[204:207], v[52:55]
	v_mfma_f32_16x16x32_bf16 v[56:59], v[152:155], v[204:207], v[56:59]
	v_mfma_f32_16x16x32_bf16 v[48:51], v[152:155], v[212:215], v[48:51]
	v_mfma_f32_16x16x32_bf16 v[44:47], v[148:151], v[212:215], v[44:47]
	v_mfma_f32_16x16x32_bf16 v[36:39], v[148:151], v[222:225], v[36:39]
	v_mfma_f32_16x16x32_bf16 v[40:43], v[152:155], v[222:225], v[40:43]
	s_setprio 3
	s_setprio 0
	v_mfma_f32_16x16x32_bf16 v[30:33], v[144:147], v[178:181], 0
	v_mfma_f32_16x16x32_bf16 v[26:29], v[140:143], v[178:181], 0
	v_mfma_f32_16x16x32_bf16 v[18:21], v[140:143], v[200:203], 0
	v_mfma_f32_16x16x32_bf16 v[22:25], v[144:147], v[200:203], 0
	v_mfma_f32_16x16x32_bf16 v[14:17], v[144:147], v[208:211], 0
	v_mfma_f32_16x16x32_bf16 v[10:13], v[140:143], v[208:211], 0
	v_mfma_f32_16x16x32_bf16 v[2:5], v[140:143], v[216:219], 0
	v_mfma_f32_16x16x32_bf16 v[6:9], v[144:147], v[216:219], 0
	s_nop 0
	v_mfma_f32_16x16x32_bf16 v[30:33], v[136:139], v[182:185], v[30:33]
	v_mfma_f32_16x16x32_bf16 v[26:29], v[132:135], v[182:185], v[26:29]
	v_mfma_f32_16x16x32_bf16 v[18:21], v[132:135], v[204:207], v[18:21]
	v_mfma_f32_16x16x32_bf16 v[22:25], v[136:139], v[204:207], v[22:25]
	v_mfma_f32_16x16x32_bf16 v[14:17], v[136:139], v[212:215], v[14:17]
	v_mfma_f32_16x16x32_bf16 v[10:13], v[132:135], v[212:215], v[10:13]
	v_mfma_f32_16x16x32_bf16 v[2:5], v[132:135], v[222:225], v[2:5]
	v_mfma_f32_16x16x32_bf16 v[6:9], v[136:139], v[222:225], v[6:9]
	s_setprio 3
	s_barrier
	s_add_i32 s64, 0, 0x18000
	s_add_i32 s66, 0, 0x1c000
	v_add_u32_e32 v132, s64, v196
	v_add_u32_e32 v133, s66, v196
	ds_read_b128 v[134:137], v132
	ds_read_b128 v[138:141], v132 offset:1024
	ds_read_b128 v[142:145], v132 offset:2048
	ds_read_b128 v[146:149], v132 offset:3072
	ds_read_b128 v[150:153], v133
	ds_read_b128 v[154:157], v133 offset:1024
	ds_read_b128 v[158:161], v133 offset:2048
	ds_read_b128 v[178:181], v133 offset:3072
	s_add_u32 s36, s30, 0x40100
	s_addc_u32 s37, s31, 0
	s_mov_b32 m0, s43
	v_lshl_add_u64 v[162:163], s[36:37], 0, v[168:169]
	ds_read_b128 v[182:185], v197 offset:32768
	ds_read_b128 v[200:203], v197 offset:33792
	ds_read_b128 v[204:207], v197 offset:34816
	ds_read_b128 v[208:211], v197 offset:35840
	ds_read_b128 v[212:215], v197 offset:36864
	ds_read_b128 v[216:219], v197 offset:37888
	ds_read_b128 v[222:225], v197 offset:38912
	ds_read_b128 v[226:229], v197 offset:39936
	global_load_lds_dwordx4 v[162:163], off
	v_lshl_add_u64 v[162:163], s[36:37], 0, v[166:167]
	s_mov_b32 m0, s44
	s_nop 0
	global_load_lds_dwordx4 v[162:163], off
	s_waitcnt vmcnt(8)
	s_waitcnt lgkmcnt(0)
	s_barrier
	s_setprio 0
	s_waitcnt lgkmcnt(0)
	v_mfma_f32_16x16x32_bf16 v[128:131], v[134:137], v[182:185], v[128:131]
	v_mfma_f32_16x16x32_bf16 v[124:127], v[142:145], v[182:185], v[124:127]
	v_mfma_f32_16x16x32_bf16 v[116:119], v[142:145], v[204:207], v[116:119]
	v_mfma_f32_16x16x32_bf16 v[120:123], v[134:137], v[204:207], v[120:123]
	v_mfma_f32_16x16x32_bf16 v[112:115], v[134:137], v[212:215], v[112:115]
	v_mfma_f32_16x16x32_bf16 v[108:111], v[142:145], v[212:215], v[108:111]
	v_mfma_f32_16x16x32_bf16 v[100:103], v[142:145], v[222:225], v[100:103]
	v_mfma_f32_16x16x32_bf16 v[104:107], v[134:137], v[222:225], v[104:107]
	v_mfma_f32_16x16x32_bf16 v[128:131], v[138:141], v[200:203], v[128:131]
	v_mfma_f32_16x16x32_bf16 v[124:127], v[146:149], v[200:203], v[124:127]
	v_mfma_f32_16x16x32_bf16 v[116:119], v[146:149], v[208:211], v[116:119]
	v_mfma_f32_16x16x32_bf16 v[120:123], v[138:141], v[208:211], v[120:123]
	v_mfma_f32_16x16x32_bf16 v[112:115], v[138:141], v[216:219], v[112:115]
	v_mfma_f32_16x16x32_bf16 v[108:111], v[146:149], v[216:219], v[108:111]
	v_mfma_f32_16x16x32_bf16 v[100:103], v[146:149], v[226:229], v[100:103]
	v_mfma_f32_16x16x32_bf16 v[104:107], v[138:141], v[226:229], v[104:107]
	s_setprio 3
	s_setprio 0
	v_mfma_f32_16x16x32_bf16 v[96:99], v[150:153], v[182:185], v[96:99]
	v_mfma_f32_16x16x32_bf16 v[92:95], v[158:161], v[182:185], v[92:95]
	v_mfma_f32_16x16x32_bf16 v[84:87], v[158:161], v[204:207], v[84:87]
	v_mfma_f32_16x16x32_bf16 v[88:91], v[150:153], v[204:207], v[88:91]
	v_mfma_f32_16x16x32_bf16 v[80:83], v[150:153], v[212:215], v[80:83]
	v_mfma_f32_16x16x32_bf16 v[76:79], v[158:161], v[212:215], v[76:79]
	v_mfma_f32_16x16x32_bf16 v[68:71], v[158:161], v[222:225], v[68:71]
	v_mfma_f32_16x16x32_bf16 v[72:75], v[150:153], v[222:225], v[72:75]
	v_mfma_f32_16x16x32_bf16 v[96:99], v[154:157], v[200:203], v[96:99]
	v_mfma_f32_16x16x32_bf16 v[92:95], v[178:181], v[200:203], v[92:95]
	v_mfma_f32_16x16x32_bf16 v[84:87], v[178:181], v[208:211], v[84:87]
	v_mfma_f32_16x16x32_bf16 v[88:91], v[154:157], v[208:211], v[88:91]
	v_mfma_f32_16x16x32_bf16 v[80:83], v[154:157], v[216:219], v[80:83]
	v_mfma_f32_16x16x32_bf16 v[76:79], v[178:181], v[216:219], v[76:79]
	v_mfma_f32_16x16x32_bf16 v[68:71], v[178:181], v[226:229], v[68:71]
	v_mfma_f32_16x16x32_bf16 v[72:75], v[154:157], v[226:229], v[72:75]
	s_setprio 3
	s_barrier
	s_add_i32 s64, s64, s40
	s_mov_b64 s[24:25], 0x180
	s_add_i32 s65, s64, 0x2000
	v_lshl_add_u64 v[162:163], v[174:175], 0, s[24:25]
	s_mov_b32 m0, s64
	s_add_u32 s36, s22, 0x40180
	ds_read_b128 v[182:185], v197 offset:49152
	ds_read_b128 v[200:203], v197 offset:50176
	ds_read_b128 v[204:207], v197 offset:51200
	ds_read_b128 v[208:211], v197 offset:52224
	ds_read_b128 v[212:215], v197 offset:53248
	ds_read_b128 v[216:219], v197 offset:54272
	ds_read_b128 v[222:225], v197 offset:55296
	ds_read_b128 v[226:229], v197 offset:56320
	global_load_lds_dwordx4 v[162:163], off
	v_lshl_add_u64 v[162:163], v[190:191], 0, s[24:25]
	s_mov_b32 m0, s65
	s_addc_u32 s37, s23, 0
	s_add_i32 s66, s66, s40
	global_load_lds_dwordx4 v[162:163], off
	v_lshl_add_u64 v[162:163], s[36:37], 0, v[34:35]
	s_mov_b32 m0, s66
	s_add_i32 s67, s66, 0x2000
	global_load_lds_dwordx4 v[162:163], off
	v_lshl_add_u64 v[162:163], s[36:37], 0, v[164:165]
	s_mov_b32 m0, s67
	s_nop 0
	global_load_lds_dwordx4 v[162:163], off
	v_lshl_add_u64 v[162:163], v[192:193], 0, s[24:25]
	s_mov_b32 m0, s47
	s_nop 0
	global_load_lds_dwordx4 v[162:163], off
	v_lshl_add_u64 v[162:163], v[194:195], 0, s[24:25]
	s_mov_b32 m0, s48
	s_nop 0
	global_load_lds_dwordx4 v[162:163], off
	s_waitcnt vmcnt(8)
	s_waitcnt lgkmcnt(0)
	s_barrier
	s_setprio 0
	s_waitcnt lgkmcnt(0)
	v_mfma_f32_16x16x32_bf16 v[64:67], v[134:137], v[182:185], v[64:67]
	v_mfma_f32_16x16x32_bf16 v[60:63], v[142:145], v[182:185], v[60:63]
	v_mfma_f32_16x16x32_bf16 v[52:55], v[142:145], v[204:207], v[52:55]
	v_mfma_f32_16x16x32_bf16 v[56:59], v[134:137], v[204:207], v[56:59]
	v_mfma_f32_16x16x32_bf16 v[48:51], v[134:137], v[212:215], v[48:51]
	v_mfma_f32_16x16x32_bf16 v[44:47], v[142:145], v[212:215], v[44:47]
	v_mfma_f32_16x16x32_bf16 v[36:39], v[142:145], v[222:225], v[36:39]
	v_mfma_f32_16x16x32_bf16 v[40:43], v[134:137], v[222:225], v[40:43]
	v_mfma_f32_16x16x32_bf16 v[64:67], v[138:141], v[200:203], v[64:67]
	v_mfma_f32_16x16x32_bf16 v[60:63], v[146:149], v[200:203], v[60:63]
	v_mfma_f32_16x16x32_bf16 v[52:55], v[146:149], v[208:211], v[52:55]
	v_mfma_f32_16x16x32_bf16 v[56:59], v[138:141], v[208:211], v[56:59]
	v_mfma_f32_16x16x32_bf16 v[48:51], v[138:141], v[216:219], v[48:51]
	v_mfma_f32_16x16x32_bf16 v[44:47], v[146:149], v[216:219], v[44:47]
	v_mfma_f32_16x16x32_bf16 v[36:39], v[146:149], v[226:229], v[36:39]
	v_mfma_f32_16x16x32_bf16 v[40:43], v[138:141], v[226:229], v[40:43]
	s_setprio 3
	s_setprio 0
	v_mfma_f32_16x16x32_bf16 v[30:33], v[150:153], v[182:185], v[30:33]
	v_mfma_f32_16x16x32_bf16 v[26:29], v[158:161], v[182:185], v[26:29]
	v_mfma_f32_16x16x32_bf16 v[18:21], v[158:161], v[204:207], v[18:21]
	v_mfma_f32_16x16x32_bf16 v[22:25], v[150:153], v[204:207], v[22:25]
	v_mfma_f32_16x16x32_bf16 v[14:17], v[150:153], v[212:215], v[14:17]
	v_mfma_f32_16x16x32_bf16 v[10:13], v[158:161], v[212:215], v[10:13]
	v_mfma_f32_16x16x32_bf16 v[2:5], v[158:161], v[222:225], v[2:5]
	v_mfma_f32_16x16x32_bf16 v[6:9], v[150:153], v[222:225], v[6:9]
	v_mfma_f32_16x16x32_bf16 v[30:33], v[154:157], v[200:203], v[30:33]
	v_mfma_f32_16x16x32_bf16 v[26:29], v[178:181], v[200:203], v[26:29]
	v_mfma_f32_16x16x32_bf16 v[18:21], v[178:181], v[208:211], v[18:21]
	v_mfma_f32_16x16x32_bf16 v[22:25], v[154:157], v[208:211], v[22:25]
	v_mfma_f32_16x16x32_bf16 v[14:17], v[154:157], v[216:219], v[14:17]
	v_mfma_f32_16x16x32_bf16 v[10:13], v[178:181], v[216:219], v[10:13]
	v_mfma_f32_16x16x32_bf16 v[2:5], v[178:181], v[226:229], v[2:5]
	v_mfma_f32_16x16x32_bf16 v[6:9], v[154:157], v[226:229], v[6:9]
	s_setprio 3
	s_barrier
	s_add_u32 s30, s30, 0x40180
	s_addc_u32 s31, s31, 0
	s_add_u32 s68, s22, 0x200
	s_addc_u32 s69, s23, 0
	s_mov_b32 s70, 0
.LBB0_287:
	ds_read_b128 v[134:137], v198
	ds_read_b128 v[138:141], v198 offset:1024
	ds_read_b128 v[142:145], v198 offset:2048
	ds_read_b128 v[146:149], v198 offset:3072
	ds_read_b128 v[150:153], v199
	ds_read_b128 v[154:157], v199 offset:1024
	ds_read_b128 v[158:161], v199 offset:2048
	ds_read_b128 v[178:181], v199 offset:3072
	s_add_u32 s14, s30, 0xfffc0080
	s_addc_u32 s22, s31, -1
	s_cmp_eq_u32 s70, 12
	s_cselect_b32 s37, s54, s22
	s_cselect_b32 s36, s55, s14
	s_cselect_b32 s23, s56, s69
	s_cselect_b32 s22, s57, s68
	s_mov_b32 m0, s58
	v_lshl_add_u64 v[162:163], s[30:31], 0, v[170:171]
	ds_read_b128 v[182:185], v197
	ds_read_b128 v[190:193], v197 offset:1024
	ds_read_b128 v[200:203], v197 offset:2048
	ds_read_b128 v[204:207], v197 offset:3072
	ds_read_b128 v[208:211], v197 offset:4096
	ds_read_b128 v[212:215], v197 offset:5120
	ds_read_b128 v[216:219], v197 offset:6144
	ds_read_b128 v[222:225], v197 offset:7168
	global_load_lds_dwordx4 v[162:163], off
	v_lshl_add_u64 v[162:163], s[30:31], 0, v[172:173]
	s_mov_b32 m0, s59
	s_nop 0
	global_load_lds_dwordx4 v[162:163], off
	s_waitcnt vmcnt(8)
	s_waitcnt lgkmcnt(0)
	s_barrier
	s_setprio 0
	s_waitcnt lgkmcnt(0)
	v_mfma_f32_16x16x32_bf16 v[128:131], v[134:137], v[182:185], v[128:131]
	v_mfma_f32_16x16x32_bf16 v[124:127], v[142:145], v[182:185], v[124:127]
	v_mfma_f32_16x16x32_bf16 v[116:119], v[142:145], v[200:203], v[116:119]
	v_mfma_f32_16x16x32_bf16 v[120:123], v[134:137], v[200:203], v[120:123]
	v_mfma_f32_16x16x32_bf16 v[112:115], v[134:137], v[208:211], v[112:115]
	v_mfma_f32_16x16x32_bf16 v[108:111], v[142:145], v[208:211], v[108:111]
	v_mfma_f32_16x16x32_bf16 v[100:103], v[142:145], v[216:219], v[100:103]
	v_mfma_f32_16x16x32_bf16 v[104:107], v[134:137], v[216:219], v[104:107]
	v_mfma_f32_16x16x32_bf16 v[128:131], v[138:141], v[190:193], v[128:131]
	v_mfma_f32_16x16x32_bf16 v[124:127], v[146:149], v[190:193], v[124:127]
	v_mfma_f32_16x16x32_bf16 v[116:119], v[146:149], v[204:207], v[116:119]
	v_mfma_f32_16x16x32_bf16 v[120:123], v[138:141], v[204:207], v[120:123]
	v_mfma_f32_16x16x32_bf16 v[112:115], v[138:141], v[212:215], v[112:115]
	v_mfma_f32_16x16x32_bf16 v[108:111], v[146:149], v[212:215], v[108:111]
	v_mfma_f32_16x16x32_bf16 v[100:103], v[146:149], v[222:225], v[100:103]
	v_mfma_f32_16x16x32_bf16 v[104:107], v[138:141], v[222:225], v[104:107]
	s_setprio 3
	s_setprio 0
	v_mfma_f32_16x16x32_bf16 v[96:99], v[150:153], v[182:185], v[96:99]
	v_mfma_f32_16x16x32_bf16 v[92:95], v[158:161], v[182:185], v[92:95]
	v_mfma_f32_16x16x32_bf16 v[84:87], v[158:161], v[200:203], v[84:87]
	v_mfma_f32_16x16x32_bf16 v[88:91], v[150:153], v[200:203], v[88:91]
	v_mfma_f32_16x16x32_bf16 v[80:83], v[150:153], v[208:211], v[80:83]
	v_mfma_f32_16x16x32_bf16 v[76:79], v[158:161], v[208:211], v[76:79]
	v_mfma_f32_16x16x32_bf16 v[68:71], v[158:161], v[216:219], v[68:71]
	v_mfma_f32_16x16x32_bf16 v[72:75], v[150:153], v[216:219], v[72:75]
	v_mfma_f32_16x16x32_bf16 v[96:99], v[154:157], v[190:193], v[96:99]
	v_mfma_f32_16x16x32_bf16 v[92:95], v[178:181], v[190:193], v[92:95]
	v_mfma_f32_16x16x32_bf16 v[84:87], v[178:181], v[204:207], v[84:87]
	v_mfma_f32_16x16x32_bf16 v[88:91], v[154:157], v[204:207], v[88:91]
	v_mfma_f32_16x16x32_bf16 v[80:83], v[154:157], v[212:215], v[80:83]
	v_mfma_f32_16x16x32_bf16 v[76:79], v[178:181], v[212:215], v[76:79]
	v_mfma_f32_16x16x32_bf16 v[68:71], v[178:181], v[222:225], v[68:71]
	v_mfma_f32_16x16x32_bf16 v[72:75], v[154:157], v[222:225], v[72:75]
	s_setprio 3
	s_barrier
	s_mov_b32 m0, s60
	v_lshl_add_u64 v[162:163], s[22:23], 0, v[34:35]
	s_add_u32 s72, s22, 0x40000
	ds_read_b128 v[182:185], v197 offset:16384
	ds_read_b128 v[190:193], v197 offset:17408
	ds_read_b128 v[200:203], v197 offset:18432
	ds_read_b128 v[204:207], v197 offset:19456
	ds_read_b128 v[208:211], v197 offset:20480
	ds_read_b128 v[212:215], v197 offset:21504
	ds_read_b128 v[216:219], v197 offset:22528
	ds_read_b128 v[222:225], v197 offset:23552
	global_load_lds_dwordx4 v[162:163], off
	v_lshl_add_u64 v[174:175], s[22:23], 0, v[164:165]
	s_mov_b32 m0, s61
	s_addc_u32 s73, s23, 0
	global_load_lds_dwordx4 v[174:175], off
	v_lshl_add_u64 v[194:195], s[72:73], 0, v[34:35]
	s_mov_b32 m0, s62
	v_lshl_add_u64 v[226:227], s[36:37], 0, v[166:167]
	global_load_lds_dwordx4 v[194:195], off
	v_lshl_add_u64 v[194:195], s[72:73], 0, v[164:165]
	s_mov_b32 m0, s63
	s_nop 0
	global_load_lds_dwordx4 v[194:195], off
	v_lshl_add_u64 v[194:195], s[36:37], 0, v[168:169]
	s_mov_b32 m0, s41
	s_nop 0
	global_load_lds_dwordx4 v[194:195], off
	s_mov_b32 m0, s42
	s_nop 0
	global_load_lds_dwordx4 v[226:227], off
	s_waitcnt vmcnt(8)
	s_waitcnt lgkmcnt(0)
	s_barrier
	s_setprio 0
	s_waitcnt lgkmcnt(0)
	v_mfma_f32_16x16x32_bf16 v[64:67], v[134:137], v[182:185], v[64:67]
	v_mfma_f32_16x16x32_bf16 v[60:63], v[142:145], v[182:185], v[60:63]
	v_mfma_f32_16x16x32_bf16 v[52:55], v[142:145], v[200:203], v[52:55]
	v_mfma_f32_16x16x32_bf16 v[56:59], v[134:137], v[200:203], v[56:59]
	v_mfma_f32_16x16x32_bf16 v[48:51], v[134:137], v[208:211], v[48:51]
	v_mfma_f32_16x16x32_bf16 v[44:47], v[142:145], v[208:211], v[44:47]
	v_mfma_f32_16x16x32_bf16 v[36:39], v[142:145], v[216:219], v[36:39]
	v_mfma_f32_16x16x32_bf16 v[40:43], v[134:137], v[216:219], v[40:43]
	v_mfma_f32_16x16x32_bf16 v[64:67], v[138:141], v[190:193], v[64:67]
	v_mfma_f32_16x16x32_bf16 v[60:63], v[146:149], v[190:193], v[60:63]
	v_mfma_f32_16x16x32_bf16 v[52:55], v[146:149], v[204:207], v[52:55]
	v_mfma_f32_16x16x32_bf16 v[56:59], v[138:141], v[204:207], v[56:59]
	v_mfma_f32_16x16x32_bf16 v[48:51], v[138:141], v[212:215], v[48:51]
	v_mfma_f32_16x16x32_bf16 v[44:47], v[146:149], v[212:215], v[44:47]
	v_mfma_f32_16x16x32_bf16 v[36:39], v[146:149], v[222:225], v[36:39]
	v_mfma_f32_16x16x32_bf16 v[40:43], v[138:141], v[222:225], v[40:43]
	s_setprio 3
	s_setprio 0
	v_mfma_f32_16x16x32_bf16 v[30:33], v[150:153], v[182:185], v[30:33]
	v_mfma_f32_16x16x32_bf16 v[26:29], v[158:161], v[182:185], v[26:29]
	v_mfma_f32_16x16x32_bf16 v[18:21], v[158:161], v[200:203], v[18:21]
	v_mfma_f32_16x16x32_bf16 v[22:25], v[150:153], v[200:203], v[22:25]
	v_mfma_f32_16x16x32_bf16 v[14:17], v[150:153], v[208:211], v[14:17]
	v_mfma_f32_16x16x32_bf16 v[10:13], v[158:161], v[208:211], v[10:13]
	v_mfma_f32_16x16x32_bf16 v[2:5], v[158:161], v[216:219], v[2:5]
	v_mfma_f32_16x16x32_bf16 v[6:9], v[150:153], v[216:219], v[6:9]
	v_mfma_f32_16x16x32_bf16 v[30:33], v[154:157], v[190:193], v[30:33]
	v_mfma_f32_16x16x32_bf16 v[26:29], v[178:181], v[190:193], v[26:29]
	v_mfma_f32_16x16x32_bf16 v[18:21], v[178:181], v[204:207], v[18:21]
	v_mfma_f32_16x16x32_bf16 v[22:25], v[154:157], v[204:207], v[22:25]
	v_mfma_f32_16x16x32_bf16 v[14:17], v[154:157], v[212:215], v[14:17]
	v_mfma_f32_16x16x32_bf16 v[10:13], v[178:181], v[212:215], v[10:13]
	v_mfma_f32_16x16x32_bf16 v[2:5], v[178:181], v[222:225], v[2:5]
	v_mfma_f32_16x16x32_bf16 v[6:9], v[154:157], v[222:225], v[6:9]
	s_setprio 3
	s_barrier
	ds_read_b128 v[134:137], v132
	ds_read_b128 v[138:141], v132 offset:1024
	ds_read_b128 v[142:145], v132 offset:2048
	ds_read_b128 v[146:149], v132 offset:3072
	ds_read_b128 v[150:153], v133
	ds_read_b128 v[154:157], v133 offset:1024
	ds_read_b128 v[158:161], v133 offset:2048
	ds_read_b128 v[178:181], v133 offset:3072
	s_add_u32 s36, s36, 0x40000
	s_addc_u32 s37, s37, 0
	s_mov_b32 m0, s43
	v_lshl_add_u64 v[228:229], s[36:37], 0, v[168:169]
	ds_read_b128 v[182:185], v197 offset:32768
	ds_read_b128 v[190:193], v197 offset:33792
	ds_read_b128 v[200:203], v197 offset:34816
	ds_read_b128 v[204:207], v197 offset:35840
	ds_read_b128 v[208:211], v197 offset:36864
	ds_read_b128 v[212:215], v197 offset:37888
	ds_read_b128 v[216:219], v197 offset:38912
	ds_read_b128 v[222:225], v197 offset:39936
	global_load_lds_dwordx4 v[228:229], off
	v_lshl_add_u64 v[228:229], s[36:37], 0, v[166:167]
	s_mov_b32 m0, s44
	s_nop 0
	global_load_lds_dwordx4 v[228:229], off
	s_waitcnt vmcnt(8)
	s_waitcnt lgkmcnt(0)
	s_barrier
	s_setprio 0
	s_waitcnt lgkmcnt(0)
	v_mfma_f32_16x16x32_bf16 v[128:131], v[134:137], v[182:185], v[128:131]
	v_mfma_f32_16x16x32_bf16 v[124:127], v[142:145], v[182:185], v[124:127]
	v_mfma_f32_16x16x32_bf16 v[116:119], v[142:145], v[200:203], v[116:119]
	v_mfma_f32_16x16x32_bf16 v[120:123], v[134:137], v[200:203], v[120:123]
	v_mfma_f32_16x16x32_bf16 v[112:115], v[134:137], v[208:211], v[112:115]
	v_mfma_f32_16x16x32_bf16 v[108:111], v[142:145], v[208:211], v[108:111]
	v_mfma_f32_16x16x32_bf16 v[100:103], v[142:145], v[216:219], v[100:103]
	v_mfma_f32_16x16x32_bf16 v[104:107], v[134:137], v[216:219], v[104:107]
	v_mfma_f32_16x16x32_bf16 v[128:131], v[138:141], v[190:193], v[128:131]
	v_mfma_f32_16x16x32_bf16 v[124:127], v[146:149], v[190:193], v[124:127]
	v_mfma_f32_16x16x32_bf16 v[116:119], v[146:149], v[204:207], v[116:119]
	v_mfma_f32_16x16x32_bf16 v[120:123], v[138:141], v[204:207], v[120:123]
	v_mfma_f32_16x16x32_bf16 v[112:115], v[138:141], v[212:215], v[112:115]
	v_mfma_f32_16x16x32_bf16 v[108:111], v[146:149], v[212:215], v[108:111]
	v_mfma_f32_16x16x32_bf16 v[100:103], v[146:149], v[222:225], v[100:103]
	v_mfma_f32_16x16x32_bf16 v[104:107], v[138:141], v[222:225], v[104:107]
	s_setprio 3
	s_setprio 0
	v_mfma_f32_16x16x32_bf16 v[96:99], v[150:153], v[182:185], v[96:99]
	v_mfma_f32_16x16x32_bf16 v[92:95], v[158:161], v[182:185], v[92:95]
	v_mfma_f32_16x16x32_bf16 v[84:87], v[158:161], v[200:203], v[84:87]
	v_mfma_f32_16x16x32_bf16 v[88:91], v[150:153], v[200:203], v[88:91]
	v_mfma_f32_16x16x32_bf16 v[80:83], v[150:153], v[208:211], v[80:83]
	v_mfma_f32_16x16x32_bf16 v[76:79], v[158:161], v[208:211], v[76:79]
	v_mfma_f32_16x16x32_bf16 v[68:71], v[158:161], v[216:219], v[68:71]
	v_mfma_f32_16x16x32_bf16 v[72:75], v[150:153], v[216:219], v[72:75]
	v_mfma_f32_16x16x32_bf16 v[96:99], v[154:157], v[190:193], v[96:99]
	v_mfma_f32_16x16x32_bf16 v[92:95], v[178:181], v[190:193], v[92:95]
	v_mfma_f32_16x16x32_bf16 v[84:87], v[178:181], v[204:207], v[84:87]
	v_mfma_f32_16x16x32_bf16 v[88:91], v[154:157], v[204:207], v[88:91]
	v_mfma_f32_16x16x32_bf16 v[80:83], v[154:157], v[212:215], v[80:83]
	v_mfma_f32_16x16x32_bf16 v[76:79], v[178:181], v[212:215], v[76:79]
	v_mfma_f32_16x16x32_bf16 v[68:71], v[178:181], v[222:225], v[68:71]
	v_mfma_f32_16x16x32_bf16 v[72:75], v[154:157], v[222:225], v[72:75]
	s_setprio 3
	s_barrier
	s_mov_b32 m0, s64
	v_lshl_add_u64 v[162:163], v[162:163], 0, s[18:19]
	s_add_u32 s22, s22, 0x40080
	ds_read_b128 v[182:185], v197 offset:49152
	ds_read_b128 v[190:193], v197 offset:50176
	ds_read_b128 v[200:203], v197 offset:51200
	ds_read_b128 v[204:207], v197 offset:52224
	ds_read_b128 v[208:211], v197 offset:53248
	ds_read_b128 v[212:215], v197 offset:54272
	ds_read_b128 v[216:219], v197 offset:55296
	ds_read_b128 v[222:225], v197 offset:56320
	global_load_lds_dwordx4 v[162:163], off
	v_lshl_add_u64 v[162:163], v[174:175], 0, s[18:19]
	s_mov_b32 m0, s65
	s_addc_u32 s23, s23, 0
	global_load_lds_dwordx4 v[162:163], off
	v_lshl_add_u64 v[162:163], s[22:23], 0, v[34:35]
	s_mov_b32 m0, s66
	s_nop 0
	global_load_lds_dwordx4 v[162:163], off
	v_lshl_add_u64 v[162:163], s[22:23], 0, v[164:165]
	s_mov_b32 m0, s67
	s_nop 0
	global_load_lds_dwordx4 v[162:163], off
	v_lshl_add_u64 v[162:163], v[194:195], 0, s[18:19]
	s_mov_b32 m0, s47
	s_nop 0
	global_load_lds_dwordx4 v[162:163], off
	v_lshl_add_u64 v[162:163], v[226:227], 0, s[18:19]
	s_mov_b32 m0, s48
	s_nop 0
	global_load_lds_dwordx4 v[162:163], off
	s_waitcnt vmcnt(8)
	s_waitcnt lgkmcnt(0)
	s_barrier
	s_setprio 0
	s_waitcnt lgkmcnt(0)
	v_mfma_f32_16x16x32_bf16 v[64:67], v[134:137], v[182:185], v[64:67]
	v_mfma_f32_16x16x32_bf16 v[60:63], v[142:145], v[182:185], v[60:63]
	v_mfma_f32_16x16x32_bf16 v[52:55], v[142:145], v[200:203], v[52:55]
	v_mfma_f32_16x16x32_bf16 v[56:59], v[134:137], v[200:203], v[56:59]
	v_mfma_f32_16x16x32_bf16 v[48:51], v[134:137], v[208:211], v[48:51]
	v_mfma_f32_16x16x32_bf16 v[44:47], v[142:145], v[208:211], v[44:47]
	v_mfma_f32_16x16x32_bf16 v[36:39], v[142:145], v[216:219], v[36:39]
	v_mfma_f32_16x16x32_bf16 v[40:43], v[134:137], v[216:219], v[40:43]
	v_mfma_f32_16x16x32_bf16 v[64:67], v[138:141], v[190:193], v[64:67]
	v_mfma_f32_16x16x32_bf16 v[60:63], v[146:149], v[190:193], v[60:63]
	v_mfma_f32_16x16x32_bf16 v[52:55], v[146:149], v[204:207], v[52:55]
	v_mfma_f32_16x16x32_bf16 v[56:59], v[138:141], v[204:207], v[56:59]
	v_mfma_f32_16x16x32_bf16 v[48:51], v[138:141], v[212:215], v[48:51]
	v_mfma_f32_16x16x32_bf16 v[44:47], v[146:149], v[212:215], v[44:47]
	v_mfma_f32_16x16x32_bf16 v[36:39], v[146:149], v[222:225], v[36:39]
	v_mfma_f32_16x16x32_bf16 v[40:43], v[138:141], v[222:225], v[40:43]
	s_setprio 3
	s_setprio 0
	v_mfma_f32_16x16x32_bf16 v[30:33], v[150:153], v[182:185], v[30:33]
	v_mfma_f32_16x16x32_bf16 v[26:29], v[158:161], v[182:185], v[26:29]
	v_mfma_f32_16x16x32_bf16 v[18:21], v[158:161], v[200:203], v[18:21]
	v_mfma_f32_16x16x32_bf16 v[22:25], v[150:153], v[200:203], v[22:25]
	v_mfma_f32_16x16x32_bf16 v[14:17], v[150:153], v[208:211], v[14:17]
	v_mfma_f32_16x16x32_bf16 v[10:13], v[158:161], v[208:211], v[10:13]
	v_mfma_f32_16x16x32_bf16 v[2:5], v[158:161], v[216:219], v[2:5]
	v_mfma_f32_16x16x32_bf16 v[6:9], v[150:153], v[216:219], v[6:9]
	v_mfma_f32_16x16x32_bf16 v[30:33], v[154:157], v[190:193], v[30:33]
	v_mfma_f32_16x16x32_bf16 v[26:29], v[178:181], v[190:193], v[26:29]
	v_mfma_f32_16x16x32_bf16 v[18:21], v[178:181], v[204:207], v[18:21]
	v_mfma_f32_16x16x32_bf16 v[22:25], v[154:157], v[204:207], v[22:25]
	v_mfma_f32_16x16x32_bf16 v[14:17], v[154:157], v[212:215], v[14:17]
	v_mfma_f32_16x16x32_bf16 v[10:13], v[178:181], v[212:215], v[10:13]
	v_mfma_f32_16x16x32_bf16 v[2:5], v[178:181], v[222:225], v[2:5]
	v_mfma_f32_16x16x32_bf16 v[6:9], v[154:157], v[222:225], v[6:9]
	s_setprio 3
	s_barrier
	s_add_i32 s70, s70, 2
	s_add_u32 s30, s30, 0x100
	s_addc_u32 s31, s31, 0
	s_add_u32 s68, s68, 0x100
	s_addc_u32 s69, s69, 0
	s_cmp_gt_u32 s70, 13
	s_cbranch_scc0 .LBB0_287
	s_and_b64 vcc, exec, s[8:9]
	s_cbranch_vccz .LBB0_290
	s_barrier

.LBB0_540:
	s_lshl_b32 s14, s55, 19
	v_readlane_b32 s16, v253, 53
	v_readlane_b32 s17, v253, 54
	s_add_u32 s16, s16, s14
	s_addc_u32 s17, s17, 0
	s_and_b64 s[22:23], s[4:5], exec
	s_cselect_b32 s58, s17, s37
	s_cselect_b32 s59, s16, s36
	s_lshl_b32 s14, s54, 19
	s_add_u32 s22, s15, s14
	s_addc_u32 s23, s26, 0
	s_and_b64 s[40:41], s[4:5], exec
	s_cselect_b32 s60, s23, s31
	s_cselect_b32 s61, s22, s30
	s_add_i32 s64, 0, 0x10000
	v_add_u32_e32 v172, s64, v222
	s_add_i32 s66, 0, 0x14000
	v_add_u32_e32 v173, s66, v222
	ds_read_b128 v[160:163], v172
	ds_read_b128 v[152:155], v172 offset:1024
	ds_read_b128 v[156:159], v172 offset:2048
	ds_read_b128 v[148:151], v172 offset:3072
	ds_read_b128 v[144:147], v173
	ds_read_b128 v[136:139], v173 offset:1024
	ds_read_b128 v[140:143], v173 offset:2048
	ds_read_b128 v[132:135], v173 offset:3072
	s_add_u32 s40, s36, 0x40080
	s_addc_u32 s41, s37, 0
	s_add_i32 s62, s43, 0xc000
	v_lshl_add_u64 v[174:175], s[40:41], 0, v[194:195]
	s_mov_b32 m0, s62
	s_add_i32 s63, s43, 0xe000
	ds_read_b128 v[164:167], v223
	ds_read_b128 v[168:171], v223 offset:1024
	ds_read_b128 v[178:181], v223 offset:2048
	ds_read_b128 v[182:185], v223 offset:3072
	ds_read_b128 v[200:203], v223 offset:4096
	ds_read_b128 v[204:207], v223 offset:5120
	ds_read_b128 v[208:211], v223 offset:6144
	ds_read_b128 v[212:215], v223 offset:7168
	global_load_lds_dwordx4 v[174:175], off
	v_lshl_add_u64 v[174:175], s[40:41], 0, v[192:193]
	s_mov_b32 m0, s63
	s_nop 0
	global_load_lds_dwordx4 v[174:175], off
	s_waitcnt vmcnt(8)
	s_waitcnt lgkmcnt(0)
	s_barrier
	s_setprio 0
	s_waitcnt lgkmcnt(0)
	v_mfma_f32_16x16x32_bf16 v[128:131], v[160:163], v[164:167], 0
	v_mfma_f32_16x16x32_bf16 v[124:127], v[156:159], v[164:167], 0
	v_mfma_f32_16x16x32_bf16 v[116:119], v[156:159], v[178:181], 0
	v_mfma_f32_16x16x32_bf16 v[120:123], v[160:163], v[178:181], 0
	v_mfma_f32_16x16x32_bf16 v[112:115], v[160:163], v[200:203], 0
	v_mfma_f32_16x16x32_bf16 v[108:111], v[156:159], v[200:203], 0
	v_mfma_f32_16x16x32_bf16 v[100:103], v[156:159], v[208:211], 0
	v_mfma_f32_16x16x32_bf16 v[104:107], v[160:163], v[208:211], 0
	s_nop 0
	v_mfma_f32_16x16x32_bf16 v[128:131], v[152:155], v[168:171], v[128:131]
	v_mfma_f32_16x16x32_bf16 v[124:127], v[148:151], v[168:171], v[124:127]
	v_mfma_f32_16x16x32_bf16 v[116:119], v[148:151], v[182:185], v[116:119]
	v_mfma_f32_16x16x32_bf16 v[120:123], v[152:155], v[182:185], v[120:123]
	v_mfma_f32_16x16x32_bf16 v[112:115], v[152:155], v[204:207], v[112:115]
	v_mfma_f32_16x16x32_bf16 v[108:111], v[148:151], v[204:207], v[108:111]
	v_mfma_f32_16x16x32_bf16 v[100:103], v[148:151], v[212:215], v[100:103]
	v_mfma_f32_16x16x32_bf16 v[104:107], v[152:155], v[212:215], v[104:107]
	s_setprio 3
	s_setprio 0
	v_mfma_f32_16x16x32_bf16 v[96:99], v[144:147], v[164:167], 0
	v_mfma_f32_16x16x32_bf16 v[92:95], v[140:143], v[164:167], 0
	v_mfma_f32_16x16x32_bf16 v[84:87], v[140:143], v[178:181], 0
	v_mfma_f32_16x16x32_bf16 v[88:91], v[144:147], v[178:181], 0
	v_mfma_f32_16x16x32_bf16 v[80:83], v[144:147], v[200:203], 0
	v_mfma_f32_16x16x32_bf16 v[76:79], v[140:143], v[200:203], 0
	v_mfma_f32_16x16x32_bf16 v[68:71], v[140:143], v[208:211], 0
	v_mfma_f32_16x16x32_bf16 v[72:75], v[144:147], v[208:211], 0
	s_nop 0
	v_mfma_f32_16x16x32_bf16 v[96:99], v[136:139], v[168:171], v[96:99]
	v_mfma_f32_16x16x32_bf16 v[92:95], v[132:135], v[168:171], v[92:95]
	v_mfma_f32_16x16x32_bf16 v[84:87], v[132:135], v[182:185], v[84:87]
	v_mfma_f32_16x16x32_bf16 v[88:91], v[136:139], v[182:185], v[88:91]
	v_mfma_f32_16x16x32_bf16 v[80:83], v[136:139], v[204:207], v[80:83]
	v_mfma_f32_16x16x32_bf16 v[76:79], v[132:135], v[204:207], v[76:79]
	v_mfma_f32_16x16x32_bf16 v[68:71], v[132:135], v[212:215], v[68:71]
	v_mfma_f32_16x16x32_bf16 v[72:75], v[136:139], v[212:215], v[72:75]
	s_setprio 3
	s_barrier
	v_lshl_add_u64 v[164:165], s[30:31], 0, v[34:35]
	s_add_i32 s64, s64, s42
	v_lshl_add_u64 v[166:167], v[164:165], 0, s[28:29]
	s_mov_b32 m0, s64
	s_add_i32 s65, s64, 0x2000
	ds_read_b128 v[178:181], v223 offset:16384
	ds_read_b128 v[182:185], v223 offset:17408
	ds_read_b128 v[200:203], v223 offset:18432
	ds_read_b128 v[204:207], v223 offset:19456
	ds_read_b128 v[208:211], v223 offset:20480
	ds_read_b128 v[212:215], v223 offset:21504
	ds_read_b128 v[216:219], v223 offset:22528
	ds_read_b128 v[224:227], v223 offset:23552
	global_load_lds_dwordx4 v[166:167], off
	v_lshl_add_u64 v[166:167], s[30:31], 0, v[190:191]
	s_add_u32 s40, s30, 0x40100
	v_lshl_add_u64 v[168:169], v[166:167], 0, s[28:29]
	s_mov_b32 m0, s65
	s_addc_u32 s41, s31, 0
	s_add_i32 s66, s66, s42
	global_load_lds_dwordx4 v[168:169], off
	v_lshl_add_u64 v[168:169], s[40:41], 0, v[34:35]
	s_mov_b32 m0, s66
	s_add_i32 s67, s66, 0x2000
	global_load_lds_dwordx4 v[168:169], off
	v_lshl_add_u64 v[168:169], s[40:41], 0, v[190:191]
	s_mov_b32 m0, s67
	s_nop 0
	global_load_lds_dwordx4 v[168:169], off
	v_lshl_add_u64 v[168:169], s[36:37], 0, v[194:195]
	v_lshl_add_u64 v[170:171], v[168:169], 0, s[28:29]
	s_mov_b32 m0, s43
	s_nop 0
	global_load_lds_dwordx4 v[170:171], off
	v_lshl_add_u64 v[170:171], s[36:37], 0, v[192:193]
	v_lshl_add_u64 v[174:175], v[170:171], 0, s[28:29]
	s_mov_b32 m0, s44
	s_nop 0
	global_load_lds_dwordx4 v[174:175], off
	s_waitcnt vmcnt(8)
	s_waitcnt lgkmcnt(0)
	s_barrier
	s_setprio 0
	s_waitcnt lgkmcnt(0)
	v_mfma_f32_16x16x32_bf16 v[64:67], v[160:163], v[178:181], 0
	v_mfma_f32_16x16x32_bf16 v[60:63], v[156:159], v[178:181], 0
	v_mfma_f32_16x16x32_bf16 v[52:55], v[156:159], v[200:203], 0
	v_mfma_f32_16x16x32_bf16 v[56:59], v[160:163], v[200:203], 0
	v_mfma_f32_16x16x32_bf16 v[48:51], v[160:163], v[208:211], 0
	v_mfma_f32_16x16x32_bf16 v[44:47], v[156:159], v[208:211], 0
	v_mfma_f32_16x16x32_bf16 v[36:39], v[156:159], v[216:219], 0
	v_mfma_f32_16x16x32_bf16 v[40:43], v[160:163], v[216:219], 0
	s_nop 0
	v_mfma_f32_16x16x32_bf16 v[64:67], v[152:155], v[182:185], v[64:67]
	v_mfma_f32_16x16x32_bf16 v[60:63], v[148:151], v[182:185], v[60:63]
	v_mfma_f32_16x16x32_bf16 v[52:55], v[148:151], v[204:207], v[52:55]
	v_mfma_f32_16x16x32_bf16 v[56:59], v[152:155], v[204:207], v[56:59]
	v_mfma_f32_16x16x32_bf16 v[48:51], v[152:155], v[212:215], v[48:51]
	v_mfma_f32_16x16x32_bf16 v[44:47], v[148:151], v[212:215], v[44:47]
	v_mfma_f32_16x16x32_bf16 v[36:39], v[148:151], v[224:227], v[36:39]
	v_mfma_f32_16x16x32_bf16 v[40:43], v[152:155], v[224:227], v[40:43]
	s_setprio 3
	s_setprio 0
	v_mfma_f32_16x16x32_bf16 v[30:33], v[144:147], v[178:181], 0
	v_mfma_f32_16x16x32_bf16 v[26:29], v[140:143], v[178:181], 0
	v_mfma_f32_16x16x32_bf16 v[18:21], v[140:143], v[200:203], 0
	v_mfma_f32_16x16x32_bf16 v[22:25], v[144:147], v[200:203], 0
	v_mfma_f32_16x16x32_bf16 v[14:17], v[144:147], v[208:211], 0
	v_mfma_f32_16x16x32_bf16 v[10:13], v[140:143], v[208:211], 0
	v_mfma_f32_16x16x32_bf16 v[2:5], v[140:143], v[216:219], 0
	v_mfma_f32_16x16x32_bf16 v[6:9], v[144:147], v[216:219], 0
	s_nop 0
	v_mfma_f32_16x16x32_bf16 v[30:33], v[136:139], v[182:185], v[30:33]
	v_mfma_f32_16x16x32_bf16 v[26:29], v[132:135], v[182:185], v[26:29]
	v_mfma_f32_16x16x32_bf16 v[18:21], v[132:135], v[204:207], v[18:21]
	v_mfma_f32_16x16x32_bf16 v[22:25], v[136:139], v[204:207], v[22:25]
	v_mfma_f32_16x16x32_bf16 v[14:17], v[136:139], v[212:215], v[14:17]
	v_mfma_f32_16x16x32_bf16 v[10:13], v[132:135], v[212:215], v[10:13]
	v_mfma_f32_16x16x32_bf16 v[2:5], v[132:135], v[224:227], v[2:5]
	v_mfma_f32_16x16x32_bf16 v[6:9], v[136:139], v[224:227], v[6:9]
	s_setprio 3
	s_barrier
	s_add_i32 s68, 0, 0x18000
	s_add_i32 s70, 0, 0x1c000
	v_add_u32_e32 v132, s68, v222
	v_add_u32_e32 v133, s70, v222
	ds_read_b128 v[134:137], v132
	ds_read_b128 v[138:141], v132 offset:1024
	ds_read_b128 v[142:145], v132 offset:2048
	ds_read_b128 v[146:149], v132 offset:3072
	ds_read_b128 v[150:153], v133
	ds_read_b128 v[154:157], v133 offset:1024
	ds_read_b128 v[158:161], v133 offset:2048
	ds_read_b128 v[178:181], v133 offset:3072
	s_add_u32 s40, s36, 0x40100
	s_addc_u32 s41, s37, 0
	s_mov_b32 m0, s45
	v_lshl_add_u64 v[162:163], s[40:41], 0, v[194:195]
	ds_read_b128 v[182:185], v223 offset:32768
	ds_read_b128 v[200:203], v223 offset:33792
	ds_read_b128 v[204:207], v223 offset:34816
	ds_read_b128 v[208:211], v223 offset:35840
	ds_read_b128 v[212:215], v223 offset:36864
	ds_read_b128 v[216:219], v223 offset:37888
	ds_read_b128 v[224:227], v223 offset:38912
	ds_read_b128 v[228:231], v223 offset:39936
	global_load_lds_dwordx4 v[162:163], off
	v_lshl_add_u64 v[162:163], s[40:41], 0, v[192:193]
	s_mov_b32 m0, s46
	s_nop 0
	global_load_lds_dwordx4 v[162:163], off
	s_waitcnt vmcnt(8)
	s_waitcnt lgkmcnt(0)
	s_barrier
	s_setprio 0
	s_waitcnt lgkmcnt(0)
	v_mfma_f32_16x16x32_bf16 v[128:131], v[134:137], v[182:185], v[128:131]
	v_mfma_f32_16x16x32_bf16 v[124:127], v[142:145], v[182:185], v[124:127]
	v_mfma_f32_16x16x32_bf16 v[116:119], v[142:145], v[204:207], v[116:119]
	v_mfma_f32_16x16x32_bf16 v[120:123], v[134:137], v[204:207], v[120:123]
	v_mfma_f32_16x16x32_bf16 v[112:115], v[134:137], v[212:215], v[112:115]
	v_mfma_f32_16x16x32_bf16 v[108:111], v[142:145], v[212:215], v[108:111]
	v_mfma_f32_16x16x32_bf16 v[100:103], v[142:145], v[224:227], v[100:103]
	v_mfma_f32_16x16x32_bf16 v[104:107], v[134:137], v[224:227], v[104:107]
	v_mfma_f32_16x16x32_bf16 v[128:131], v[138:141], v[200:203], v[128:131]
	v_mfma_f32_16x16x32_bf16 v[124:127], v[146:149], v[200:203], v[124:127]
	v_mfma_f32_16x16x32_bf16 v[116:119], v[146:149], v[208:211], v[116:119]
	v_mfma_f32_16x16x32_bf16 v[120:123], v[138:141], v[208:211], v[120:123]
	v_mfma_f32_16x16x32_bf16 v[112:115], v[138:141], v[216:219], v[112:115]
	v_mfma_f32_16x16x32_bf16 v[108:111], v[146:149], v[216:219], v[108:111]
	v_mfma_f32_16x16x32_bf16 v[100:103], v[146:149], v[228:231], v[100:103]
	v_mfma_f32_16x16x32_bf16 v[104:107], v[138:141], v[228:231], v[104:107]
	s_setprio 3
	s_setprio 0
	v_mfma_f32_16x16x32_bf16 v[96:99], v[150:153], v[182:185], v[96:99]
	v_mfma_f32_16x16x32_bf16 v[92:95], v[158:161], v[182:185], v[92:95]
	v_mfma_f32_16x16x32_bf16 v[84:87], v[158:161], v[204:207], v[84:87]
	v_mfma_f32_16x16x32_bf16 v[88:91], v[150:153], v[204:207], v[88:91]
	v_mfma_f32_16x16x32_bf16 v[80:83], v[150:153], v[212:215], v[80:83]
	v_mfma_f32_16x16x32_bf16 v[76:79], v[158:161], v[212:215], v[76:79]
	v_mfma_f32_16x16x32_bf16 v[68:71], v[158:161], v[224:227], v[68:71]
	v_mfma_f32_16x16x32_bf16 v[72:75], v[150:153], v[224:227], v[72:75]
	v_mfma_f32_16x16x32_bf16 v[96:99], v[154:157], v[200:203], v[96:99]
	v_mfma_f32_16x16x32_bf16 v[92:95], v[178:181], v[200:203], v[92:95]
	v_mfma_f32_16x16x32_bf16 v[84:87], v[178:181], v[208:211], v[84:87]
	v_mfma_f32_16x16x32_bf16 v[88:91], v[154:157], v[208:211], v[88:91]
	v_mfma_f32_16x16x32_bf16 v[80:83], v[154:157], v[216:219], v[80:83]
	v_mfma_f32_16x16x32_bf16 v[76:79], v[178:181], v[216:219], v[76:79]
	v_mfma_f32_16x16x32_bf16 v[68:71], v[178:181], v[228:231], v[68:71]
	v_mfma_f32_16x16x32_bf16 v[72:75], v[154:157], v[228:231], v[72:75]
	s_setprio 3
	s_barrier
	s_add_i32 s68, s68, s42
	s_mov_b64 s[24:25], 0x180
	s_add_i32 s69, s68, 0x2000
	v_lshl_add_u64 v[162:163], v[164:165], 0, s[24:25]
	s_mov_b32 m0, s68
	s_add_u32 s40, s30, 0x40180
	ds_read_b128 v[182:185], v223 offset:49152
	ds_read_b128 v[200:203], v223 offset:50176
	ds_read_b128 v[204:207], v223 offset:51200
	ds_read_b128 v[208:211], v223 offset:52224
	ds_read_b128 v[212:215], v223 offset:53248
	ds_read_b128 v[216:219], v223 offset:54272
	ds_read_b128 v[224:227], v223 offset:55296
	ds_read_b128 v[228:231], v223 offset:56320
	global_load_lds_dwordx4 v[162:163], off
	v_lshl_add_u64 v[162:163], v[166:167], 0, s[24:25]
	s_mov_b32 m0, s69
	s_addc_u32 s41, s31, 0
	s_add_i32 s70, s70, s42
	global_load_lds_dwordx4 v[162:163], off
	v_lshl_add_u64 v[162:163], s[40:41], 0, v[34:35]
	s_mov_b32 m0, s70
	s_add_i32 s71, s70, 0x2000
	global_load_lds_dwordx4 v[162:163], off
	v_lshl_add_u64 v[162:163], s[40:41], 0, v[190:191]
	s_mov_b32 m0, s71
	s_nop 0
	global_load_lds_dwordx4 v[162:163], off
	v_lshl_add_u64 v[162:163], v[168:169], 0, s[24:25]
	s_mov_b32 m0, s51
	s_nop 0
	global_load_lds_dwordx4 v[162:163], off
	v_lshl_add_u64 v[162:163], v[170:171], 0, s[24:25]
	s_mov_b32 m0, s52
	s_nop 0
	global_load_lds_dwordx4 v[162:163], off
	s_waitcnt vmcnt(8)
	s_waitcnt lgkmcnt(0)
	s_barrier
	s_setprio 0
	s_waitcnt lgkmcnt(0)
	v_mfma_f32_16x16x32_bf16 v[64:67], v[134:137], v[182:185], v[64:67]
	v_mfma_f32_16x16x32_bf16 v[60:63], v[142:145], v[182:185], v[60:63]
	v_mfma_f32_16x16x32_bf16 v[52:55], v[142:145], v[204:207], v[52:55]
	v_mfma_f32_16x16x32_bf16 v[56:59], v[134:137], v[204:207], v[56:59]
	v_mfma_f32_16x16x32_bf16 v[48:51], v[134:137], v[212:215], v[48:51]
	v_mfma_f32_16x16x32_bf16 v[44:47], v[142:145], v[212:215], v[44:47]
	v_mfma_f32_16x16x32_bf16 v[36:39], v[142:145], v[224:227], v[36:39]
	v_mfma_f32_16x16x32_bf16 v[40:43], v[134:137], v[224:227], v[40:43]
	v_mfma_f32_16x16x32_bf16 v[64:67], v[138:141], v[200:203], v[64:67]
	v_mfma_f32_16x16x32_bf16 v[60:63], v[146:149], v[200:203], v[60:63]
	v_mfma_f32_16x16x32_bf16 v[52:55], v[146:149], v[208:211], v[52:55]
	v_mfma_f32_16x16x32_bf16 v[56:59], v[138:141], v[208:211], v[56:59]
	v_mfma_f32_16x16x32_bf16 v[48:51], v[138:141], v[216:219], v[48:51]
	v_mfma_f32_16x16x32_bf16 v[44:47], v[146:149], v[216:219], v[44:47]
	v_mfma_f32_16x16x32_bf16 v[36:39], v[146:149], v[228:231], v[36:39]
	v_mfma_f32_16x16x32_bf16 v[40:43], v[138:141], v[228:231], v[40:43]
	s_setprio 3
	s_setprio 0
	v_mfma_f32_16x16x32_bf16 v[30:33], v[150:153], v[182:185], v[30:33]
	v_mfma_f32_16x16x32_bf16 v[26:29], v[158:161], v[182:185], v[26:29]
	v_mfma_f32_16x16x32_bf16 v[18:21], v[158:161], v[204:207], v[18:21]
	v_mfma_f32_16x16x32_bf16 v[22:25], v[150:153], v[204:207], v[22:25]
	v_mfma_f32_16x16x32_bf16 v[14:17], v[150:153], v[212:215], v[14:17]
	v_mfma_f32_16x16x32_bf16 v[10:13], v[158:161], v[212:215], v[10:13]
	v_mfma_f32_16x16x32_bf16 v[2:5], v[158:161], v[224:227], v[2:5]
	v_mfma_f32_16x16x32_bf16 v[6:9], v[150:153], v[224:227], v[6:9]
	v_mfma_f32_16x16x32_bf16 v[30:33], v[154:157], v[200:203], v[30:33]
	v_mfma_f32_16x16x32_bf16 v[26:29], v[178:181], v[200:203], v[26:29]
	v_mfma_f32_16x16x32_bf16 v[18:21], v[178:181], v[208:211], v[18:21]
	v_mfma_f32_16x16x32_bf16 v[22:25], v[154:157], v[208:211], v[22:25]
	v_mfma_f32_16x16x32_bf16 v[14:17], v[154:157], v[216:219], v[14:17]
	v_mfma_f32_16x16x32_bf16 v[10:13], v[178:181], v[216:219], v[10:13]
	v_mfma_f32_16x16x32_bf16 v[2:5], v[178:181], v[228:231], v[2:5]
	v_mfma_f32_16x16x32_bf16 v[6:9], v[154:157], v[228:231], v[6:9]
	s_setprio 3
	s_barrier
	s_add_u32 s36, s36, 0x40180
	s_addc_u32 s37, s37, 0
	s_add_u32 s72, s30, 0x200
	s_addc_u32 s73, s31, 0
	s_mov_b32 s74, 0
.LBB0_541:
	ds_read_b128 v[134:137], v172
	ds_read_b128 v[138:141], v172 offset:1024
	ds_read_b128 v[142:145], v172 offset:2048
	ds_read_b128 v[146:149], v172 offset:3072
	ds_read_b128 v[150:153], v173
	ds_read_b128 v[154:157], v173 offset:1024
	ds_read_b128 v[158:161], v173 offset:2048
	ds_read_b128 v[162:165], v173 offset:3072
	s_add_u32 s14, s36, 0xfffc0080
	s_addc_u32 s30, s37, -1
	s_cmp_eq_u32 s74, 12
	s_cselect_b32 s41, s58, s30
	s_cselect_b32 s40, s59, s14
	s_cselect_b32 s31, s60, s73
	s_cselect_b32 s30, s61, s72
	s_mov_b32 m0, s62
	v_lshl_add_u64 v[170:171], s[36:37], 0, v[196:197]
	ds_read_b128 v[166:169], v223
	ds_read_b128 v[178:181], v223 offset:1024
	ds_read_b128 v[182:185], v223 offset:2048
	ds_read_b128 v[200:203], v223 offset:3072
	ds_read_b128 v[204:207], v223 offset:4096
	ds_read_b128 v[208:211], v223 offset:5120
	ds_read_b128 v[212:215], v223 offset:6144
	ds_read_b128 v[216:219], v223 offset:7168
	global_load_lds_dwordx4 v[170:171], off
	v_lshl_add_u64 v[170:171], s[36:37], 0, v[198:199]
	s_mov_b32 m0, s63
	s_nop 0
	global_load_lds_dwordx4 v[170:171], off
	s_waitcnt vmcnt(8)
	s_waitcnt lgkmcnt(0)
	s_barrier
	s_setprio 0
	s_waitcnt lgkmcnt(0)
	v_mfma_f32_16x16x32_bf16 v[128:131], v[134:137], v[166:169], v[128:131]
	v_mfma_f32_16x16x32_bf16 v[124:127], v[142:145], v[166:169], v[124:127]
	v_mfma_f32_16x16x32_bf16 v[116:119], v[142:145], v[182:185], v[116:119]
	v_mfma_f32_16x16x32_bf16 v[120:123], v[134:137], v[182:185], v[120:123]
	v_mfma_f32_16x16x32_bf16 v[112:115], v[134:137], v[204:207], v[112:115]
	v_mfma_f32_16x16x32_bf16 v[108:111], v[142:145], v[204:207], v[108:111]
	v_mfma_f32_16x16x32_bf16 v[100:103], v[142:145], v[212:215], v[100:103]
	v_mfma_f32_16x16x32_bf16 v[104:107], v[134:137], v[212:215], v[104:107]
	v_mfma_f32_16x16x32_bf16 v[128:131], v[138:141], v[178:181], v[128:131]
	v_mfma_f32_16x16x32_bf16 v[124:127], v[146:149], v[178:181], v[124:127]
	v_mfma_f32_16x16x32_bf16 v[116:119], v[146:149], v[200:203], v[116:119]
	v_mfma_f32_16x16x32_bf16 v[120:123], v[138:141], v[200:203], v[120:123]
	v_mfma_f32_16x16x32_bf16 v[112:115], v[138:141], v[208:211], v[112:115]
	v_mfma_f32_16x16x32_bf16 v[108:111], v[146:149], v[208:211], v[108:111]
	v_mfma_f32_16x16x32_bf16 v[100:103], v[146:149], v[216:219], v[100:103]
	v_mfma_f32_16x16x32_bf16 v[104:107], v[138:141], v[216:219], v[104:107]
	s_setprio 3
	s_setprio 0
	v_mfma_f32_16x16x32_bf16 v[96:99], v[150:153], v[166:169], v[96:99]
	v_mfma_f32_16x16x32_bf16 v[92:95], v[158:161], v[166:169], v[92:95]
	v_mfma_f32_16x16x32_bf16 v[84:87], v[158:161], v[182:185], v[84:87]
	v_mfma_f32_16x16x32_bf16 v[88:91], v[150:153], v[182:185], v[88:91]
	v_mfma_f32_16x16x32_bf16 v[80:83], v[150:153], v[204:207], v[80:83]
	v_mfma_f32_16x16x32_bf16 v[76:79], v[158:161], v[204:207], v[76:79]
	v_mfma_f32_16x16x32_bf16 v[68:71], v[158:161], v[212:215], v[68:71]
	v_mfma_f32_16x16x32_bf16 v[72:75], v[150:153], v[212:215], v[72:75]
	v_mfma_f32_16x16x32_bf16 v[96:99], v[154:157], v[178:181], v[96:99]
	v_mfma_f32_16x16x32_bf16 v[92:95], v[162:165], v[178:181], v[92:95]
	v_mfma_f32_16x16x32_bf16 v[84:87], v[162:165], v[200:203], v[84:87]
	v_mfma_f32_16x16x32_bf16 v[88:91], v[154:157], v[200:203], v[88:91]
	v_mfma_f32_16x16x32_bf16 v[80:83], v[154:157], v[208:211], v[80:83]
	v_mfma_f32_16x16x32_bf16 v[76:79], v[162:165], v[208:211], v[76:79]
	v_mfma_f32_16x16x32_bf16 v[68:71], v[162:165], v[216:219], v[68:71]
	v_mfma_f32_16x16x32_bf16 v[72:75], v[154:157], v[216:219], v[72:75]
	s_setprio 3
	s_barrier
	s_mov_b32 m0, s64
	v_lshl_add_u64 v[170:171], s[30:31], 0, v[34:35]
	s_add_u32 s76, s30, 0x40000
	ds_read_b128 v[166:169], v223 offset:16384
	ds_read_b128 v[178:181], v223 offset:17408
	ds_read_b128 v[182:185], v223 offset:18432
	ds_read_b128 v[200:203], v223 offset:19456
	ds_read_b128 v[204:207], v223 offset:20480
	ds_read_b128 v[208:211], v223 offset:21504
	ds_read_b128 v[212:215], v223 offset:22528
	ds_read_b128 v[216:219], v223 offset:23552
	global_load_lds_dwordx4 v[170:171], off
	v_lshl_add_u64 v[174:175], s[30:31], 0, v[190:191]
	s_mov_b32 m0, s65
	s_addc_u32 s77, s31, 0
	global_load_lds_dwordx4 v[174:175], off
	v_lshl_add_u64 v[224:225], s[76:77], 0, v[34:35]
	s_mov_b32 m0, s66
	v_lshl_add_u64 v[226:227], s[40:41], 0, v[192:193]
	global_load_lds_dwordx4 v[224:225], off
	v_lshl_add_u64 v[224:225], s[76:77], 0, v[190:191]
	s_mov_b32 m0, s67
	s_nop 0
	global_load_lds_dwordx4 v[224:225], off
	v_lshl_add_u64 v[224:225], s[40:41], 0, v[194:195]
	s_mov_b32 m0, s43
	s_nop 0
	global_load_lds_dwordx4 v[224:225], off
	s_mov_b32 m0, s44
	s_nop 0
	global_load_lds_dwordx4 v[226:227], off
	s_waitcnt vmcnt(8)
	s_waitcnt lgkmcnt(0)
	s_barrier
	s_setprio 0
	s_waitcnt lgkmcnt(0)
	v_mfma_f32_16x16x32_bf16 v[64:67], v[134:137], v[166:169], v[64:67]
	v_mfma_f32_16x16x32_bf16 v[60:63], v[142:145], v[166:169], v[60:63]
	v_mfma_f32_16x16x32_bf16 v[52:55], v[142:145], v[182:185], v[52:55]
	v_mfma_f32_16x16x32_bf16 v[56:59], v[134:137], v[182:185], v[56:59]
	v_mfma_f32_16x16x32_bf16 v[48:51], v[134:137], v[204:207], v[48:51]
	v_mfma_f32_16x16x32_bf16 v[44:47], v[142:145], v[204:207], v[44:47]
	v_mfma_f32_16x16x32_bf16 v[36:39], v[142:145], v[212:215], v[36:39]
	v_mfma_f32_16x16x32_bf16 v[40:43], v[134:137], v[212:215], v[40:43]
	v_mfma_f32_16x16x32_bf16 v[64:67], v[138:141], v[178:181], v[64:67]
	v_mfma_f32_16x16x32_bf16 v[60:63], v[146:149], v[178:181], v[60:63]
	v_mfma_f32_16x16x32_bf16 v[52:55], v[146:149], v[200:203], v[52:55]
	v_mfma_f32_16x16x32_bf16 v[56:59], v[138:141], v[200:203], v[56:59]
	v_mfma_f32_16x16x32_bf16 v[48:51], v[138:141], v[208:211], v[48:51]
	v_mfma_f32_16x16x32_bf16 v[44:47], v[146:149], v[208:211], v[44:47]
	v_mfma_f32_16x16x32_bf16 v[36:39], v[146:149], v[216:219], v[36:39]
	v_mfma_f32_16x16x32_bf16 v[40:43], v[138:141], v[216:219], v[40:43]
	s_setprio 3
	s_setprio 0
	v_mfma_f32_16x16x32_bf16 v[30:33], v[150:153], v[166:169], v[30:33]
	v_mfma_f32_16x16x32_bf16 v[26:29], v[158:161], v[166:169], v[26:29]
	v_mfma_f32_16x16x32_bf16 v[18:21], v[158:161], v[182:185], v[18:21]
	v_mfma_f32_16x16x32_bf16 v[22:25], v[150:153], v[182:185], v[22:25]
	v_mfma_f32_16x16x32_bf16 v[14:17], v[150:153], v[204:207], v[14:17]
	v_mfma_f32_16x16x32_bf16 v[10:13], v[158:161], v[204:207], v[10:13]
	v_mfma_f32_16x16x32_bf16 v[2:5], v[158:161], v[212:215], v[2:5]
	v_mfma_f32_16x16x32_bf16 v[6:9], v[150:153], v[212:215], v[6:9]
	v_mfma_f32_16x16x32_bf16 v[30:33], v[154:157], v[178:181], v[30:33]
	v_mfma_f32_16x16x32_bf16 v[26:29], v[162:165], v[178:181], v[26:29]
	v_mfma_f32_16x16x32_bf16 v[18:21], v[162:165], v[200:203], v[18:21]
	v_mfma_f32_16x16x32_bf16 v[22:25], v[154:157], v[200:203], v[22:25]
	v_mfma_f32_16x16x32_bf16 v[14:17], v[154:157], v[208:211], v[14:17]
	v_mfma_f32_16x16x32_bf16 v[10:13], v[162:165], v[208:211], v[10:13]
	v_mfma_f32_16x16x32_bf16 v[2:5], v[162:165], v[216:219], v[2:5]
	v_mfma_f32_16x16x32_bf16 v[6:9], v[154:157], v[216:219], v[6:9]
	s_setprio 3
	s_barrier
	ds_read_b128 v[134:137], v132
	ds_read_b128 v[138:141], v132 offset:1024
	ds_read_b128 v[142:145], v132 offset:2048
	ds_read_b128 v[146:149], v132 offset:3072
	ds_read_b128 v[150:153], v133
	ds_read_b128 v[154:157], v133 offset:1024
	ds_read_b128 v[158:161], v133 offset:2048
	ds_read_b128 v[162:165], v133 offset:3072
	s_add_u32 s40, s40, 0x40000
	s_addc_u32 s41, s41, 0
	s_mov_b32 m0, s45
	v_lshl_add_u64 v[228:229], s[40:41], 0, v[194:195]
	ds_read_b128 v[166:169], v223 offset:32768
	ds_read_b128 v[178:181], v223 offset:33792
	ds_read_b128 v[182:185], v223 offset:34816
	ds_read_b128 v[200:203], v223 offset:35840
	ds_read_b128 v[204:207], v223 offset:36864
	ds_read_b128 v[208:211], v223 offset:37888
	ds_read_b128 v[212:215], v223 offset:38912
	ds_read_b128 v[216:219], v223 offset:39936
	global_load_lds_dwordx4 v[228:229], off
	v_lshl_add_u64 v[228:229], s[40:41], 0, v[192:193]
	s_mov_b32 m0, s46
	s_nop 0
	global_load_lds_dwordx4 v[228:229], off
	s_waitcnt vmcnt(8)
	s_waitcnt lgkmcnt(0)
	s_barrier
	s_setprio 0
	s_waitcnt lgkmcnt(0)
	v_mfma_f32_16x16x32_bf16 v[128:131], v[134:137], v[166:169], v[128:131]
	v_mfma_f32_16x16x32_bf16 v[124:127], v[142:145], v[166:169], v[124:127]
	v_mfma_f32_16x16x32_bf16 v[116:119], v[142:145], v[182:185], v[116:119]
	v_mfma_f32_16x16x32_bf16 v[120:123], v[134:137], v[182:185], v[120:123]
	v_mfma_f32_16x16x32_bf16 v[112:115], v[134:137], v[204:207], v[112:115]
	v_mfma_f32_16x16x32_bf16 v[108:111], v[142:145], v[204:207], v[108:111]
	v_mfma_f32_16x16x32_bf16 v[100:103], v[142:145], v[212:215], v[100:103]
	v_mfma_f32_16x16x32_bf16 v[104:107], v[134:137], v[212:215], v[104:107]
	v_mfma_f32_16x16x32_bf16 v[128:131], v[138:141], v[178:181], v[128:131]
	v_mfma_f32_16x16x32_bf16 v[124:127], v[146:149], v[178:181], v[124:127]
	v_mfma_f32_16x16x32_bf16 v[116:119], v[146:149], v[200:203], v[116:119]
	v_mfma_f32_16x16x32_bf16 v[120:123], v[138:141], v[200:203], v[120:123]
	v_mfma_f32_16x16x32_bf16 v[112:115], v[138:141], v[208:211], v[112:115]
	v_mfma_f32_16x16x32_bf16 v[108:111], v[146:149], v[208:211], v[108:111]
	v_mfma_f32_16x16x32_bf16 v[100:103], v[146:149], v[216:219], v[100:103]
	v_mfma_f32_16x16x32_bf16 v[104:107], v[138:141], v[216:219], v[104:107]
	s_setprio 3
	s_setprio 0
	v_mfma_f32_16x16x32_bf16 v[96:99], v[150:153], v[166:169], v[96:99]
	v_mfma_f32_16x16x32_bf16 v[92:95], v[158:161], v[166:169], v[92:95]
	v_mfma_f32_16x16x32_bf16 v[84:87], v[158:161], v[182:185], v[84:87]
	v_mfma_f32_16x16x32_bf16 v[88:91], v[150:153], v[182:185], v[88:91]
	v_mfma_f32_16x16x32_bf16 v[80:83], v[150:153], v[204:207], v[80:83]
	v_mfma_f32_16x16x32_bf16 v[76:79], v[158:161], v[204:207], v[76:79]
	v_mfma_f32_16x16x32_bf16 v[68:71], v[158:161], v[212:215], v[68:71]
	v_mfma_f32_16x16x32_bf16 v[72:75], v[150:153], v[212:215], v[72:75]
	v_mfma_f32_16x16x32_bf16 v[96:99], v[154:157], v[178:181], v[96:99]
	v_mfma_f32_16x16x32_bf16 v[92:95], v[162:165], v[178:181], v[92:95]
	v_mfma_f32_16x16x32_bf16 v[84:87], v[162:165], v[200:203], v[84:87]
	v_mfma_f32_16x16x32_bf16 v[88:91], v[154:157], v[200:203], v[88:91]
	v_mfma_f32_16x16x32_bf16 v[80:83], v[154:157], v[208:211], v[80:83]
	v_mfma_f32_16x16x32_bf16 v[76:79], v[162:165], v[208:211], v[76:79]
	v_mfma_f32_16x16x32_bf16 v[68:71], v[162:165], v[216:219], v[68:71]
	v_mfma_f32_16x16x32_bf16 v[72:75], v[154:157], v[216:219], v[72:75]
	s_setprio 3
	s_barrier
	s_mov_b32 m0, s68
	v_lshl_add_u64 v[170:171], v[170:171], 0, s[18:19]
	s_add_u32 s30, s30, 0x40080
	ds_read_b128 v[166:169], v223 offset:49152
	ds_read_b128 v[178:181], v223 offset:50176
	ds_read_b128 v[182:185], v223 offset:51200
	ds_read_b128 v[200:203], v223 offset:52224
	ds_read_b128 v[204:207], v223 offset:53248
	ds_read_b128 v[208:211], v223 offset:54272
	ds_read_b128 v[212:215], v223 offset:55296
	ds_read_b128 v[216:219], v223 offset:56320
	global_load_lds_dwordx4 v[170:171], off
	v_lshl_add_u64 v[170:171], v[174:175], 0, s[18:19]
	s_mov_b32 m0, s69
	s_addc_u32 s31, s31, 0
	global_load_lds_dwordx4 v[170:171], off
	v_lshl_add_u64 v[170:171], s[30:31], 0, v[34:35]
	s_mov_b32 m0, s70
	s_nop 0
	global_load_lds_dwordx4 v[170:171], off
	v_lshl_add_u64 v[170:171], s[30:31], 0, v[190:191]
	s_mov_b32 m0, s71
	s_nop 0
	global_load_lds_dwordx4 v[170:171], off
	v_lshl_add_u64 v[170:171], v[224:225], 0, s[18:19]
	s_mov_b32 m0, s51
	s_nop 0
	global_load_lds_dwordx4 v[170:171], off
	v_lshl_add_u64 v[170:171], v[226:227], 0, s[18:19]
	s_mov_b32 m0, s52
	s_nop 0
	global_load_lds_dwordx4 v[170:171], off
	s_waitcnt vmcnt(8)
	s_waitcnt lgkmcnt(0)
	s_barrier
	s_setprio 0
	s_waitcnt lgkmcnt(0)
	v_mfma_f32_16x16x32_bf16 v[64:67], v[134:137], v[166:169], v[64:67]
	v_mfma_f32_16x16x32_bf16 v[60:63], v[142:145], v[166:169], v[60:63]
	v_mfma_f32_16x16x32_bf16 v[52:55], v[142:145], v[182:185], v[52:55]
	v_mfma_f32_16x16x32_bf16 v[56:59], v[134:137], v[182:185], v[56:59]
	v_mfma_f32_16x16x32_bf16 v[48:51], v[134:137], v[204:207], v[48:51]
	v_mfma_f32_16x16x32_bf16 v[44:47], v[142:145], v[204:207], v[44:47]
	v_mfma_f32_16x16x32_bf16 v[36:39], v[142:145], v[212:215], v[36:39]
	v_mfma_f32_16x16x32_bf16 v[40:43], v[134:137], v[212:215], v[40:43]
	v_mfma_f32_16x16x32_bf16 v[64:67], v[138:141], v[178:181], v[64:67]
	v_mfma_f32_16x16x32_bf16 v[60:63], v[146:149], v[178:181], v[60:63]
	v_mfma_f32_16x16x32_bf16 v[52:55], v[146:149], v[200:203], v[52:55]
	v_mfma_f32_16x16x32_bf16 v[56:59], v[138:141], v[200:203], v[56:59]
	v_mfma_f32_16x16x32_bf16 v[48:51], v[138:141], v[208:211], v[48:51]
	v_mfma_f32_16x16x32_bf16 v[44:47], v[146:149], v[208:211], v[44:47]
	v_mfma_f32_16x16x32_bf16 v[36:39], v[146:149], v[216:219], v[36:39]
	v_mfma_f32_16x16x32_bf16 v[40:43], v[138:141], v[216:219], v[40:43]
	s_setprio 3
	s_setprio 0
	v_mfma_f32_16x16x32_bf16 v[30:33], v[150:153], v[166:169], v[30:33]
	v_mfma_f32_16x16x32_bf16 v[26:29], v[158:161], v[166:169], v[26:29]
	v_mfma_f32_16x16x32_bf16 v[18:21], v[158:161], v[182:185], v[18:21]
	v_mfma_f32_16x16x32_bf16 v[22:25], v[150:153], v[182:185], v[22:25]
	v_mfma_f32_16x16x32_bf16 v[14:17], v[150:153], v[204:207], v[14:17]
	v_mfma_f32_16x16x32_bf16 v[10:13], v[158:161], v[204:207], v[10:13]
	v_mfma_f32_16x16x32_bf16 v[2:5], v[158:161], v[212:215], v[2:5]
	v_mfma_f32_16x16x32_bf16 v[6:9], v[150:153], v[212:215], v[6:9]
	v_mfma_f32_16x16x32_bf16 v[30:33], v[154:157], v[178:181], v[30:33]
	v_mfma_f32_16x16x32_bf16 v[26:29], v[162:165], v[178:181], v[26:29]
	v_mfma_f32_16x16x32_bf16 v[18:21], v[162:165], v[200:203], v[18:21]
	v_mfma_f32_16x16x32_bf16 v[22:25], v[154:157], v[200:203], v[22:25]
	v_mfma_f32_16x16x32_bf16 v[14:17], v[154:157], v[208:211], v[14:17]
	v_mfma_f32_16x16x32_bf16 v[10:13], v[162:165], v[208:211], v[10:13]
	v_mfma_f32_16x16x32_bf16 v[2:5], v[162:165], v[216:219], v[2:5]
	v_mfma_f32_16x16x32_bf16 v[6:9], v[154:157], v[216:219], v[6:9]
	s_setprio 3
	s_barrier
	s_add_i32 s74, s74, 2
	s_add_u32 s36, s36, 0x100
	s_addc_u32 s37, s37, 0
	s_add_u32 s72, s72, 0x100
	s_addc_u32 s73, s73, 0
	s_cmp_gt_u32 s74, 13
	s_cbranch_scc0 .LBB0_541
	v_readlane_b32 s74, v255, 3
	s_and_b64 vcc, exec, s[10:11]
	v_readlane_b32 s75, v255, 4
	s_mov_b32 s58, 0x19b00000
	v_readlane_b32 s59, v255, 10
	s_mov_b32 s60, 0xff61b1e6
	s_mov_b64 s[62:63], 0x800
	s_mov_b32 s64, 0x3b000000
	s_cbranch_vccz .LBB0_544
	s_barrier

.LBB0_819:
	s_add_u32 s81, s30, 0x200
	s_addc_u32 s82, s31, 0
	s_add_i32 s55, 0, 0x14000
	s_add_i32 s52, 0, 0x10000
	v_add_u32_e32 v199, s55, v167
	v_add_u32_e32 v200, s52, v167
	ds_read_b128 v[10:13], v199
	ds_read_b128 v[14:17], v199 offset:1024
	ds_read_b128 v[2:5], v199 offset:2048
	ds_read_b128 v[6:9], v199 offset:3072
	ds_read_b128 v[22:25], v200 offset:3072
	ds_read_b128 v[18:21], v200 offset:2048
	ds_read_b128 v[30:33], v200 offset:1024
	ds_read_b128 v[26:29], v200
	s_lshl_b32 s14, s80, 10
	s_add_i32 s83, s14, 0
	s_add_i32 s83, s83, 0x20400
	v_mov_b32_e32 v191, v35
	v_mov_b32_e32 v175, v35
	s_add_i32 s84, s69, 0xc000
	v_readlane_b32 s26, v253, 28
	s_mov_b32 m0, s84
	v_readlane_b32 s27, v253, 29
	s_add_i32 s53, s69, 0xe000
	ds_read_b128 v[202:205], v169
	ds_read_b128 v[206:209], v169 offset:1024
	ds_read_b128 v[222:225], v169 offset:2048
	ds_read_b128 v[226:229], v169 offset:3072
	ds_read_b128 v[230:233], v169 offset:4096
	ds_read_b128 v[234:237], v169 offset:5120
	ds_read_b128 v[238:241], v169 offset:6144
	ds_read_b128 v[242:245], v169 offset:7168
	global_load_lds_dwordx4 v190, s[26:27]
	s_mov_b32 m0, s53
	s_nop 0
	global_load_lds_dwordx4 v174, s[26:27]
	s_waitcnt vmcnt(8)
	s_waitcnt lgkmcnt(0)
	s_barrier
	s_setprio 0
	s_waitcnt lgkmcnt(0)
	v_mfma_f32_16x16x128_f8f6f4 v[160:163], v[26:33], v[202:209], 0
	v_mfma_f32_16x16x128_f8f6f4 v[156:159], v[18:25], v[202:209], 0
	v_mfma_f32_16x16x128_f8f6f4 v[148:151], v[18:25], v[222:229], 0
	v_mfma_f32_16x16x128_f8f6f4 v[152:155], v[26:33], v[222:229], 0
	v_mfma_f32_16x16x128_f8f6f4 v[144:147], v[26:33], v[230:237], 0
	v_mfma_f32_16x16x128_f8f6f4 v[140:143], v[18:25], v[230:237], 0
	v_mfma_f32_16x16x128_f8f6f4 v[132:135], v[18:25], v[238:245], 0
	v_mfma_f32_16x16x128_f8f6f4 v[136:139], v[26:33], v[238:245], 0
	s_setprio 3
	s_setprio 0
	v_mfma_f32_16x16x128_f8f6f4 v[128:131], v[10:17], v[202:209], 0
	v_mfma_f32_16x16x128_f8f6f4 v[124:127], v[2:9], v[202:209], 0
	v_mfma_f32_16x16x128_f8f6f4 v[116:119], v[2:9], v[222:229], 0
	v_mfma_f32_16x16x128_f8f6f4 v[120:123], v[10:17], v[222:229], 0
	v_mfma_f32_16x16x128_f8f6f4 v[112:115], v[10:17], v[230:237], 0
	v_mfma_f32_16x16x128_f8f6f4 v[108:111], v[2:9], v[230:237], 0
	v_mfma_f32_16x16x128_f8f6f4 v[100:103], v[2:9], v[238:245], 0
	v_mfma_f32_16x16x128_f8f6f4 v[104:107], v[10:17], v[238:245], 0
	s_setprio 3
	s_barrier
	s_add_i32 s52, s52, s68
	v_lshl_add_u64 v[194:195], s[30:31], 0, v[170:171]
	s_add_i32 s85, s52, 0x2000
	v_lshl_add_u64 v[178:179], v[194:195], 0, s[28:29]
	s_mov_b32 m0, s52
	v_lshl_add_u64 v[196:197], s[30:31], 0, v[172:173]
	s_add_u32 s36, s30, 0x20100
	ds_read_b128 v[202:205], v169 offset:16384
	ds_read_b128 v[206:209], v169 offset:17408
	ds_read_b128 v[222:225], v169 offset:18432
	ds_read_b128 v[226:229], v169 offset:19456
	ds_read_b128 v[230:233], v169 offset:20480
	ds_read_b128 v[234:237], v169 offset:21504
	ds_read_b128 v[238:241], v169 offset:22528
	ds_read_b128 v[242:245], v169 offset:23552
	global_load_lds_dwordx4 v[178:179], off
	v_lshl_add_u64 v[178:179], v[196:197], 0, s[28:29]
	s_mov_b32 m0, s85
	s_addc_u32 s37, s31, 0
	s_add_i32 s55, s55, s68
	global_load_lds_dwordx4 v[178:179], off
	v_lshl_add_u64 v[178:179], s[36:37], 0, v[170:171]
	s_mov_b32 m0, s55
	s_add_i32 s65, s55, 0x2000
	global_load_lds_dwordx4 v[178:179], off
	v_lshl_add_u64 v[178:179], s[36:37], 0, v[172:173]
	s_mov_b32 m0, s65
	v_readlane_b32 s26, v253, 37
	global_load_lds_dwordx4 v[178:179], off
	s_mov_b32 m0, s69
	v_readlane_b32 s27, v253, 38
	s_nop 4
	global_load_lds_dwordx4 v34, s[26:27]
	s_mov_b32 m0, s70
	s_nop 0
	global_load_lds_dwordx4 v192, s[26:27]
	s_waitcnt vmcnt(8)
	s_waitcnt lgkmcnt(0)
	s_barrier
	s_setprio 0
	s_waitcnt lgkmcnt(0)
	v_mfma_f32_16x16x128_f8f6f4 v[96:99], v[26:33], v[202:209], 0
	v_mfma_f32_16x16x128_f8f6f4 v[92:95], v[18:25], v[202:209], 0
	v_mfma_f32_16x16x128_f8f6f4 v[84:87], v[18:25], v[222:229], 0
	v_mfma_f32_16x16x128_f8f6f4 v[88:91], v[26:33], v[222:229], 0
	v_mfma_f32_16x16x128_f8f6f4 v[80:83], v[26:33], v[230:237], 0
	v_mfma_f32_16x16x128_f8f6f4 v[76:79], v[18:25], v[230:237], 0
	v_mfma_f32_16x16x128_f8f6f4 v[68:71], v[18:25], v[238:245], 0
	v_mfma_f32_16x16x128_f8f6f4 v[72:75], v[26:33], v[238:245], 0
	s_setprio 3
	s_setprio 0
	v_mfma_f32_16x16x128_f8f6f4 v[64:67], v[10:17], v[202:209], 0
	v_mfma_f32_16x16x128_f8f6f4 v[60:63], v[2:9], v[202:209], 0
	v_mfma_f32_16x16x128_f8f6f4 v[52:55], v[2:9], v[222:229], 0
	v_mfma_f32_16x16x128_f8f6f4 v[56:59], v[10:17], v[222:229], 0
	v_mfma_f32_16x16x128_f8f6f4 v[48:51], v[10:17], v[230:237], 0
	v_mfma_f32_16x16x128_f8f6f4 v[44:47], v[2:9], v[230:237], 0
	v_mfma_f32_16x16x128_f8f6f4 v[36:39], v[2:9], v[238:245], 0
	v_mfma_f32_16x16x128_f8f6f4 v[40:43], v[10:17], v[238:245], 0
	s_setprio 3
	s_barrier
	s_add_i32 s54, 0, 0x18000
	s_add_i32 s51, 0, 0x1c000
	v_add_u32_e32 v201, s54, v167
	v_add_u32_e32 v202, s51, v167
	ds_read_b128 v[26:29], v201
	ds_read_b128 v[30:33], v201 offset:1024
	ds_read_b128 v[18:21], v201 offset:2048
	ds_read_b128 v[22:25], v201 offset:3072
	ds_read_b128 v[10:13], v202
	ds_read_b128 v[14:17], v202 offset:1024
	ds_read_b128 v[2:5], v202 offset:2048
	ds_read_b128 v[6:9], v202 offset:3072
	s_mov_b32 m0, s71
	ds_read_b128 v[204:207], v169 offset:32768
	ds_read_b128 v[208:211], v169 offset:33792
	ds_read_b128 v[222:225], v169 offset:34816
	ds_read_b128 v[226:229], v169 offset:35840
	ds_read_b128 v[230:233], v169 offset:36864
	ds_read_b128 v[234:237], v169 offset:37888
	ds_read_b128 v[238:241], v169 offset:38912
	ds_read_b128 v[242:245], v169 offset:39936
	global_load_lds_dwordx4 v189, s[26:27]
	s_mov_b32 m0, s72
	s_nop 0
	global_load_lds_dwordx4 v198, s[26:27]
	s_waitcnt vmcnt(8)
	s_waitcnt lgkmcnt(0)
	s_barrier
	s_setprio 0
	s_waitcnt lgkmcnt(0)
	v_mfma_f32_16x16x128_f8f6f4 v[160:163], v[26:33], v[204:211], v[160:163]
	v_mfma_f32_16x16x128_f8f6f4 v[156:159], v[18:25], v[204:211], v[156:159]
	v_mfma_f32_16x16x128_f8f6f4 v[148:151], v[18:25], v[222:229], v[148:151]
	v_mfma_f32_16x16x128_f8f6f4 v[152:155], v[26:33], v[222:229], v[152:155]
	v_mfma_f32_16x16x128_f8f6f4 v[144:147], v[26:33], v[230:237], v[144:147]
	v_mfma_f32_16x16x128_f8f6f4 v[140:143], v[18:25], v[230:237], v[140:143]
	v_mfma_f32_16x16x128_f8f6f4 v[132:135], v[18:25], v[238:245], v[132:135]
	v_mfma_f32_16x16x128_f8f6f4 v[136:139], v[26:33], v[238:245], v[136:139]
	s_setprio 3
	s_setprio 0
	v_mfma_f32_16x16x128_f8f6f4 v[128:131], v[10:17], v[204:211], v[128:131]
	v_mfma_f32_16x16x128_f8f6f4 v[124:127], v[2:9], v[204:211], v[124:127]
	v_mfma_f32_16x16x128_f8f6f4 v[116:119], v[2:9], v[222:229], v[116:119]
	v_mfma_f32_16x16x128_f8f6f4 v[120:123], v[10:17], v[222:229], v[120:123]
	v_mfma_f32_16x16x128_f8f6f4 v[112:115], v[10:17], v[230:237], v[112:115]
	v_mfma_f32_16x16x128_f8f6f4 v[108:111], v[2:9], v[230:237], v[108:111]
	v_mfma_f32_16x16x128_f8f6f4 v[100:103], v[2:9], v[238:245], v[100:103]
	v_mfma_f32_16x16x128_f8f6f4 v[104:107], v[10:17], v[238:245], v[104:107]
	s_setprio 3
	s_barrier
	s_add_i32 s54, s54, s68
	s_mov_b64 s[26:27], 0x180
	s_add_i32 s50, s54, 0x2000
	v_lshl_add_u64 v[178:179], v[194:195], 0, s[26:27]
	s_mov_b32 m0, s54
	s_add_u32 s30, s30, 0x20180
	ds_read_b128 v[204:207], v169 offset:49152
	ds_read_b128 v[208:211], v169 offset:50176
	ds_read_b128 v[222:225], v169 offset:51200
	ds_read_b128 v[226:229], v169 offset:52224
	ds_read_b128 v[230:233], v169 offset:53248
	ds_read_b128 v[234:237], v169 offset:54272
	ds_read_b128 v[238:241], v169 offset:55296
	ds_read_b128 v[242:245], v169 offset:56320
	global_load_lds_dwordx4 v[178:179], off
	v_lshl_add_u64 v[178:179], v[196:197], 0, s[26:27]
	s_mov_b32 m0, s50
	s_addc_u32 s31, s31, 0
	s_add_i32 s51, s51, s68
	global_load_lds_dwordx4 v[178:179], off
	v_lshl_add_u64 v[178:179], s[30:31], 0, v[170:171]
	s_mov_b32 m0, s51
	s_add_i32 s64, s51, 0x2000
	global_load_lds_dwordx4 v[178:179], off
	v_lshl_add_u64 v[178:179], s[30:31], 0, v[172:173]
	s_mov_b32 m0, s64
	v_readlane_b32 s26, v253, 39
	global_load_lds_dwordx4 v[178:179], off
	s_mov_b32 m0, s75
	v_readlane_b32 s27, v253, 40
	s_nop 4
	global_load_lds_dwordx4 v34, s[26:27]
	s_mov_b32 m0, s76
	s_nop 0
	global_load_lds_dwordx4 v192, s[26:27]
	s_waitcnt vmcnt(8)
	s_waitcnt lgkmcnt(0)
	s_barrier
	s_setprio 0
	s_waitcnt lgkmcnt(0)
	v_mfma_f32_16x16x128_f8f6f4 v[96:99], v[26:33], v[204:211], v[96:99]
	v_mfma_f32_16x16x128_f8f6f4 v[92:95], v[18:25], v[204:211], v[92:95]
	v_mfma_f32_16x16x128_f8f6f4 v[84:87], v[18:25], v[222:229], v[84:87]
	v_mfma_f32_16x16x128_f8f6f4 v[88:91], v[26:33], v[222:229], v[88:91]
	v_mfma_f32_16x16x128_f8f6f4 v[80:83], v[26:33], v[230:237], v[80:83]
	v_mfma_f32_16x16x128_f8f6f4 v[76:79], v[18:25], v[230:237], v[76:79]
	v_mfma_f32_16x16x128_f8f6f4 v[68:71], v[18:25], v[238:245], v[68:71]
	v_mfma_f32_16x16x128_f8f6f4 v[72:75], v[26:33], v[238:245], v[72:75]
	s_setprio 3
	s_setprio 0
	v_mfma_f32_16x16x128_f8f6f4 v[64:67], v[10:17], v[204:211], v[64:67]
	v_mfma_f32_16x16x128_f8f6f4 v[60:63], v[2:9], v[204:211], v[60:63]
	v_mfma_f32_16x16x128_f8f6f4 v[52:55], v[2:9], v[222:229], v[52:55]
	v_mfma_f32_16x16x128_f8f6f4 v[56:59], v[10:17], v[222:229], v[56:59]
	v_mfma_f32_16x16x128_f8f6f4 v[48:51], v[10:17], v[230:237], v[48:51]
	v_mfma_f32_16x16x128_f8f6f4 v[44:47], v[2:9], v[230:237], v[44:47]
	v_mfma_f32_16x16x128_f8f6f4 v[36:39], v[2:9], v[238:245], v[36:39]
	v_mfma_f32_16x16x128_f8f6f4 v[40:43], v[10:17], v[238:245], v[40:43]
	s_setprio 3
	s_barrier
	v_lshl_add_u64 v[18:19], s[26:27], 0, v[174:175]
	v_lshl_add_u64 v[20:21], s[26:27], 0, v[190:191]
	s_mov_b32 s63, 0
	s_mov_b64 s[30:31], 0
	s_branch .LBB0_821
.LBB0_820:
	ds_read_b128 v[204:207], v200
	ds_read_b128 v[208:211], v200 offset:1024
	ds_read_b128 v[222:225], v200 offset:2048
	ds_read_b128 v[226:229], v200 offset:3072
	ds_read_b128 v[10:13], v199
	ds_read_b128 v[14:17], v199 offset:1024
	ds_read_b128 v[2:5], v199 offset:2048
	ds_read_b128 v[6:9], v199 offset:3072
	s_add_u32 s14, s30, 0x200
	s_addc_u32 s86, s31, 0
	s_and_b64 s[40:41], s[36:37], exec
	s_cselect_b32 s14, 0, s14
	s_cselect_b32 s41, 0, s86
	s_add_u32 s40, s20, s14
	s_addc_u32 s41, s21, s41
	s_add_u32 s14, s81, s30
	s_addc_u32 s86, s82, s31
	s_and_b64 s[36:37], s[36:37], exec
	s_cselect_b32 s37, s23, s86
	s_cselect_b32 s36, s22, s14
	s_mov_b32 m0, s84
	v_lshl_add_u64 v[30:31], v[20:21], 0, s[30:31]
	ds_read_b128 v[22:25], v169
	ds_read_b128 v[26:29], v169 offset:1024
	ds_read_b128 v[230:233], v169 offset:2048
	ds_read_b128 v[234:237], v169 offset:3072
	ds_read_b128 v[238:241], v169 offset:4096
	ds_read_b128 v[242:245], v169 offset:5120
	ds_read_b128 v[178:181], v169 offset:6144
	ds_read_b128 v[182:185], v169 offset:7168
	global_load_lds_dwordx4 v[30:31], off
	v_lshl_add_u64 v[30:31], v[18:19], 0, s[30:31]
	s_mov_b32 m0, s53
	s_nop 0
	global_load_lds_dwordx4 v[30:31], off
	s_waitcnt vmcnt(8)
	s_waitcnt lgkmcnt(0)
	s_barrier
	s_setprio 0
	s_waitcnt lgkmcnt(0)
	v_mfma_f32_16x16x128_f8f6f4 v[160:163], v[204:211], v[22:29], v[160:163]
	v_mfma_f32_16x16x128_f8f6f4 v[156:159], v[222:229], v[22:29], v[156:159]
	v_mfma_f32_16x16x128_f8f6f4 v[148:151], v[222:229], v[230:237], v[148:151]
	v_mfma_f32_16x16x128_f8f6f4 v[152:155], v[204:211], v[230:237], v[152:155]
	v_mfma_f32_16x16x128_f8f6f4 v[144:147], v[204:211], v[238:245], v[144:147]
	v_mfma_f32_16x16x128_f8f6f4 v[140:143], v[222:229], v[238:245], v[140:143]
	v_mfma_f32_16x16x128_f8f6f4 v[132:135], v[222:229], v[178:185], v[132:135]
	v_mfma_f32_16x16x128_f8f6f4 v[136:139], v[204:211], v[178:185], v[136:139]
	s_setprio 3
	s_setprio 0
	v_mfma_f32_16x16x128_f8f6f4 v[128:131], v[10:17], v[22:29], v[128:131]
	v_mfma_f32_16x16x128_f8f6f4 v[124:127], v[2:9], v[22:29], v[124:127]
	v_mfma_f32_16x16x128_f8f6f4 v[116:119], v[2:9], v[230:237], v[116:119]
	v_mfma_f32_16x16x128_f8f6f4 v[120:123], v[10:17], v[230:237], v[120:123]
	v_mfma_f32_16x16x128_f8f6f4 v[112:115], v[10:17], v[238:245], v[112:115]
	v_mfma_f32_16x16x128_f8f6f4 v[108:111], v[2:9], v[238:245], v[108:111]
	v_mfma_f32_16x16x128_f8f6f4 v[100:103], v[2:9], v[178:185], v[100:103]
	v_mfma_f32_16x16x128_f8f6f4 v[104:107], v[10:17], v[178:185], v[104:107]
	s_setprio 3
	s_barrier
	s_mov_b32 m0, s52
	v_lshl_add_u64 v[22:23], s[36:37], 0, v[170:171]
	s_add_u32 s86, s36, 0x20000
	ds_read_b128 v[178:181], v169 offset:16384
	ds_read_b128 v[182:185], v169 offset:17408
	ds_read_b128 v[230:233], v169 offset:18432
	ds_read_b128 v[234:237], v169 offset:19456
	ds_read_b128 v[238:241], v169 offset:20480
	ds_read_b128 v[242:245], v169 offset:21504
	ds_read_b128 v[212:215], v169 offset:22528
	ds_read_b128 v[216:219], v169 offset:23552
	global_load_lds_dwordx4 v[22:23], off
	v_lshl_add_u64 v[24:25], s[36:37], 0, v[172:173]
	s_mov_b32 m0, s85
	s_addc_u32 s87, s37, 0
	global_load_lds_dwordx4 v[24:25], off
	v_lshl_add_u64 v[26:27], s[86:87], 0, v[170:171]
	s_mov_b32 m0, s55
	v_mov_b32_e32 v193, v35
	global_load_lds_dwordx4 v[26:27], off
	v_lshl_add_u64 v[26:27], s[86:87], 0, v[172:173]
	s_mov_b32 m0, s65
	v_lshl_add_u64 v[28:29], s[40:41], 0, v[34:35]
	global_load_lds_dwordx4 v[26:27], off
	s_mov_b32 m0, s69
	v_lshl_add_u64 v[26:27], s[40:41], 0, v[192:193]
	global_load_lds_dwordx4 v34, s[40:41]
	s_mov_b32 m0, s70
	s_nop 0
	global_load_lds_dwordx4 v192, s[40:41]
	s_waitcnt vmcnt(8)
	s_waitcnt lgkmcnt(0)
	s_barrier
	s_setprio 0
	s_waitcnt lgkmcnt(0)
	v_mfma_f32_16x16x128_f8f6f4 v[96:99], v[204:211], v[178:185], v[96:99]
	v_mfma_f32_16x16x128_f8f6f4 v[92:95], v[222:229], v[178:185], v[92:95]
	v_mfma_f32_16x16x128_f8f6f4 v[84:87], v[222:229], v[230:237], v[84:87]
	v_mfma_f32_16x16x128_f8f6f4 v[88:91], v[204:211], v[230:237], v[88:91]
	v_mfma_f32_16x16x128_f8f6f4 v[80:83], v[204:211], v[238:245], v[80:83]
	v_mfma_f32_16x16x128_f8f6f4 v[76:79], v[222:229], v[238:245], v[76:79]
	v_mfma_f32_16x16x128_f8f6f4 v[68:71], v[222:229], v[212:219], v[68:71]
	v_mfma_f32_16x16x128_f8f6f4 v[72:75], v[204:211], v[212:219], v[72:75]
	s_setprio 3
	s_setprio 0
	v_mfma_f32_16x16x128_f8f6f4 v[64:67], v[10:17], v[178:185], v[64:67]
	v_mfma_f32_16x16x128_f8f6f4 v[60:63], v[2:9], v[178:185], v[60:63]
	v_mfma_f32_16x16x128_f8f6f4 v[52:55], v[2:9], v[230:237], v[52:55]
	v_mfma_f32_16x16x128_f8f6f4 v[56:59], v[10:17], v[230:237], v[56:59]
	v_mfma_f32_16x16x128_f8f6f4 v[48:51], v[10:17], v[238:245], v[48:51]
	v_mfma_f32_16x16x128_f8f6f4 v[44:47], v[2:9], v[238:245], v[44:47]
	v_mfma_f32_16x16x128_f8f6f4 v[36:39], v[2:9], v[212:219], v[36:39]
	v_mfma_f32_16x16x128_f8f6f4 v[40:43], v[10:17], v[212:219], v[40:43]
	s_setprio 3
	s_barrier
	ds_read_b128 v[178:181], v201
	ds_read_b128 v[182:185], v201 offset:1024
	ds_read_b128 v[204:207], v201 offset:2048
	ds_read_b128 v[208:211], v201 offset:3072
	ds_read_b128 v[10:13], v202
	ds_read_b128 v[14:17], v202 offset:1024
	ds_read_b128 v[2:5], v202 offset:2048
	ds_read_b128 v[6:9], v202 offset:3072
	s_mov_b32 m0, s71
	ds_read_b128 v[212:215], v169 offset:32768
	ds_read_b128 v[216:219], v169 offset:33792
	ds_read_b128 v[222:225], v169 offset:34816
	ds_read_b128 v[226:229], v169 offset:35840
	ds_read_b128 v[230:233], v169 offset:36864
	ds_read_b128 v[234:237], v169 offset:37888
	ds_read_b128 v[238:241], v169 offset:38912
	ds_read_b128 v[242:245], v169 offset:39936
	global_load_lds_dwordx4 v189, s[40:41]
	s_mov_b32 m0, s72
	s_nop 0
	global_load_lds_dwordx4 v198, s[40:41]
	s_waitcnt vmcnt(8)
	s_waitcnt lgkmcnt(0)
	s_barrier
	s_setprio 0
	s_waitcnt lgkmcnt(0)
	v_mfma_f32_16x16x128_f8f6f4 v[160:163], v[178:185], v[212:219], v[160:163]
	v_mfma_f32_16x16x128_f8f6f4 v[156:159], v[204:211], v[212:219], v[156:159]
	v_mfma_f32_16x16x128_f8f6f4 v[148:151], v[204:211], v[222:229], v[148:151]
	v_mfma_f32_16x16x128_f8f6f4 v[152:155], v[178:185], v[222:229], v[152:155]
	v_mfma_f32_16x16x128_f8f6f4 v[144:147], v[178:185], v[230:237], v[144:147]
	v_mfma_f32_16x16x128_f8f6f4 v[140:143], v[204:211], v[230:237], v[140:143]
	v_mfma_f32_16x16x128_f8f6f4 v[132:135], v[204:211], v[238:245], v[132:135]
	v_mfma_f32_16x16x128_f8f6f4 v[136:139], v[178:185], v[238:245], v[136:139]
	s_setprio 3
	s_setprio 0
	v_mfma_f32_16x16x128_f8f6f4 v[128:131], v[10:17], v[212:219], v[128:131]
	v_mfma_f32_16x16x128_f8f6f4 v[124:127], v[2:9], v[212:219], v[124:127]
	v_mfma_f32_16x16x128_f8f6f4 v[116:119], v[2:9], v[222:229], v[116:119]
	v_mfma_f32_16x16x128_f8f6f4 v[120:123], v[10:17], v[222:229], v[120:123]
	v_mfma_f32_16x16x128_f8f6f4 v[112:115], v[10:17], v[230:237], v[112:115]
	v_mfma_f32_16x16x128_f8f6f4 v[108:111], v[2:9], v[230:237], v[108:111]
	v_mfma_f32_16x16x128_f8f6f4 v[100:103], v[2:9], v[238:245], v[100:103]
	v_mfma_f32_16x16x128_f8f6f4 v[104:107], v[10:17], v[238:245], v[104:107]
	s_setprio 3
	s_barrier
	s_mov_b32 m0, s54
	v_lshl_add_u64 v[22:23], v[22:23], 0, s[18:19]
	s_add_u32 s36, s36, 0x20080
	ds_read_b128 v[212:215], v169 offset:49152
	ds_read_b128 v[216:219], v169 offset:50176
	ds_read_b128 v[222:225], v169 offset:51200
	ds_read_b128 v[226:229], v169 offset:52224
	ds_read_b128 v[230:233], v169 offset:53248
	ds_read_b128 v[234:237], v169 offset:54272
	ds_read_b128 v[238:241], v169 offset:55296
	ds_read_b128 v[242:245], v169 offset:56320
	global_load_lds_dwordx4 v[22:23], off
	v_lshl_add_u64 v[22:23], v[24:25], 0, s[18:19]
	s_mov_b32 m0, s50
	s_addc_u32 s37, s37, 0
	global_load_lds_dwordx4 v[22:23], off
	v_lshl_add_u64 v[22:23], s[36:37], 0, v[170:171]
	s_mov_b32 m0, s51
	s_nop 0
	global_load_lds_dwordx4 v[22:23], off
	v_lshl_add_u64 v[22:23], s[36:37], 0, v[172:173]
	s_mov_b32 m0, s64
	s_nop 0
	global_load_lds_dwordx4 v[22:23], off
	v_lshl_add_u64 v[22:23], v[28:29], 0, s[18:19]
	s_mov_b32 m0, s75
	s_nop 0
	global_load_lds_dwordx4 v[22:23], off
	v_lshl_add_u64 v[22:23], v[26:27], 0, s[18:19]
	s_mov_b32 m0, s76
	s_nop 0
	global_load_lds_dwordx4 v[22:23], off
	s_waitcnt vmcnt(8)
	s_waitcnt lgkmcnt(0)
	s_barrier
	s_setprio 0
	s_waitcnt lgkmcnt(0)
	v_mfma_f32_16x16x128_f8f6f4 v[96:99], v[178:185], v[212:219], v[96:99]
	v_mfma_f32_16x16x128_f8f6f4 v[92:95], v[204:211], v[212:219], v[92:95]
	v_mfma_f32_16x16x128_f8f6f4 v[84:87], v[204:211], v[222:229], v[84:87]
	v_mfma_f32_16x16x128_f8f6f4 v[88:91], v[178:185], v[222:229], v[88:91]
	v_mfma_f32_16x16x128_f8f6f4 v[80:83], v[178:185], v[230:237], v[80:83]
	v_mfma_f32_16x16x128_f8f6f4 v[76:79], v[204:211], v[230:237], v[76:79]
	v_mfma_f32_16x16x128_f8f6f4 v[68:71], v[204:211], v[238:245], v[68:71]
	v_mfma_f32_16x16x128_f8f6f4 v[72:75], v[178:185], v[238:245], v[72:75]
	s_setprio 3
	s_setprio 0
	v_mfma_f32_16x16x128_f8f6f4 v[64:67], v[10:17], v[212:219], v[64:67]
	v_mfma_f32_16x16x128_f8f6f4 v[60:63], v[2:9], v[212:219], v[60:63]
	v_mfma_f32_16x16x128_f8f6f4 v[52:55], v[2:9], v[222:229], v[52:55]
	v_mfma_f32_16x16x128_f8f6f4 v[56:59], v[10:17], v[222:229], v[56:59]
	v_mfma_f32_16x16x128_f8f6f4 v[48:51], v[10:17], v[230:237], v[48:51]
	v_mfma_f32_16x16x128_f8f6f4 v[44:47], v[2:9], v[230:237], v[44:47]
	v_mfma_f32_16x16x128_f8f6f4 v[36:39], v[2:9], v[238:245], v[36:39]
	v_mfma_f32_16x16x128_f8f6f4 v[40:43], v[10:17], v[238:245], v[40:43]
	s_setprio 3
	s_barrier
	s_add_i32 s63, s63, 2
	s_add_u32 s30, s30, 0x100
	s_addc_u32 s31, s31, 0
	s_cmp_gt_u32 s63, 5
	s_cbranch_scc1 .LBB0_823

.LBB0_899:
	s_mul_i32 s14, s81, 0xe0000
	s_add_u32 s40, s44, s14
	s_addc_u32 s41, s45, 0
	s_and_b64 s[6:7], s[6:7], exec
	s_cselect_b32 s52, s41, s43
	s_cselect_b32 s53, s40, s42
	s_add_i32 s54, 0, 0x10000
	s_add_i32 s65, 0, 0x14000
	v_add_u32_e32 v34, s54, v167
	v_add_u32_e32 v206, s65, v167
	ds_read_b128 v[26:29], v34
	ds_read_b128 v[30:33], v34 offset:1024
	ds_read_b128 v[18:21], v34 offset:2048
	ds_read_b128 v[22:25], v34 offset:3072
	ds_read_b128 v[10:13], v206
	ds_read_b128 v[14:17], v206 offset:1024
	ds_read_b128 v[2:5], v206 offset:2048
	ds_read_b128 v[6:9], v206 offset:3072
	s_add_u32 s6, s42, 0x70080
	s_addc_u32 s7, s43, 0
	s_add_i32 s84, s72, 0xc000
	v_lshl_add_u64 v[216:217], s[6:7], 0, v[174:175]
	s_mov_b32 m0, s84
	s_add_i32 s85, s72, 0xe000
	ds_read_b128 v[178:181], v189
	ds_read_b128 v[182:185], v189 offset:1024
	ds_read_b128 v[198:201], v189 offset:2048
	ds_read_b128 v[202:205], v189 offset:3072
	ds_read_b128 v[208:211], v189 offset:4096
	ds_read_b128 v[212:215], v189 offset:5120
	ds_read_b128 v[222:225], v189 offset:6144
	ds_read_b128 v[226:229], v189 offset:7168
	global_load_lds_dwordx4 v[216:217], off
	v_lshl_add_u64 v[216:217], s[6:7], 0, v[170:171]
	s_mov_b32 m0, s85
	s_nop 0
	global_load_lds_dwordx4 v[216:217], off
	s_waitcnt vmcnt(8)
	s_waitcnt lgkmcnt(0)
	s_barrier
	s_setprio 0
	s_waitcnt lgkmcnt(0)
	v_mfma_f32_16x16x128_f8f6f4 v[160:163], v[26:33], v[178:185], 0
	v_mfma_f32_16x16x128_f8f6f4 v[156:159], v[18:25], v[178:185], 0
	v_mfma_f32_16x16x128_f8f6f4 v[148:151], v[18:25], v[198:205], 0
	v_mfma_f32_16x16x128_f8f6f4 v[152:155], v[26:33], v[198:205], 0
	v_mfma_f32_16x16x128_f8f6f4 v[144:147], v[26:33], v[208:215], 0
	v_mfma_f32_16x16x128_f8f6f4 v[140:143], v[18:25], v[208:215], 0
	v_mfma_f32_16x16x128_f8f6f4 v[132:135], v[18:25], v[222:229], 0
	v_mfma_f32_16x16x128_f8f6f4 v[136:139], v[26:33], v[222:229], 0
	s_setprio 3
	s_setprio 0
	v_mfma_f32_16x16x128_f8f6f4 v[128:131], v[10:17], v[178:185], 0
	v_mfma_f32_16x16x128_f8f6f4 v[124:127], v[2:9], v[178:185], 0
	v_mfma_f32_16x16x128_f8f6f4 v[116:119], v[2:9], v[198:205], 0
	v_mfma_f32_16x16x128_f8f6f4 v[120:123], v[10:17], v[198:205], 0
	v_mfma_f32_16x16x128_f8f6f4 v[112:115], v[10:17], v[208:215], 0
	v_mfma_f32_16x16x128_f8f6f4 v[108:111], v[2:9], v[208:215], 0
	v_mfma_f32_16x16x128_f8f6f4 v[100:103], v[2:9], v[222:229], 0
	v_mfma_f32_16x16x128_f8f6f4 v[104:107], v[10:17], v[222:229], 0
	s_setprio 3
	s_barrier
	v_lshl_add_u64 v[198:199], v[196:197], 0, v[172:173]
	s_add_i32 s54, s54, s71
	v_lshl_add_u64 v[200:201], v[198:199], 0, s[28:29]
	s_mov_b32 m0, s54
	ds_read_b128 v[178:181], v189 offset:16384
	ds_read_b128 v[182:185], v189 offset:17408
	ds_read_b128 v[208:211], v189 offset:18432
	ds_read_b128 v[212:215], v189 offset:19456
	ds_read_b128 v[222:225], v189 offset:20480
	ds_read_b128 v[226:229], v189 offset:21504
	ds_read_b128 v[230:233], v189 offset:22528
	ds_read_b128 v[234:237], v189 offset:23552
	global_load_lds_dwordx4 v[200:201], off
	v_lshl_add_u64 v[200:201], v[196:197], 0, v[168:169]
	s_add_i32 s55, s54, 0x2000
	v_lshl_add_u64 v[202:203], v[200:201], 0, s[28:29]
	s_mov_b32 m0, s55
	s_mov_b64 s[6:7], 0x70100
	global_load_lds_dwordx4 v[202:203], off
	v_lshl_add_u64 v[202:203], v[196:197], 0, s[6:7]
	s_add_i32 s65, s65, s71
	v_lshl_add_u64 v[204:205], v[202:203], 0, v[172:173]
	s_mov_b32 m0, s65
	s_add_i32 s67, s65, 0x2000
	global_load_lds_dwordx4 v[204:205], off
	v_lshl_add_u64 v[202:203], v[202:203], 0, v[168:169]
	s_mov_b32 m0, s67
	s_nop 0
	global_load_lds_dwordx4 v[202:203], off
	v_lshl_add_u64 v[202:203], s[42:43], 0, v[174:175]
	v_lshl_add_u64 v[204:205], v[202:203], 0, s[28:29]
	s_mov_b32 m0, s72
	s_nop 0
	global_load_lds_dwordx4 v[204:205], off
	v_lshl_add_u64 v[204:205], s[42:43], 0, v[170:171]
	v_lshl_add_u64 v[216:217], v[204:205], 0, s[28:29]
	s_mov_b32 m0, s73
	s_nop 0
	global_load_lds_dwordx4 v[216:217], off
	s_waitcnt vmcnt(8)
	s_waitcnt lgkmcnt(0)
	s_barrier
	s_setprio 0
	s_waitcnt lgkmcnt(0)
	v_mfma_f32_16x16x128_f8f6f4 v[96:99], v[26:33], v[178:185], 0
	v_mfma_f32_16x16x128_f8f6f4 v[92:95], v[18:25], v[178:185], 0
	v_mfma_f32_16x16x128_f8f6f4 v[84:87], v[18:25], v[208:215], 0
	v_mfma_f32_16x16x128_f8f6f4 v[88:91], v[26:33], v[208:215], 0
	v_mfma_f32_16x16x128_f8f6f4 v[80:83], v[26:33], v[222:229], 0
	v_mfma_f32_16x16x128_f8f6f4 v[76:79], v[18:25], v[222:229], 0
	v_mfma_f32_16x16x128_f8f6f4 v[68:71], v[18:25], v[230:237], 0
	v_mfma_f32_16x16x128_f8f6f4 v[72:75], v[26:33], v[230:237], 0
	s_setprio 3
	s_setprio 0
	v_mfma_f32_16x16x128_f8f6f4 v[64:67], v[10:17], v[178:185], 0
	v_mfma_f32_16x16x128_f8f6f4 v[60:63], v[2:9], v[178:185], 0
	v_mfma_f32_16x16x128_f8f6f4 v[52:55], v[2:9], v[208:215], 0
	v_mfma_f32_16x16x128_f8f6f4 v[56:59], v[10:17], v[208:215], 0
	v_mfma_f32_16x16x128_f8f6f4 v[48:51], v[10:17], v[222:229], 0
	v_mfma_f32_16x16x128_f8f6f4 v[44:47], v[2:9], v[222:229], 0
	v_mfma_f32_16x16x128_f8f6f4 v[36:39], v[2:9], v[230:237], 0
	v_mfma_f32_16x16x128_f8f6f4 v[40:43], v[10:17], v[230:237], 0
	s_setprio 3
	s_barrier
	s_add_i32 s50, 0, 0x18000
	s_add_i32 s63, 0, 0x1c000
	v_add_u32_e32 v207, s50, v167
	v_add_u32_e32 v208, s63, v167
	ds_read_b128 v[26:29], v207
	ds_read_b128 v[30:33], v207 offset:1024
	ds_read_b128 v[18:21], v207 offset:2048
	ds_read_b128 v[22:25], v207 offset:3072
	ds_read_b128 v[10:13], v208
	ds_read_b128 v[14:17], v208 offset:1024
	ds_read_b128 v[2:5], v208 offset:2048
	ds_read_b128 v[6:9], v208 offset:3072
	s_add_u32 s6, s42, 0x70100
	s_addc_u32 s7, s43, 0
	s_mov_b32 m0, s74
	v_lshl_add_u64 v[218:219], s[6:7], 0, v[174:175]
	ds_read_b128 v[178:181], v189 offset:32768
	ds_read_b128 v[182:185], v189 offset:33792
	ds_read_b128 v[210:213], v189 offset:34816
	ds_read_b128 v[214:217], v189 offset:35840
	ds_read_b128 v[222:225], v189 offset:36864
	ds_read_b128 v[226:229], v189 offset:37888
	ds_read_b128 v[230:233], v189 offset:38912
	ds_read_b128 v[234:237], v189 offset:39936
	global_load_lds_dwordx4 v[218:219], off
	v_lshl_add_u64 v[218:219], s[6:7], 0, v[170:171]
	s_mov_b32 m0, s75
	s_nop 0
	global_load_lds_dwordx4 v[218:219], off
	s_waitcnt vmcnt(8)
	s_waitcnt lgkmcnt(0)
	s_barrier
	s_setprio 0
	s_waitcnt lgkmcnt(0)
	v_mfma_f32_16x16x128_f8f6f4 v[160:163], v[26:33], v[178:185], v[160:163]
	v_mfma_f32_16x16x128_f8f6f4 v[156:159], v[18:25], v[178:185], v[156:159]
	v_mfma_f32_16x16x128_f8f6f4 v[148:151], v[18:25], v[210:217], v[148:151]
	v_mfma_f32_16x16x128_f8f6f4 v[152:155], v[26:33], v[210:217], v[152:155]
	v_mfma_f32_16x16x128_f8f6f4 v[144:147], v[26:33], v[222:229], v[144:147]
	v_mfma_f32_16x16x128_f8f6f4 v[140:143], v[18:25], v[222:229], v[140:143]
	v_mfma_f32_16x16x128_f8f6f4 v[132:135], v[18:25], v[230:237], v[132:135]
	v_mfma_f32_16x16x128_f8f6f4 v[136:139], v[26:33], v[230:237], v[136:139]
	s_setprio 3
	s_setprio 0
	v_mfma_f32_16x16x128_f8f6f4 v[128:131], v[10:17], v[178:185], v[128:131]
	v_mfma_f32_16x16x128_f8f6f4 v[124:127], v[2:9], v[178:185], v[124:127]
	v_mfma_f32_16x16x128_f8f6f4 v[116:119], v[2:9], v[210:217], v[116:119]
	v_mfma_f32_16x16x128_f8f6f4 v[120:123], v[10:17], v[210:217], v[120:123]
	v_mfma_f32_16x16x128_f8f6f4 v[112:115], v[10:17], v[222:229], v[112:115]
	v_mfma_f32_16x16x128_f8f6f4 v[108:111], v[2:9], v[222:229], v[108:111]
	v_mfma_f32_16x16x128_f8f6f4 v[100:103], v[2:9], v[230:237], v[100:103]
	v_mfma_f32_16x16x128_f8f6f4 v[104:107], v[10:17], v[230:237], v[104:107]
	s_setprio 3
	s_barrier
	s_mov_b64 s[6:7], 0x180
	s_add_i32 s50, s50, s71
	v_lshl_add_u64 v[198:199], v[198:199], 0, s[6:7]
	s_mov_b32 m0, s50
	s_add_i32 s51, s50, 0x2000
	ds_read_b128 v[178:181], v189 offset:49152
	ds_read_b128 v[182:185], v189 offset:50176
	ds_read_b128 v[210:213], v189 offset:51200
	ds_read_b128 v[214:217], v189 offset:52224
	ds_read_b128 v[222:225], v189 offset:53248
	ds_read_b128 v[226:229], v189 offset:54272
	ds_read_b128 v[230:233], v189 offset:55296
	ds_read_b128 v[234:237], v189 offset:56320
	global_load_lds_dwordx4 v[198:199], off
	v_lshl_add_u64 v[198:199], v[200:201], 0, s[6:7]
	s_mov_b32 m0, s51
	s_add_i32 s63, s63, s71
	global_load_lds_dwordx4 v[198:199], off
	v_lshl_add_u64 v[198:199], v[196:197], 0, s[26:27]
	v_lshl_add_u64 v[200:201], v[198:199], 0, v[172:173]
	s_mov_b32 m0, s63
	s_add_i32 s64, s63, 0x2000
	global_load_lds_dwordx4 v[200:201], off
	v_lshl_add_u64 v[198:199], v[198:199], 0, v[168:169]
	s_mov_b32 m0, s64
	s_nop 0
	global_load_lds_dwordx4 v[198:199], off
	v_lshl_add_u64 v[198:199], v[202:203], 0, s[6:7]
	s_mov_b32 m0, s77
	s_nop 0
	global_load_lds_dwordx4 v[198:199], off
	v_lshl_add_u64 v[198:199], v[204:205], 0, s[6:7]
	s_mov_b32 m0, s78
	s_nop 0
	global_load_lds_dwordx4 v[198:199], off
	s_waitcnt vmcnt(8)
	s_waitcnt lgkmcnt(0)
	s_barrier
	s_setprio 0
	s_waitcnt lgkmcnt(0)
	v_mfma_f32_16x16x128_f8f6f4 v[96:99], v[26:33], v[178:185], v[96:99]
	v_mfma_f32_16x16x128_f8f6f4 v[92:95], v[18:25], v[178:185], v[92:95]
	v_mfma_f32_16x16x128_f8f6f4 v[84:87], v[18:25], v[210:217], v[84:87]
	v_mfma_f32_16x16x128_f8f6f4 v[88:91], v[26:33], v[210:217], v[88:91]
	v_mfma_f32_16x16x128_f8f6f4 v[80:83], v[26:33], v[222:229], v[80:83]
	v_mfma_f32_16x16x128_f8f6f4 v[76:79], v[18:25], v[222:229], v[76:79]
	v_mfma_f32_16x16x128_f8f6f4 v[68:71], v[18:25], v[230:237], v[68:71]
	v_mfma_f32_16x16x128_f8f6f4 v[72:75], v[26:33], v[230:237], v[72:75]
	s_setprio 3
	s_setprio 0
	v_mfma_f32_16x16x128_f8f6f4 v[64:67], v[10:17], v[178:185], v[64:67]
	v_mfma_f32_16x16x128_f8f6f4 v[60:63], v[2:9], v[178:185], v[60:63]
	v_mfma_f32_16x16x128_f8f6f4 v[52:55], v[2:9], v[210:217], v[52:55]
	v_mfma_f32_16x16x128_f8f6f4 v[56:59], v[10:17], v[210:217], v[56:59]
	v_mfma_f32_16x16x128_f8f6f4 v[48:51], v[10:17], v[222:229], v[48:51]
	v_mfma_f32_16x16x128_f8f6f4 v[44:47], v[2:9], v[222:229], v[44:47]
	v_mfma_f32_16x16x128_f8f6f4 v[36:39], v[2:9], v[230:237], v[36:39]
	v_mfma_f32_16x16x128_f8f6f4 v[40:43], v[10:17], v[230:237], v[40:43]
	s_setprio 3
	s_barrier
	s_mov_b64 s[6:7], 0x200
	v_lshl_add_u64 v[18:19], v[196:197], 0, s[6:7]
	s_mov_b32 s86, 0
.LBB0_900:
	ds_read_b128 v[2:5], v34
	ds_read_b128 v[6:9], v34 offset:1024
	ds_read_b128 v[10:13], v34 offset:2048
	ds_read_b128 v[14:17], v34 offset:3072
	ds_read_b128 v[178:181], v206
	ds_read_b128 v[182:185], v206 offset:1024
	ds_read_b128 v[196:199], v206 offset:2048
	ds_read_b128 v[200:203], v206 offset:3072
	s_add_u32 s6, s42, 0x200
	s_addc_u32 s7, s43, 0
	s_cmp_eq_u32 s86, 24
	s_cselect_b64 vcc, -1, 0
	s_cselect_b32 s7, s52, s7
	s_cselect_b32 s6, s53, s6
	v_cndmask_b32_e32 v21, v19, v195, vcc
	v_cndmask_b32_e32 v20, v18, v194, vcc
	s_mov_b32 m0, s84
	v_lshl_add_u64 v[30:31], s[42:43], 0, v[190:191]
	ds_read_b128 v[22:25], v189
	ds_read_b128 v[26:29], v189 offset:1024
	ds_read_b128 v[210:213], v189 offset:2048
	ds_read_b128 v[214:217], v189 offset:3072
	ds_read_b128 v[222:225], v189 offset:4096
	ds_read_b128 v[226:229], v189 offset:5120
	ds_read_b128 v[230:233], v189 offset:6144
	ds_read_b128 v[234:237], v189 offset:7168
	global_load_lds_dwordx4 v[30:31], off
	v_lshl_add_u64 v[30:31], s[42:43], 0, v[192:193]
	s_mov_b32 m0, s85
	s_nop 0
	global_load_lds_dwordx4 v[30:31], off
	s_waitcnt vmcnt(8)
	s_waitcnt lgkmcnt(0)
	s_barrier
	s_setprio 0
	s_waitcnt lgkmcnt(0)
	v_mfma_f32_16x16x128_f8f6f4 v[160:163], v[2:9], v[22:29], v[160:163]
	v_mfma_f32_16x16x128_f8f6f4 v[156:159], v[10:17], v[22:29], v[156:159]
	v_mfma_f32_16x16x128_f8f6f4 v[148:151], v[10:17], v[210:217], v[148:151]
	v_mfma_f32_16x16x128_f8f6f4 v[152:155], v[2:9], v[210:217], v[152:155]
	v_mfma_f32_16x16x128_f8f6f4 v[144:147], v[2:9], v[222:229], v[144:147]
	v_mfma_f32_16x16x128_f8f6f4 v[140:143], v[10:17], v[222:229], v[140:143]
	v_mfma_f32_16x16x128_f8f6f4 v[132:135], v[10:17], v[230:237], v[132:135]
	v_mfma_f32_16x16x128_f8f6f4 v[136:139], v[2:9], v[230:237], v[136:139]
	s_setprio 3
	s_setprio 0
	v_mfma_f32_16x16x128_f8f6f4 v[128:131], v[178:185], v[22:29], v[128:131]
	v_mfma_f32_16x16x128_f8f6f4 v[124:127], v[196:203], v[22:29], v[124:127]
	v_mfma_f32_16x16x128_f8f6f4 v[116:119], v[196:203], v[210:217], v[116:119]
	v_mfma_f32_16x16x128_f8f6f4 v[120:123], v[178:185], v[210:217], v[120:123]
	v_mfma_f32_16x16x128_f8f6f4 v[112:115], v[178:185], v[222:229], v[112:115]
	v_mfma_f32_16x16x128_f8f6f4 v[108:111], v[196:203], v[222:229], v[108:111]
	v_mfma_f32_16x16x128_f8f6f4 v[100:103], v[196:203], v[230:237], v[100:103]
	v_mfma_f32_16x16x128_f8f6f4 v[104:107], v[178:185], v[230:237], v[104:107]
	s_setprio 3
	s_barrier
	s_mov_b32 m0, s54
	v_lshl_add_u64 v[22:23], v[20:21], 0, v[172:173]
	ds_read_b128 v[210:213], v189 offset:16384
	ds_read_b128 v[214:217], v189 offset:17408
	ds_read_b128 v[222:225], v189 offset:18432
	ds_read_b128 v[226:229], v189 offset:19456
	ds_read_b128 v[230:233], v189 offset:20480
	ds_read_b128 v[234:237], v189 offset:21504
	ds_read_b128 v[238:241], v189 offset:22528
	ds_read_b128 v[242:245], v189 offset:23552
	global_load_lds_dwordx4 v[22:23], off
	v_lshl_add_u64 v[24:25], v[20:21], 0, v[168:169]
	s_mov_b32 m0, s55
	v_lshl_add_u64 v[26:27], v[20:21], 0, s[2:3]
	global_load_lds_dwordx4 v[24:25], off
	v_lshl_add_u64 v[28:29], v[26:27], 0, v[172:173]
	s_mov_b32 m0, s65
	v_lshl_add_u64 v[26:27], v[26:27], 0, v[168:169]
	global_load_lds_dwordx4 v[28:29], off
	s_mov_b32 m0, s67
	v_lshl_add_u64 v[28:29], s[6:7], 0, v[170:171]
	global_load_lds_dwordx4 v[26:27], off
	v_lshl_add_u64 v[26:27], s[6:7], 0, v[174:175]
	s_mov_b32 m0, s72
	s_nop 0
	global_load_lds_dwordx4 v[26:27], off
	s_mov_b32 m0, s73
	s_nop 0
	global_load_lds_dwordx4 v[28:29], off
	s_waitcnt vmcnt(8)
	s_waitcnt lgkmcnt(0)
	s_barrier
	s_setprio 0
	s_waitcnt lgkmcnt(0)
	v_mfma_f32_16x16x128_f8f6f4 v[96:99], v[2:9], v[210:217], v[96:99]
	v_mfma_f32_16x16x128_f8f6f4 v[92:95], v[10:17], v[210:217], v[92:95]
	v_mfma_f32_16x16x128_f8f6f4 v[84:87], v[10:17], v[222:229], v[84:87]
	v_mfma_f32_16x16x128_f8f6f4 v[88:91], v[2:9], v[222:229], v[88:91]
	v_mfma_f32_16x16x128_f8f6f4 v[80:83], v[2:9], v[230:237], v[80:83]
	v_mfma_f32_16x16x128_f8f6f4 v[76:79], v[10:17], v[230:237], v[76:79]
	v_mfma_f32_16x16x128_f8f6f4 v[68:71], v[10:17], v[238:245], v[68:71]
	v_mfma_f32_16x16x128_f8f6f4 v[72:75], v[2:9], v[238:245], v[72:75]
	s_setprio 3
	s_setprio 0
	v_mfma_f32_16x16x128_f8f6f4 v[64:67], v[178:185], v[210:217], v[64:67]
	v_mfma_f32_16x16x128_f8f6f4 v[60:63], v[196:203], v[210:217], v[60:63]
	v_mfma_f32_16x16x128_f8f6f4 v[52:55], v[196:203], v[222:229], v[52:55]
	v_mfma_f32_16x16x128_f8f6f4 v[56:59], v[178:185], v[222:229], v[56:59]
	v_mfma_f32_16x16x128_f8f6f4 v[48:51], v[178:185], v[230:237], v[48:51]
	v_mfma_f32_16x16x128_f8f6f4 v[44:47], v[196:203], v[230:237], v[44:47]
	v_mfma_f32_16x16x128_f8f6f4 v[36:39], v[196:203], v[238:245], v[36:39]
	v_mfma_f32_16x16x128_f8f6f4 v[40:43], v[178:185], v[238:245], v[40:43]
	s_setprio 3
	s_barrier
	ds_read_b128 v[178:181], v207
	ds_read_b128 v[182:185], v207 offset:1024
	ds_read_b128 v[196:199], v207 offset:2048
	ds_read_b128 v[200:203], v207 offset:3072
	ds_read_b128 v[10:13], v208
	ds_read_b128 v[14:17], v208 offset:1024
	ds_read_b128 v[2:5], v208 offset:2048
	ds_read_b128 v[6:9], v208 offset:3072
	s_add_u32 s6, s6, 0x70000
	s_addc_u32 s7, s7, 0
	s_mov_b32 m0, s74
	v_lshl_add_u64 v[30:31], s[6:7], 0, v[174:175]
	ds_read_b128 v[210:213], v189 offset:32768
	ds_read_b128 v[214:217], v189 offset:33792
	ds_read_b128 v[222:225], v189 offset:34816
	ds_read_b128 v[226:229], v189 offset:35840
	ds_read_b128 v[230:233], v189 offset:36864
	ds_read_b128 v[234:237], v189 offset:37888
	ds_read_b128 v[238:241], v189 offset:38912
	ds_read_b128 v[242:245], v189 offset:39936
	global_load_lds_dwordx4 v[30:31], off
	v_lshl_add_u64 v[30:31], s[6:7], 0, v[170:171]
	s_mov_b32 m0, s75
	s_nop 0
	global_load_lds_dwordx4 v[30:31], off
	s_waitcnt vmcnt(8)
	s_waitcnt lgkmcnt(0)
	s_barrier
	s_setprio 0
	s_waitcnt lgkmcnt(0)
	v_mfma_f32_16x16x128_f8f6f4 v[160:163], v[178:185], v[210:217], v[160:163]
	v_mfma_f32_16x16x128_f8f6f4 v[156:159], v[196:203], v[210:217], v[156:159]
	v_mfma_f32_16x16x128_f8f6f4 v[148:151], v[196:203], v[222:229], v[148:151]
	v_mfma_f32_16x16x128_f8f6f4 v[152:155], v[178:185], v[222:229], v[152:155]
	v_mfma_f32_16x16x128_f8f6f4 v[144:147], v[178:185], v[230:237], v[144:147]
	v_mfma_f32_16x16x128_f8f6f4 v[140:143], v[196:203], v[230:237], v[140:143]
	v_mfma_f32_16x16x128_f8f6f4 v[132:135], v[196:203], v[238:245], v[132:135]
	v_mfma_f32_16x16x128_f8f6f4 v[136:139], v[178:185], v[238:245], v[136:139]
	s_setprio 3
	s_setprio 0
	v_mfma_f32_16x16x128_f8f6f4 v[128:131], v[10:17], v[210:217], v[128:131]
	v_mfma_f32_16x16x128_f8f6f4 v[124:127], v[2:9], v[210:217], v[124:127]
	v_mfma_f32_16x16x128_f8f6f4 v[116:119], v[2:9], v[222:229], v[116:119]
	v_mfma_f32_16x16x128_f8f6f4 v[120:123], v[10:17], v[222:229], v[120:123]
	v_mfma_f32_16x16x128_f8f6f4 v[112:115], v[10:17], v[230:237], v[112:115]
	v_mfma_f32_16x16x128_f8f6f4 v[108:111], v[2:9], v[230:237], v[108:111]
	v_mfma_f32_16x16x128_f8f6f4 v[100:103], v[2:9], v[238:245], v[100:103]
	v_mfma_f32_16x16x128_f8f6f4 v[104:107], v[10:17], v[238:245], v[104:107]
	s_setprio 3
	s_barrier
	s_mov_b32 m0, s50
	v_lshl_add_u64 v[22:23], v[22:23], 0, s[18:19]
	ds_read_b128 v[210:213], v189 offset:49152
	ds_read_b128 v[214:217], v189 offset:50176
	ds_read_b128 v[222:225], v189 offset:51200
	ds_read_b128 v[226:229], v189 offset:52224
	ds_read_b128 v[230:233], v189 offset:53248
	ds_read_b128 v[234:237], v189 offset:54272
	ds_read_b128 v[238:241], v189 offset:55296
	ds_read_b128 v[242:245], v189 offset:56320
	global_load_lds_dwordx4 v[22:23], off
	v_lshl_add_u64 v[22:23], v[24:25], 0, s[18:19]
	s_mov_b32 m0, s51
	v_lshl_add_u64 v[20:21], v[20:21], 0, s[34:35]
	global_load_lds_dwordx4 v[22:23], off
	v_lshl_add_u64 v[22:23], v[20:21], 0, v[172:173]
	s_mov_b32 m0, s63
	v_lshl_add_u64 v[20:21], v[20:21], 0, v[168:169]
	global_load_lds_dwordx4 v[22:23], off
	s_mov_b32 m0, s64
	s_nop 0
	global_load_lds_dwordx4 v[20:21], off
	v_lshl_add_u64 v[20:21], v[26:27], 0, s[18:19]
	s_mov_b32 m0, s77
	s_nop 0
	global_load_lds_dwordx4 v[20:21], off
	v_lshl_add_u64 v[20:21], v[28:29], 0, s[18:19]
	s_mov_b32 m0, s78
	s_nop 0
	global_load_lds_dwordx4 v[20:21], off
	s_waitcnt vmcnt(8)
	s_waitcnt lgkmcnt(0)
	s_barrier
	s_setprio 0
	s_waitcnt lgkmcnt(0)
	v_mfma_f32_16x16x128_f8f6f4 v[96:99], v[178:185], v[210:217], v[96:99]
	v_mfma_f32_16x16x128_f8f6f4 v[92:95], v[196:203], v[210:217], v[92:95]
	v_mfma_f32_16x16x128_f8f6f4 v[84:87], v[196:203], v[222:229], v[84:87]
	v_mfma_f32_16x16x128_f8f6f4 v[88:91], v[178:185], v[222:229], v[88:91]
	v_mfma_f32_16x16x128_f8f6f4 v[80:83], v[178:185], v[230:237], v[80:83]
	v_mfma_f32_16x16x128_f8f6f4 v[76:79], v[196:203], v[230:237], v[76:79]
	v_mfma_f32_16x16x128_f8f6f4 v[68:71], v[196:203], v[238:245], v[68:71]
	v_mfma_f32_16x16x128_f8f6f4 v[72:75], v[178:185], v[238:245], v[72:75]
	s_setprio 3
	s_setprio 0
	v_mfma_f32_16x16x128_f8f6f4 v[64:67], v[10:17], v[210:217], v[64:67]
	v_mfma_f32_16x16x128_f8f6f4 v[60:63], v[2:9], v[210:217], v[60:63]
	v_mfma_f32_16x16x128_f8f6f4 v[52:55], v[2:9], v[222:229], v[52:55]
	v_mfma_f32_16x16x128_f8f6f4 v[56:59], v[10:17], v[222:229], v[56:59]
	v_mfma_f32_16x16x128_f8f6f4 v[48:51], v[10:17], v[230:237], v[48:51]
	v_mfma_f32_16x16x128_f8f6f4 v[44:47], v[2:9], v[230:237], v[44:47]
	v_mfma_f32_16x16x128_f8f6f4 v[36:39], v[2:9], v[238:245], v[36:39]
	v_mfma_f32_16x16x128_f8f6f4 v[40:43], v[10:17], v[238:245], v[40:43]
	s_setprio 3
	s_barrier
	s_add_i32 s86, s86, 2
	s_add_u32 s42, s42, 0x100
	s_addc_u32 s43, s43, 0
	s_cmp_gt_u32 s86, 25
	v_lshl_add_u64 v[18:19], v[18:19], 0, s[28:29]
	s_cbranch_scc0 .LBB0_900
	s_and_b64 vcc, exec, s[36:37]
	s_mov_b64 s[84:85], s[24:25]
	s_cbranch_vccz .LBB0_903
	s_barrier

.LBB0_953:
	s_add_u32 s95, s30, 0x200
	s_addc_u32 s96, s31, 0
	s_add_i32 s65, 0, 0x14000
	s_add_i32 s67, 0, 0x10000
	v_add_u32_e32 v199, s65, v167
	v_add_u32_e32 v200, s67, v167
	ds_read_b128 v[10:13], v199
	ds_read_b128 v[14:17], v199 offset:1024
	ds_read_b128 v[2:5], v199 offset:2048
	ds_read_b128 v[6:9], v199 offset:3072
	ds_read_b128 v[22:25], v200 offset:3072
	ds_read_b128 v[18:21], v200 offset:2048
	ds_read_b128 v[30:33], v200 offset:1024
	ds_read_b128 v[26:29], v200
	s_lshl_b32 s14, s94, 10
	s_add_i32 s97, s14, 0
	s_add_i32 s97, s97, 0x20400
	v_mov_b32_e32 v191, v35
	v_mov_b32_e32 v175, v35
	s_add_i32 s83, s52, 0xc000
	v_readlane_b32 s26, v253, 28
	s_mov_b32 m0, s83
	v_readlane_b32 s27, v253, 29
	s_add_i32 s53, s52, 0xe000
	ds_read_b128 v[178:181], v169
	ds_read_b128 v[182:185], v169 offset:1024
	ds_read_b128 v[202:205], v169 offset:2048
	ds_read_b128 v[206:209], v169 offset:3072
	ds_read_b128 v[210:213], v169 offset:4096
	ds_read_b128 v[214:217], v169 offset:5120
	ds_read_b128 v[222:225], v169 offset:6144
	ds_read_b128 v[226:229], v169 offset:7168
	global_load_lds_dwordx4 v190, s[26:27]
	s_mov_b32 m0, s53
	s_nop 0
	global_load_lds_dwordx4 v174, s[26:27]
	s_waitcnt vmcnt(8)
	s_waitcnt lgkmcnt(0)
	s_barrier
	s_setprio 0
	s_waitcnt lgkmcnt(0)
	v_mfma_f32_16x16x128_f8f6f4 v[160:163], v[26:33], v[178:185], 0
	v_mfma_f32_16x16x128_f8f6f4 v[156:159], v[18:25], v[178:185], 0
	v_mfma_f32_16x16x128_f8f6f4 v[148:151], v[18:25], v[202:209], 0
	v_mfma_f32_16x16x128_f8f6f4 v[152:155], v[26:33], v[202:209], 0
	v_mfma_f32_16x16x128_f8f6f4 v[144:147], v[26:33], v[210:217], 0
	v_mfma_f32_16x16x128_f8f6f4 v[140:143], v[18:25], v[210:217], 0
	v_mfma_f32_16x16x128_f8f6f4 v[132:135], v[18:25], v[222:229], 0
	v_mfma_f32_16x16x128_f8f6f4 v[136:139], v[26:33], v[222:229], 0
	s_setprio 3
	s_setprio 0
	v_mfma_f32_16x16x128_f8f6f4 v[128:131], v[10:17], v[178:185], 0
	v_mfma_f32_16x16x128_f8f6f4 v[124:127], v[2:9], v[178:185], 0
	v_mfma_f32_16x16x128_f8f6f4 v[116:119], v[2:9], v[202:209], 0
	v_mfma_f32_16x16x128_f8f6f4 v[120:123], v[10:17], v[202:209], 0
	v_mfma_f32_16x16x128_f8f6f4 v[112:115], v[10:17], v[210:217], 0
	v_mfma_f32_16x16x128_f8f6f4 v[108:111], v[2:9], v[210:217], 0
	v_mfma_f32_16x16x128_f8f6f4 v[100:103], v[2:9], v[222:229], 0
	v_mfma_f32_16x16x128_f8f6f4 v[104:107], v[10:17], v[222:229], 0
	s_setprio 3
	s_barrier
	v_lshl_add_u64 v[194:195], s[30:31], 0, v[170:171]
	s_add_i32 s67, s67, s82
	v_lshl_add_u64 v[196:197], v[194:195], 0, s[28:29]
	s_mov_b32 m0, s67
	s_add_i32 s55, s67, 0x2000
	ds_read_b128 v[178:181], v169 offset:16384
	ds_read_b128 v[182:185], v169 offset:17408
	ds_read_b128 v[202:205], v169 offset:18432
	ds_read_b128 v[206:209], v169 offset:19456
	ds_read_b128 v[210:213], v169 offset:20480
	ds_read_b128 v[214:217], v169 offset:21504
	ds_read_b128 v[222:225], v169 offset:22528
	ds_read_b128 v[226:229], v169 offset:23552
	global_load_lds_dwordx4 v[196:197], off
	v_lshl_add_u64 v[196:197], s[30:31], 0, v[172:173]
	s_add_u32 s46, s30, 0x20100
	v_lshl_add_u64 v[218:219], v[196:197], 0, s[28:29]
	s_mov_b32 m0, s55
	s_addc_u32 s47, s31, 0
	s_add_i32 s65, s65, s82
	global_load_lds_dwordx4 v[218:219], off
	v_lshl_add_u64 v[218:219], s[46:47], 0, v[170:171]
	s_mov_b32 m0, s65
	s_add_i32 s54, s65, 0x2000
	global_load_lds_dwordx4 v[218:219], off
	v_lshl_add_u64 v[218:219], s[46:47], 0, v[172:173]
	s_mov_b32 m0, s54
	v_readlane_b32 s26, v253, 37
	global_load_lds_dwordx4 v[218:219], off
	s_mov_b32 m0, s52
	v_readlane_b32 s27, v253, 38
	s_nop 4
	global_load_lds_dwordx4 v34, s[26:27]
	s_mov_b32 m0, s84
	s_nop 0
	global_load_lds_dwordx4 v192, s[26:27]
	s_waitcnt vmcnt(8)
	s_waitcnt lgkmcnt(0)
	s_barrier
	s_setprio 0
	s_waitcnt lgkmcnt(0)
	v_mfma_f32_16x16x128_f8f6f4 v[96:99], v[26:33], v[178:185], 0
	v_mfma_f32_16x16x128_f8f6f4 v[92:95], v[18:25], v[178:185], 0
	v_mfma_f32_16x16x128_f8f6f4 v[84:87], v[18:25], v[202:209], 0
	v_mfma_f32_16x16x128_f8f6f4 v[88:91], v[26:33], v[202:209], 0
	v_mfma_f32_16x16x128_f8f6f4 v[80:83], v[26:33], v[210:217], 0
	v_mfma_f32_16x16x128_f8f6f4 v[76:79], v[18:25], v[210:217], 0
	v_mfma_f32_16x16x128_f8f6f4 v[68:71], v[18:25], v[222:229], 0
	v_mfma_f32_16x16x128_f8f6f4 v[72:75], v[26:33], v[222:229], 0
	s_setprio 3
	s_setprio 0
	v_mfma_f32_16x16x128_f8f6f4 v[64:67], v[10:17], v[178:185], 0
	v_mfma_f32_16x16x128_f8f6f4 v[60:63], v[2:9], v[178:185], 0
	v_mfma_f32_16x16x128_f8f6f4 v[52:55], v[2:9], v[202:209], 0
	v_mfma_f32_16x16x128_f8f6f4 v[56:59], v[10:17], v[202:209], 0
	v_mfma_f32_16x16x128_f8f6f4 v[48:51], v[10:17], v[210:217], 0
	v_mfma_f32_16x16x128_f8f6f4 v[44:47], v[2:9], v[210:217], 0
	v_mfma_f32_16x16x128_f8f6f4 v[36:39], v[2:9], v[222:229], 0
	v_mfma_f32_16x16x128_f8f6f4 v[40:43], v[10:17], v[222:229], 0
	s_setprio 3
	s_barrier
	s_add_i32 s50, 0, 0x18000
	s_add_i32 s64, 0, 0x1c000
	v_add_u32_e32 v201, s50, v167
	v_add_u32_e32 v202, s64, v167
	ds_read_b128 v[26:29], v201
	ds_read_b128 v[30:33], v201 offset:1024
	ds_read_b128 v[18:21], v201 offset:2048
	ds_read_b128 v[22:25], v201 offset:3072
	ds_read_b128 v[10:13], v202
	ds_read_b128 v[14:17], v202 offset:1024
	ds_read_b128 v[2:5], v202 offset:2048
	ds_read_b128 v[6:9], v202 offset:3072
	s_mov_b32 m0, s85
	ds_read_b128 v[178:181], v169 offset:32768
	ds_read_b128 v[182:185], v169 offset:33792
	ds_read_b128 v[204:207], v169 offset:34816
	ds_read_b128 v[208:211], v169 offset:35840
	ds_read_b128 v[212:215], v169 offset:36864
	ds_read_b128 v[216:219], v169 offset:37888
	ds_read_b128 v[222:225], v169 offset:38912
	ds_read_b128 v[226:229], v169 offset:39936
	global_load_lds_dwordx4 v189, s[26:27]
	s_mov_b32 m0, s86
	s_nop 0
	global_load_lds_dwordx4 v198, s[26:27]
	s_waitcnt vmcnt(8)
	s_waitcnt lgkmcnt(0)
	s_barrier
	s_setprio 0
	s_waitcnt lgkmcnt(0)
	v_mfma_f32_16x16x128_f8f6f4 v[160:163], v[26:33], v[178:185], v[160:163]
	v_mfma_f32_16x16x128_f8f6f4 v[156:159], v[18:25], v[178:185], v[156:159]
	v_mfma_f32_16x16x128_f8f6f4 v[148:151], v[18:25], v[204:211], v[148:151]
	v_mfma_f32_16x16x128_f8f6f4 v[152:155], v[26:33], v[204:211], v[152:155]
	v_mfma_f32_16x16x128_f8f6f4 v[144:147], v[26:33], v[212:219], v[144:147]
	v_mfma_f32_16x16x128_f8f6f4 v[140:143], v[18:25], v[212:219], v[140:143]
	v_mfma_f32_16x16x128_f8f6f4 v[132:135], v[18:25], v[222:229], v[132:135]
	v_mfma_f32_16x16x128_f8f6f4 v[136:139], v[26:33], v[222:229], v[136:139]
	s_setprio 3
	s_setprio 0
	v_mfma_f32_16x16x128_f8f6f4 v[128:131], v[10:17], v[178:185], v[128:131]
	v_mfma_f32_16x16x128_f8f6f4 v[124:127], v[2:9], v[178:185], v[124:127]
	v_mfma_f32_16x16x128_f8f6f4 v[116:119], v[2:9], v[204:211], v[116:119]
	v_mfma_f32_16x16x128_f8f6f4 v[120:123], v[10:17], v[204:211], v[120:123]
	v_mfma_f32_16x16x128_f8f6f4 v[112:115], v[10:17], v[212:219], v[112:115]
	v_mfma_f32_16x16x128_f8f6f4 v[108:111], v[2:9], v[212:219], v[108:111]
	v_mfma_f32_16x16x128_f8f6f4 v[100:103], v[2:9], v[222:229], v[100:103]
	v_mfma_f32_16x16x128_f8f6f4 v[104:107], v[10:17], v[222:229], v[104:107]
	s_setprio 3
	s_barrier
	s_add_i32 s50, s50, s82
	s_mov_b64 s[26:27], 0x180
	s_add_i32 s51, s50, 0x2000
	v_lshl_add_u64 v[194:195], v[194:195], 0, s[26:27]
	s_mov_b32 m0, s50
	s_add_u32 s30, s30, 0x20180
	ds_read_b128 v[178:181], v169 offset:49152
	ds_read_b128 v[182:185], v169 offset:50176
	ds_read_b128 v[204:207], v169 offset:51200
	ds_read_b128 v[208:211], v169 offset:52224
	ds_read_b128 v[212:215], v169 offset:53248
	ds_read_b128 v[216:219], v169 offset:54272
	ds_read_b128 v[222:225], v169 offset:55296
	ds_read_b128 v[226:229], v169 offset:56320
	global_load_lds_dwordx4 v[194:195], off
	v_lshl_add_u64 v[194:195], v[196:197], 0, s[26:27]
	s_mov_b32 m0, s51
	s_addc_u32 s31, s31, 0
	s_add_i32 s64, s64, s82
	global_load_lds_dwordx4 v[194:195], off
	v_lshl_add_u64 v[194:195], s[30:31], 0, v[170:171]
	s_mov_b32 m0, s64
	s_add_i32 s63, s64, 0x2000
	global_load_lds_dwordx4 v[194:195], off
	v_lshl_add_u64 v[194:195], s[30:31], 0, v[172:173]
	s_mov_b32 m0, s63
	v_readlane_b32 s26, v253, 39
	global_load_lds_dwordx4 v[194:195], off
	s_mov_b32 m0, s90
	v_readlane_b32 s27, v253, 40
	s_nop 4
	global_load_lds_dwordx4 v34, s[26:27]
	s_mov_b32 m0, s91
	s_nop 0
	global_load_lds_dwordx4 v192, s[26:27]
	s_waitcnt vmcnt(8)
	s_waitcnt lgkmcnt(0)
	s_barrier
	s_setprio 0
	s_waitcnt lgkmcnt(0)
	v_mfma_f32_16x16x128_f8f6f4 v[96:99], v[26:33], v[178:185], v[96:99]
	v_mfma_f32_16x16x128_f8f6f4 v[92:95], v[18:25], v[178:185], v[92:95]
	v_mfma_f32_16x16x128_f8f6f4 v[84:87], v[18:25], v[204:211], v[84:87]
	v_mfma_f32_16x16x128_f8f6f4 v[88:91], v[26:33], v[204:211], v[88:91]
	v_mfma_f32_16x16x128_f8f6f4 v[80:83], v[26:33], v[212:219], v[80:83]
	v_mfma_f32_16x16x128_f8f6f4 v[76:79], v[18:25], v[212:219], v[76:79]
	v_mfma_f32_16x16x128_f8f6f4 v[68:71], v[18:25], v[222:229], v[68:71]
	v_mfma_f32_16x16x128_f8f6f4 v[72:75], v[26:33], v[222:229], v[72:75]
	s_setprio 3
	s_setprio 0
	v_mfma_f32_16x16x128_f8f6f4 v[64:67], v[10:17], v[178:185], v[64:67]
	v_mfma_f32_16x16x128_f8f6f4 v[60:63], v[2:9], v[178:185], v[60:63]
	v_mfma_f32_16x16x128_f8f6f4 v[52:55], v[2:9], v[204:211], v[52:55]
	v_mfma_f32_16x16x128_f8f6f4 v[56:59], v[10:17], v[204:211], v[56:59]
	v_mfma_f32_16x16x128_f8f6f4 v[48:51], v[10:17], v[212:219], v[48:51]
	v_mfma_f32_16x16x128_f8f6f4 v[44:47], v[2:9], v[212:219], v[44:47]
	v_mfma_f32_16x16x128_f8f6f4 v[36:39], v[2:9], v[222:229], v[36:39]
	v_mfma_f32_16x16x128_f8f6f4 v[40:43], v[10:17], v[222:229], v[40:43]
	s_setprio 3
	s_barrier
	v_lshl_add_u64 v[18:19], s[26:27], 0, v[174:175]
	v_lshl_add_u64 v[20:21], s[26:27], 0, v[190:191]
	s_mov_b32 s75, 0
	s_mov_b64 s[30:31], 0
	s_branch .LBB0_955
.LBB0_954:
	ds_read_b128 v[178:181], v200
	ds_read_b128 v[182:185], v200 offset:1024
	ds_read_b128 v[204:207], v200 offset:2048
	ds_read_b128 v[208:211], v200 offset:3072
	ds_read_b128 v[10:13], v199
	ds_read_b128 v[14:17], v199 offset:1024
	ds_read_b128 v[2:5], v199 offset:2048
	ds_read_b128 v[6:9], v199 offset:3072
	s_add_u32 s14, s30, 0x200
	s_addc_u32 vcc_lo, s31, 0
	s_and_b64 s[48:49], s[46:47], exec
	s_cselect_b32 s14, 0, s14
	s_cselect_b32 s49, 0, vcc_lo
	s_add_u32 s48, s20, s14
	s_addc_u32 s49, s21, s49
	s_add_u32 s14, s95, s30
	s_addc_u32 vcc_lo, s96, s31
	s_and_b64 s[46:47], s[46:47], exec
	s_cselect_b32 s47, s43, vcc_lo
	s_cselect_b32 s46, s42, s14
	s_mov_b32 m0, s83
	v_lshl_add_u64 v[30:31], v[20:21], 0, s[30:31]
	ds_read_b128 v[22:25], v169
	ds_read_b128 v[26:29], v169 offset:1024
	ds_read_b128 v[212:215], v169 offset:2048
	ds_read_b128 v[216:219], v169 offset:3072
	ds_read_b128 v[222:225], v169 offset:4096
	ds_read_b128 v[226:229], v169 offset:5120
	ds_read_b128 v[230:233], v169 offset:6144
	ds_read_b128 v[234:237], v169 offset:7168
	global_load_lds_dwordx4 v[30:31], off
	v_lshl_add_u64 v[30:31], v[18:19], 0, s[30:31]
	s_mov_b32 m0, s53
	s_nop 0
	global_load_lds_dwordx4 v[30:31], off
	s_waitcnt vmcnt(8)
	s_waitcnt lgkmcnt(0)
	s_barrier
	s_setprio 0
	s_waitcnt lgkmcnt(0)
	v_mfma_f32_16x16x128_f8f6f4 v[160:163], v[178:185], v[22:29], v[160:163]
	v_mfma_f32_16x16x128_f8f6f4 v[156:159], v[204:211], v[22:29], v[156:159]
	v_mfma_f32_16x16x128_f8f6f4 v[148:151], v[204:211], v[212:219], v[148:151]
	v_mfma_f32_16x16x128_f8f6f4 v[152:155], v[178:185], v[212:219], v[152:155]
	v_mfma_f32_16x16x128_f8f6f4 v[144:147], v[178:185], v[222:229], v[144:147]
	v_mfma_f32_16x16x128_f8f6f4 v[140:143], v[204:211], v[222:229], v[140:143]
	v_mfma_f32_16x16x128_f8f6f4 v[132:135], v[204:211], v[230:237], v[132:135]
	v_mfma_f32_16x16x128_f8f6f4 v[136:139], v[178:185], v[230:237], v[136:139]
	s_setprio 3
	s_setprio 0
	v_mfma_f32_16x16x128_f8f6f4 v[128:131], v[10:17], v[22:29], v[128:131]
	v_mfma_f32_16x16x128_f8f6f4 v[124:127], v[2:9], v[22:29], v[124:127]
	v_mfma_f32_16x16x128_f8f6f4 v[116:119], v[2:9], v[212:219], v[116:119]
	v_mfma_f32_16x16x128_f8f6f4 v[120:123], v[10:17], v[212:219], v[120:123]
	v_mfma_f32_16x16x128_f8f6f4 v[112:115], v[10:17], v[222:229], v[112:115]
	v_mfma_f32_16x16x128_f8f6f4 v[108:111], v[2:9], v[222:229], v[108:111]
	v_mfma_f32_16x16x128_f8f6f4 v[100:103], v[2:9], v[230:237], v[100:103]
	v_mfma_f32_16x16x128_f8f6f4 v[104:107], v[10:17], v[230:237], v[104:107]
	s_setprio 3
	s_barrier
	s_mov_b32 m0, s67
	v_lshl_add_u64 v[22:23], s[46:47], 0, v[170:171]
	s_add_u32 vcc_lo, s46, 0x20000
	ds_read_b128 v[212:215], v169 offset:16384
	ds_read_b128 v[216:219], v169 offset:17408
	ds_read_b128 v[222:225], v169 offset:18432
	ds_read_b128 v[226:229], v169 offset:19456
	ds_read_b128 v[230:233], v169 offset:20480
	ds_read_b128 v[234:237], v169 offset:21504
	ds_read_b128 v[238:241], v169 offset:22528
	ds_read_b128 v[242:245], v169 offset:23552
	global_load_lds_dwordx4 v[22:23], off
	v_lshl_add_u64 v[24:25], s[46:47], 0, v[172:173]
	s_mov_b32 m0, s55
	s_addc_u32 vcc_hi, s47, 0
	global_load_lds_dwordx4 v[24:25], off
	v_lshl_add_u64 v[26:27], vcc, 0, v[170:171]
	s_mov_b32 m0, s65
	v_mov_b32_e32 v193, v35
	global_load_lds_dwordx4 v[26:27], off
	v_lshl_add_u64 v[26:27], vcc, 0, v[172:173]
	s_mov_b32 m0, s54
	v_lshl_add_u64 v[28:29], s[48:49], 0, v[34:35]
	global_load_lds_dwordx4 v[26:27], off
	s_mov_b32 m0, s52
	v_lshl_add_u64 v[26:27], s[48:49], 0, v[192:193]
	global_load_lds_dwordx4 v34, s[48:49]
	s_mov_b32 m0, s84
	s_nop 0
	global_load_lds_dwordx4 v192, s[48:49]
	s_waitcnt vmcnt(8)
	s_waitcnt lgkmcnt(0)
	s_barrier
	s_setprio 0
	s_waitcnt lgkmcnt(0)
	v_mfma_f32_16x16x128_f8f6f4 v[96:99], v[178:185], v[212:219], v[96:99]
	v_mfma_f32_16x16x128_f8f6f4 v[92:95], v[204:211], v[212:219], v[92:95]
	v_mfma_f32_16x16x128_f8f6f4 v[84:87], v[204:211], v[222:229], v[84:87]
	v_mfma_f32_16x16x128_f8f6f4 v[88:91], v[178:185], v[222:229], v[88:91]
	v_mfma_f32_16x16x128_f8f6f4 v[80:83], v[178:185], v[230:237], v[80:83]
	v_mfma_f32_16x16x128_f8f6f4 v[76:79], v[204:211], v[230:237], v[76:79]
	v_mfma_f32_16x16x128_f8f6f4 v[68:71], v[204:211], v[238:245], v[68:71]
	v_mfma_f32_16x16x128_f8f6f4 v[72:75], v[178:185], v[238:245], v[72:75]
	s_setprio 3
	s_setprio 0
	v_mfma_f32_16x16x128_f8f6f4 v[64:67], v[10:17], v[212:219], v[64:67]
	v_mfma_f32_16x16x128_f8f6f4 v[60:63], v[2:9], v[212:219], v[60:63]
	v_mfma_f32_16x16x128_f8f6f4 v[52:55], v[2:9], v[222:229], v[52:55]
	v_mfma_f32_16x16x128_f8f6f4 v[56:59], v[10:17], v[222:229], v[56:59]
	v_mfma_f32_16x16x128_f8f6f4 v[48:51], v[10:17], v[230:237], v[48:51]
	v_mfma_f32_16x16x128_f8f6f4 v[44:47], v[2:9], v[230:237], v[44:47]
	v_mfma_f32_16x16x128_f8f6f4 v[36:39], v[2:9], v[238:245], v[36:39]
	v_mfma_f32_16x16x128_f8f6f4 v[40:43], v[10:17], v[238:245], v[40:43]
	s_setprio 3
	s_barrier
	ds_read_b128 v[178:181], v201
	ds_read_b128 v[182:185], v201 offset:1024
	ds_read_b128 v[204:207], v201 offset:2048
	ds_read_b128 v[208:211], v201 offset:3072
	ds_read_b128 v[10:13], v202
	ds_read_b128 v[14:17], v202 offset:1024
	ds_read_b128 v[2:5], v202 offset:2048
	ds_read_b128 v[6:9], v202 offset:3072
	s_mov_b32 m0, s85
	ds_read_b128 v[212:215], v169 offset:32768
	ds_read_b128 v[216:219], v169 offset:33792
	ds_read_b128 v[222:225], v169 offset:34816
	ds_read_b128 v[226:229], v169 offset:35840
	ds_read_b128 v[230:233], v169 offset:36864
	ds_read_b128 v[234:237], v169 offset:37888
	ds_read_b128 v[238:241], v169 offset:38912
	ds_read_b128 v[242:245], v169 offset:39936
	global_load_lds_dwordx4 v189, s[48:49]
	s_mov_b32 m0, s86
	s_nop 0
	global_load_lds_dwordx4 v198, s[48:49]
	s_waitcnt vmcnt(8)
	s_waitcnt lgkmcnt(0)
	s_barrier
	s_setprio 0
	s_waitcnt lgkmcnt(0)
	v_mfma_f32_16x16x128_f8f6f4 v[160:163], v[178:185], v[212:219], v[160:163]
	v_mfma_f32_16x16x128_f8f6f4 v[156:159], v[204:211], v[212:219], v[156:159]
	v_mfma_f32_16x16x128_f8f6f4 v[148:151], v[204:211], v[222:229], v[148:151]
	v_mfma_f32_16x16x128_f8f6f4 v[152:155], v[178:185], v[222:229], v[152:155]
	v_mfma_f32_16x16x128_f8f6f4 v[144:147], v[178:185], v[230:237], v[144:147]
	v_mfma_f32_16x16x128_f8f6f4 v[140:143], v[204:211], v[230:237], v[140:143]
	v_mfma_f32_16x16x128_f8f6f4 v[132:135], v[204:211], v[238:245], v[132:135]
	v_mfma_f32_16x16x128_f8f6f4 v[136:139], v[178:185], v[238:245], v[136:139]
	s_setprio 3
	s_setprio 0
	v_mfma_f32_16x16x128_f8f6f4 v[128:131], v[10:17], v[212:219], v[128:131]
	v_mfma_f32_16x16x128_f8f6f4 v[124:127], v[2:9], v[212:219], v[124:127]
	v_mfma_f32_16x16x128_f8f6f4 v[116:119], v[2:9], v[222:229], v[116:119]
	v_mfma_f32_16x16x128_f8f6f4 v[120:123], v[10:17], v[222:229], v[120:123]
	v_mfma_f32_16x16x128_f8f6f4 v[112:115], v[10:17], v[230:237], v[112:115]
	v_mfma_f32_16x16x128_f8f6f4 v[108:111], v[2:9], v[230:237], v[108:111]
	v_mfma_f32_16x16x128_f8f6f4 v[100:103], v[2:9], v[238:245], v[100:103]
	v_mfma_f32_16x16x128_f8f6f4 v[104:107], v[10:17], v[238:245], v[104:107]
	s_setprio 3
	s_barrier
	s_mov_b32 m0, s50
	v_lshl_add_u64 v[22:23], v[22:23], 0, s[18:19]
	s_add_u32 s46, s46, 0x20080
	ds_read_b128 v[212:215], v169 offset:49152
	ds_read_b128 v[216:219], v169 offset:50176
	ds_read_b128 v[222:225], v169 offset:51200
	ds_read_b128 v[226:229], v169 offset:52224
	ds_read_b128 v[230:233], v169 offset:53248
	ds_read_b128 v[234:237], v169 offset:54272
	ds_read_b128 v[238:241], v169 offset:55296
	ds_read_b128 v[242:245], v169 offset:56320
	global_load_lds_dwordx4 v[22:23], off
	v_lshl_add_u64 v[22:23], v[24:25], 0, s[18:19]
	s_mov_b32 m0, s51
	s_addc_u32 s47, s47, 0
	global_load_lds_dwordx4 v[22:23], off
	v_lshl_add_u64 v[22:23], s[46:47], 0, v[170:171]
	s_mov_b32 m0, s64
	s_nop 0
	global_load_lds_dwordx4 v[22:23], off
	v_lshl_add_u64 v[22:23], s[46:47], 0, v[172:173]
	s_mov_b32 m0, s63
	s_nop 0
	global_load_lds_dwordx4 v[22:23], off
	v_lshl_add_u64 v[22:23], v[28:29], 0, s[18:19]
	s_mov_b32 m0, s90
	s_nop 0
	global_load_lds_dwordx4 v[22:23], off
	v_lshl_add_u64 v[22:23], v[26:27], 0, s[18:19]
	s_mov_b32 m0, s91
	s_nop 0
	global_load_lds_dwordx4 v[22:23], off
	s_waitcnt vmcnt(8)
	s_waitcnt lgkmcnt(0)
	s_barrier
	s_setprio 0
	s_waitcnt lgkmcnt(0)
	v_mfma_f32_16x16x128_f8f6f4 v[96:99], v[178:185], v[212:219], v[96:99]
	v_mfma_f32_16x16x128_f8f6f4 v[92:95], v[204:211], v[212:219], v[92:95]
	v_mfma_f32_16x16x128_f8f6f4 v[84:87], v[204:211], v[222:229], v[84:87]
	v_mfma_f32_16x16x128_f8f6f4 v[88:91], v[178:185], v[222:229], v[88:91]
	v_mfma_f32_16x16x128_f8f6f4 v[80:83], v[178:185], v[230:237], v[80:83]
	v_mfma_f32_16x16x128_f8f6f4 v[76:79], v[204:211], v[230:237], v[76:79]
	v_mfma_f32_16x16x128_f8f6f4 v[68:71], v[204:211], v[238:245], v[68:71]
	v_mfma_f32_16x16x128_f8f6f4 v[72:75], v[178:185], v[238:245], v[72:75]
	s_setprio 3
	s_setprio 0
	v_mfma_f32_16x16x128_f8f6f4 v[64:67], v[10:17], v[212:219], v[64:67]
	v_mfma_f32_16x16x128_f8f6f4 v[60:63], v[2:9], v[212:219], v[60:63]
	v_mfma_f32_16x16x128_f8f6f4 v[52:55], v[2:9], v[222:229], v[52:55]
	v_mfma_f32_16x16x128_f8f6f4 v[56:59], v[10:17], v[222:229], v[56:59]
	v_mfma_f32_16x16x128_f8f6f4 v[48:51], v[10:17], v[230:237], v[48:51]
	v_mfma_f32_16x16x128_f8f6f4 v[44:47], v[2:9], v[230:237], v[44:47]
	v_mfma_f32_16x16x128_f8f6f4 v[36:39], v[2:9], v[238:245], v[36:39]
	v_mfma_f32_16x16x128_f8f6f4 v[40:43], v[10:17], v[238:245], v[40:43]
	s_setprio 3
	s_barrier
	s_add_i32 s75, s75, 2
	s_add_u32 s30, s30, 0x100
	s_addc_u32 s31, s31, 0
	s_cmp_gt_u32 s75, 5
	s_cbranch_scc1 .LBB0_957

.LBB0_1086:
	s_lshl_b32 s10, s51, 18
	s_add_u32 s10, s20, s10
	s_addc_u32 s11, s21, 0
	s_and_b64 s[16:17], s[4:5], exec
	s_cselect_b32 s54, s11, s31
	s_cselect_b32 s55, s10, s30
	s_lshl_b32 s14, s50, 18
	s_add_u32 s16, s15, s14
	s_addc_u32 s17, s26, 0
	s_and_b64 s[36:37], s[4:5], exec
	s_cselect_b32 s56, s17, s23
	s_cselect_b32 s57, s16, s22
	s_add_i32 s60, 0, 0x10000
	s_add_i32 s62, 0, 0x14000
	v_add_u32_e32 v198, s60, v196
	v_add_u32_e32 v199, s62, v196
	ds_read_b128 v[26:29], v198
	ds_read_b128 v[30:33], v198 offset:1024
	ds_read_b128 v[18:21], v198 offset:2048
	ds_read_b128 v[22:25], v198 offset:3072
	ds_read_b128 v[10:13], v199
	ds_read_b128 v[14:17], v199 offset:1024
	ds_read_b128 v[2:5], v199 offset:2048
	ds_read_b128 v[6:9], v199 offset:3072
	s_add_u32 s36, s30, 0x20080
	s_addc_u32 s37, s31, 0
	s_add_i32 s58, s41, 0xc000
	v_lshl_add_u64 v[174:175], s[36:37], 0, v[168:169]
	s_mov_b32 m0, s58
	s_add_i32 s59, s41, 0xe000
	ds_read_b128 v[200:203], v197
	ds_read_b128 v[204:207], v197 offset:1024
	ds_read_b128 v[222:225], v197 offset:2048
	ds_read_b128 v[226:229], v197 offset:3072
	ds_read_b128 v[230:233], v197 offset:4096
	ds_read_b128 v[234:237], v197 offset:5120
	ds_read_b128 v[238:241], v197 offset:6144
	ds_read_b128 v[242:245], v197 offset:7168
	global_load_lds_dwordx4 v[174:175], off
	v_lshl_add_u64 v[174:175], s[36:37], 0, v[166:167]
	s_mov_b32 m0, s59
	s_nop 0
	global_load_lds_dwordx4 v[174:175], off
	s_waitcnt vmcnt(8)
	s_waitcnt lgkmcnt(0)
	s_barrier
	s_setprio 0
	s_waitcnt lgkmcnt(0)
	v_mfma_f32_16x16x128_f8f6f4 v[160:163], v[26:33], v[200:207], 0
	v_mfma_f32_16x16x128_f8f6f4 v[156:159], v[18:25], v[200:207], 0
	v_mfma_f32_16x16x128_f8f6f4 v[148:151], v[18:25], v[222:229], 0
	v_mfma_f32_16x16x128_f8f6f4 v[152:155], v[26:33], v[222:229], 0
	v_mfma_f32_16x16x128_f8f6f4 v[144:147], v[26:33], v[230:237], 0
	v_mfma_f32_16x16x128_f8f6f4 v[140:143], v[18:25], v[230:237], 0
	v_mfma_f32_16x16x128_f8f6f4 v[132:135], v[18:25], v[238:245], 0
	v_mfma_f32_16x16x128_f8f6f4 v[136:139], v[26:33], v[238:245], 0
	s_setprio 3
	s_setprio 0
	v_mfma_f32_16x16x128_f8f6f4 v[128:131], v[10:17], v[200:207], 0
	v_mfma_f32_16x16x128_f8f6f4 v[124:127], v[2:9], v[200:207], 0
	v_mfma_f32_16x16x128_f8f6f4 v[116:119], v[2:9], v[222:229], 0
	v_mfma_f32_16x16x128_f8f6f4 v[120:123], v[10:17], v[222:229], 0
	v_mfma_f32_16x16x128_f8f6f4 v[112:115], v[10:17], v[230:237], 0
	v_mfma_f32_16x16x128_f8f6f4 v[108:111], v[2:9], v[230:237], 0
	v_mfma_f32_16x16x128_f8f6f4 v[100:103], v[2:9], v[238:245], 0
	v_mfma_f32_16x16x128_f8f6f4 v[104:107], v[10:17], v[238:245], 0
	s_setprio 3
	s_barrier
	s_add_i32 s60, s60, s40
	v_lshl_add_u64 v[174:175], s[22:23], 0, v[34:35]
	s_add_i32 s61, s60, 0x2000
	v_lshl_add_u64 v[178:179], v[174:175], 0, s[28:29]
	s_mov_b32 m0, s60
	v_lshl_add_u64 v[190:191], s[22:23], 0, v[164:165]
	s_add_u32 s36, s22, 0x20100
	ds_read_b128 v[200:203], v197 offset:16384
	ds_read_b128 v[204:207], v197 offset:17408
	ds_read_b128 v[222:225], v197 offset:18432
	ds_read_b128 v[226:229], v197 offset:19456
	ds_read_b128 v[230:233], v197 offset:20480
	ds_read_b128 v[234:237], v197 offset:21504
	ds_read_b128 v[238:241], v197 offset:22528
	ds_read_b128 v[242:245], v197 offset:23552
	global_load_lds_dwordx4 v[178:179], off
	v_lshl_add_u64 v[178:179], v[190:191], 0, s[28:29]
	s_mov_b32 m0, s61
	s_addc_u32 s37, s23, 0
	s_add_i32 s62, s62, s40
	global_load_lds_dwordx4 v[178:179], off
	v_lshl_add_u64 v[178:179], s[36:37], 0, v[34:35]
	s_mov_b32 m0, s62
	s_add_i32 s63, s62, 0x2000
	global_load_lds_dwordx4 v[178:179], off
	v_lshl_add_u64 v[178:179], s[36:37], 0, v[164:165]
	s_mov_b32 m0, s63
	v_lshl_add_u64 v[192:193], s[30:31], 0, v[168:169]
	global_load_lds_dwordx4 v[178:179], off
	v_lshl_add_u64 v[178:179], v[192:193], 0, s[28:29]
	s_mov_b32 m0, s41
	v_lshl_add_u64 v[194:195], s[30:31], 0, v[166:167]
	global_load_lds_dwordx4 v[178:179], off
	v_lshl_add_u64 v[178:179], v[194:195], 0, s[28:29]
	s_mov_b32 m0, s42
	s_nop 0
	global_load_lds_dwordx4 v[178:179], off
	s_waitcnt vmcnt(8)
	s_waitcnt lgkmcnt(0)
	s_barrier
	s_setprio 0
	s_waitcnt lgkmcnt(0)
	v_mfma_f32_16x16x128_f8f6f4 v[96:99], v[26:33], v[200:207], 0
	v_mfma_f32_16x16x128_f8f6f4 v[92:95], v[18:25], v[200:207], 0
	v_mfma_f32_16x16x128_f8f6f4 v[84:87], v[18:25], v[222:229], 0
	v_mfma_f32_16x16x128_f8f6f4 v[88:91], v[26:33], v[222:229], 0
	v_mfma_f32_16x16x128_f8f6f4 v[80:83], v[26:33], v[230:237], 0
	v_mfma_f32_16x16x128_f8f6f4 v[76:79], v[18:25], v[230:237], 0
	v_mfma_f32_16x16x128_f8f6f4 v[68:71], v[18:25], v[238:245], 0
	v_mfma_f32_16x16x128_f8f6f4 v[72:75], v[26:33], v[238:245], 0
	s_setprio 3
	s_setprio 0
	v_mfma_f32_16x16x128_f8f6f4 v[64:67], v[10:17], v[200:207], 0
	v_mfma_f32_16x16x128_f8f6f4 v[60:63], v[2:9], v[200:207], 0
	v_mfma_f32_16x16x128_f8f6f4 v[52:55], v[2:9], v[222:229], 0
	v_mfma_f32_16x16x128_f8f6f4 v[56:59], v[10:17], v[222:229], 0
	v_mfma_f32_16x16x128_f8f6f4 v[48:51], v[10:17], v[230:237], 0
	v_mfma_f32_16x16x128_f8f6f4 v[44:47], v[2:9], v[230:237], 0
	v_mfma_f32_16x16x128_f8f6f4 v[36:39], v[2:9], v[238:245], 0
	v_mfma_f32_16x16x128_f8f6f4 v[40:43], v[10:17], v[238:245], 0
	s_setprio 3
	s_barrier
	s_add_i32 s64, 0, 0x18000
	s_add_i32 s66, 0, 0x1c000
	v_add_u32_e32 v200, s64, v196
	v_add_u32_e32 v201, s66, v196
	ds_read_b128 v[26:29], v200
	ds_read_b128 v[30:33], v200 offset:1024
	ds_read_b128 v[18:21], v200 offset:2048
	ds_read_b128 v[22:25], v200 offset:3072
	ds_read_b128 v[10:13], v201
	ds_read_b128 v[14:17], v201 offset:1024
	ds_read_b128 v[2:5], v201 offset:2048
	ds_read_b128 v[6:9], v201 offset:3072
	s_add_u32 s36, s30, 0x20100
	s_addc_u32 s37, s31, 0
	s_mov_b32 m0, s43
	v_lshl_add_u64 v[178:179], s[36:37], 0, v[168:169]
	ds_read_b128 v[202:205], v197 offset:32768
	ds_read_b128 v[206:209], v197 offset:33792
	ds_read_b128 v[222:225], v197 offset:34816
	ds_read_b128 v[226:229], v197 offset:35840
	ds_read_b128 v[230:233], v197 offset:36864
	ds_read_b128 v[234:237], v197 offset:37888
	ds_read_b128 v[238:241], v197 offset:38912
	ds_read_b128 v[242:245], v197 offset:39936
	global_load_lds_dwordx4 v[178:179], off
	v_lshl_add_u64 v[178:179], s[36:37], 0, v[166:167]
	s_mov_b32 m0, s44
	s_nop 0
	global_load_lds_dwordx4 v[178:179], off
	s_waitcnt vmcnt(8)
	s_waitcnt lgkmcnt(0)
	s_barrier
	s_setprio 0
	s_waitcnt lgkmcnt(0)
	v_mfma_f32_16x16x128_f8f6f4 v[160:163], v[26:33], v[202:209], v[160:163]
	v_mfma_f32_16x16x128_f8f6f4 v[156:159], v[18:25], v[202:209], v[156:159]
	v_mfma_f32_16x16x128_f8f6f4 v[148:151], v[18:25], v[222:229], v[148:151]
	v_mfma_f32_16x16x128_f8f6f4 v[152:155], v[26:33], v[222:229], v[152:155]
	v_mfma_f32_16x16x128_f8f6f4 v[144:147], v[26:33], v[230:237], v[144:147]
	v_mfma_f32_16x16x128_f8f6f4 v[140:143], v[18:25], v[230:237], v[140:143]
	v_mfma_f32_16x16x128_f8f6f4 v[132:135], v[18:25], v[238:245], v[132:135]
	v_mfma_f32_16x16x128_f8f6f4 v[136:139], v[26:33], v[238:245], v[136:139]
	s_setprio 3
	s_setprio 0
	v_mfma_f32_16x16x128_f8f6f4 v[128:131], v[10:17], v[202:209], v[128:131]
	v_mfma_f32_16x16x128_f8f6f4 v[124:127], v[2:9], v[202:209], v[124:127]
	v_mfma_f32_16x16x128_f8f6f4 v[116:119], v[2:9], v[222:229], v[116:119]
	v_mfma_f32_16x16x128_f8f6f4 v[120:123], v[10:17], v[222:229], v[120:123]
	v_mfma_f32_16x16x128_f8f6f4 v[112:115], v[10:17], v[230:237], v[112:115]
	v_mfma_f32_16x16x128_f8f6f4 v[108:111], v[2:9], v[230:237], v[108:111]
	v_mfma_f32_16x16x128_f8f6f4 v[100:103], v[2:9], v[238:245], v[100:103]
	v_mfma_f32_16x16x128_f8f6f4 v[104:107], v[10:17], v[238:245], v[104:107]
	s_setprio 3
	s_barrier
	s_add_i32 s64, s64, s40
	s_mov_b64 s[24:25], 0x180
	s_add_i32 s65, s64, 0x2000
	v_lshl_add_u64 v[174:175], v[174:175], 0, s[24:25]
	s_mov_b32 m0, s64
	s_add_u32 s36, s22, 0x20180
	ds_read_b128 v[202:205], v197 offset:49152
	ds_read_b128 v[206:209], v197 offset:50176
	ds_read_b128 v[222:225], v197 offset:51200
	ds_read_b128 v[226:229], v197 offset:52224
	ds_read_b128 v[230:233], v197 offset:53248
	ds_read_b128 v[234:237], v197 offset:54272
	ds_read_b128 v[238:241], v197 offset:55296
	ds_read_b128 v[242:245], v197 offset:56320
	global_load_lds_dwordx4 v[174:175], off
	v_lshl_add_u64 v[174:175], v[190:191], 0, s[24:25]
	s_mov_b32 m0, s65
	s_addc_u32 s37, s23, 0
	s_add_i32 s66, s66, s40
	global_load_lds_dwordx4 v[174:175], off
	v_lshl_add_u64 v[174:175], s[36:37], 0, v[34:35]
	s_mov_b32 m0, s66
	s_add_i32 s67, s66, 0x2000
	global_load_lds_dwordx4 v[174:175], off
	v_lshl_add_u64 v[174:175], s[36:37], 0, v[164:165]
	s_mov_b32 m0, s67
	s_nop 0
	global_load_lds_dwordx4 v[174:175], off
	v_lshl_add_u64 v[174:175], v[192:193], 0, s[24:25]
	s_mov_b32 m0, s47
	s_nop 0
	global_load_lds_dwordx4 v[174:175], off
	v_lshl_add_u64 v[174:175], v[194:195], 0, s[24:25]
	s_mov_b32 m0, s48
	s_nop 0
	global_load_lds_dwordx4 v[174:175], off
	s_waitcnt vmcnt(8)
	s_waitcnt lgkmcnt(0)
	s_barrier
	s_setprio 0
	s_waitcnt lgkmcnt(0)
	v_mfma_f32_16x16x128_f8f6f4 v[96:99], v[26:33], v[202:209], v[96:99]
	v_mfma_f32_16x16x128_f8f6f4 v[92:95], v[18:25], v[202:209], v[92:95]
	v_mfma_f32_16x16x128_f8f6f4 v[84:87], v[18:25], v[222:229], v[84:87]
	v_mfma_f32_16x16x128_f8f6f4 v[88:91], v[26:33], v[222:229], v[88:91]
	v_mfma_f32_16x16x128_f8f6f4 v[80:83], v[26:33], v[230:237], v[80:83]
	v_mfma_f32_16x16x128_f8f6f4 v[76:79], v[18:25], v[230:237], v[76:79]
	v_mfma_f32_16x16x128_f8f6f4 v[68:71], v[18:25], v[238:245], v[68:71]
	v_mfma_f32_16x16x128_f8f6f4 v[72:75], v[26:33], v[238:245], v[72:75]
	s_setprio 3
	s_setprio 0
	v_mfma_f32_16x16x128_f8f6f4 v[64:67], v[10:17], v[202:209], v[64:67]
	v_mfma_f32_16x16x128_f8f6f4 v[60:63], v[2:9], v[202:209], v[60:63]
	v_mfma_f32_16x16x128_f8f6f4 v[52:55], v[2:9], v[222:229], v[52:55]
	v_mfma_f32_16x16x128_f8f6f4 v[56:59], v[10:17], v[222:229], v[56:59]
	v_mfma_f32_16x16x128_f8f6f4 v[48:51], v[10:17], v[230:237], v[48:51]
	v_mfma_f32_16x16x128_f8f6f4 v[44:47], v[2:9], v[230:237], v[44:47]
	v_mfma_f32_16x16x128_f8f6f4 v[36:39], v[2:9], v[238:245], v[36:39]
	v_mfma_f32_16x16x128_f8f6f4 v[40:43], v[10:17], v[238:245], v[40:43]
	s_setprio 3
	s_barrier
	s_add_u32 s30, s30, 0x20180
	s_addc_u32 s31, s31, 0
	s_add_u32 s68, s22, 0x200
	s_addc_u32 s69, s23, 0
	s_mov_b32 s70, 0
.LBB0_1087:
	ds_read_b128 v[2:5], v198
	ds_read_b128 v[6:9], v198 offset:1024
	ds_read_b128 v[10:13], v198 offset:2048
	ds_read_b128 v[14:17], v198 offset:3072
	ds_read_b128 v[18:21], v199
	ds_read_b128 v[22:25], v199 offset:1024
	ds_read_b128 v[26:29], v199 offset:2048
	ds_read_b128 v[30:33], v199 offset:3072
	s_add_u32 s14, s30, 0xfffe0080
	s_addc_u32 s22, s31, -1
	s_cmp_eq_u32 s70, 4
	s_cselect_b32 s37, s54, s22
	s_cselect_b32 s36, s55, s14
	s_cselect_b32 s23, s56, s69
	s_cselect_b32 s22, s57, s68
	s_mov_b32 m0, s58
	v_lshl_add_u64 v[174:175], s[30:31], 0, v[170:171]
	ds_read_b128 v[202:205], v197
	ds_read_b128 v[206:209], v197 offset:1024
	ds_read_b128 v[222:225], v197 offset:2048
	ds_read_b128 v[226:229], v197 offset:3072
	ds_read_b128 v[230:233], v197 offset:4096
	ds_read_b128 v[234:237], v197 offset:5120
	ds_read_b128 v[238:241], v197 offset:6144
	ds_read_b128 v[242:245], v197 offset:7168
	global_load_lds_dwordx4 v[174:175], off
	v_lshl_add_u64 v[174:175], s[30:31], 0, v[172:173]
	s_mov_b32 m0, s59
	s_nop 0
	global_load_lds_dwordx4 v[174:175], off
	s_waitcnt vmcnt(8)
	s_waitcnt lgkmcnt(0)
	s_barrier
	s_setprio 0
	s_waitcnt lgkmcnt(0)
	v_mfma_f32_16x16x128_f8f6f4 v[160:163], v[2:9], v[202:209], v[160:163]
	v_mfma_f32_16x16x128_f8f6f4 v[156:159], v[10:17], v[202:209], v[156:159]
	v_mfma_f32_16x16x128_f8f6f4 v[148:151], v[10:17], v[222:229], v[148:151]
	v_mfma_f32_16x16x128_f8f6f4 v[152:155], v[2:9], v[222:229], v[152:155]
	v_mfma_f32_16x16x128_f8f6f4 v[144:147], v[2:9], v[230:237], v[144:147]
	v_mfma_f32_16x16x128_f8f6f4 v[140:143], v[10:17], v[230:237], v[140:143]
	v_mfma_f32_16x16x128_f8f6f4 v[132:135], v[10:17], v[238:245], v[132:135]
	v_mfma_f32_16x16x128_f8f6f4 v[136:139], v[2:9], v[238:245], v[136:139]
	s_setprio 3
	s_setprio 0
	v_mfma_f32_16x16x128_f8f6f4 v[128:131], v[18:25], v[202:209], v[128:131]
	v_mfma_f32_16x16x128_f8f6f4 v[124:127], v[26:33], v[202:209], v[124:127]
	v_mfma_f32_16x16x128_f8f6f4 v[116:119], v[26:33], v[222:229], v[116:119]
	v_mfma_f32_16x16x128_f8f6f4 v[120:123], v[18:25], v[222:229], v[120:123]
	v_mfma_f32_16x16x128_f8f6f4 v[112:115], v[18:25], v[230:237], v[112:115]
	v_mfma_f32_16x16x128_f8f6f4 v[108:111], v[26:33], v[230:237], v[108:111]
	v_mfma_f32_16x16x128_f8f6f4 v[100:103], v[26:33], v[238:245], v[100:103]
	v_mfma_f32_16x16x128_f8f6f4 v[104:107], v[18:25], v[238:245], v[104:107]
	s_setprio 3
	s_barrier
	s_mov_b32 m0, s60
	v_lshl_add_u64 v[174:175], s[22:23], 0, v[34:35]
	s_add_u32 s72, s22, 0x20000
	ds_read_b128 v[202:205], v197 offset:16384
	ds_read_b128 v[206:209], v197 offset:17408
	ds_read_b128 v[222:225], v197 offset:18432
	ds_read_b128 v[226:229], v197 offset:19456
	ds_read_b128 v[230:233], v197 offset:20480
	ds_read_b128 v[234:237], v197 offset:21504
	ds_read_b128 v[238:241], v197 offset:22528
	ds_read_b128 v[242:245], v197 offset:23552
	global_load_lds_dwordx4 v[174:175], off
	v_lshl_add_u64 v[190:191], s[22:23], 0, v[164:165]
	s_mov_b32 m0, s61
	s_addc_u32 s73, s23, 0
	global_load_lds_dwordx4 v[190:191], off
	v_lshl_add_u64 v[178:179], s[72:73], 0, v[34:35]
	s_mov_b32 m0, s62
	v_lshl_add_u64 v[192:193], s[36:37], 0, v[168:169]
	global_load_lds_dwordx4 v[178:179], off
	v_lshl_add_u64 v[178:179], s[72:73], 0, v[164:165]
	s_mov_b32 m0, s63
	v_lshl_add_u64 v[194:195], s[36:37], 0, v[166:167]
	global_load_lds_dwordx4 v[178:179], off
	s_mov_b32 m0, s41
	s_nop 0
	global_load_lds_dwordx4 v[192:193], off
	s_mov_b32 m0, s42
	s_nop 0
	global_load_lds_dwordx4 v[194:195], off
	s_waitcnt vmcnt(8)
	s_waitcnt lgkmcnt(0)
	s_barrier
	s_setprio 0
	s_waitcnt lgkmcnt(0)
	v_mfma_f32_16x16x128_f8f6f4 v[96:99], v[2:9], v[202:209], v[96:99]
	v_mfma_f32_16x16x128_f8f6f4 v[92:95], v[10:17], v[202:209], v[92:95]
	v_mfma_f32_16x16x128_f8f6f4 v[84:87], v[10:17], v[222:229], v[84:87]
	v_mfma_f32_16x16x128_f8f6f4 v[88:91], v[2:9], v[222:229], v[88:91]
	v_mfma_f32_16x16x128_f8f6f4 v[80:83], v[2:9], v[230:237], v[80:83]
	v_mfma_f32_16x16x128_f8f6f4 v[76:79], v[10:17], v[230:237], v[76:79]
	v_mfma_f32_16x16x128_f8f6f4 v[68:71], v[10:17], v[238:245], v[68:71]
	v_mfma_f32_16x16x128_f8f6f4 v[72:75], v[2:9], v[238:245], v[72:75]
	s_setprio 3
	s_setprio 0
	v_mfma_f32_16x16x128_f8f6f4 v[64:67], v[18:25], v[202:209], v[64:67]
	v_mfma_f32_16x16x128_f8f6f4 v[60:63], v[26:33], v[202:209], v[60:63]
	v_mfma_f32_16x16x128_f8f6f4 v[52:55], v[26:33], v[222:229], v[52:55]
	v_mfma_f32_16x16x128_f8f6f4 v[56:59], v[18:25], v[222:229], v[56:59]
	v_mfma_f32_16x16x128_f8f6f4 v[48:51], v[18:25], v[230:237], v[48:51]
	v_mfma_f32_16x16x128_f8f6f4 v[44:47], v[26:33], v[230:237], v[44:47]
	v_mfma_f32_16x16x128_f8f6f4 v[36:39], v[26:33], v[238:245], v[36:39]
	v_mfma_f32_16x16x128_f8f6f4 v[40:43], v[18:25], v[238:245], v[40:43]
	s_setprio 3
	s_barrier
	ds_read_b128 v[26:29], v200
	ds_read_b128 v[30:33], v200 offset:1024
	ds_read_b128 v[18:21], v200 offset:2048
	ds_read_b128 v[22:25], v200 offset:3072
	ds_read_b128 v[10:13], v201
	ds_read_b128 v[14:17], v201 offset:1024
	ds_read_b128 v[2:5], v201 offset:2048
	ds_read_b128 v[6:9], v201 offset:3072
	s_add_u32 s36, s36, 0x20000
	s_addc_u32 s37, s37, 0
	s_mov_b32 m0, s43
	v_lshl_add_u64 v[178:179], s[36:37], 0, v[168:169]
	ds_read_b128 v[202:205], v197 offset:32768
	ds_read_b128 v[206:209], v197 offset:33792
	ds_read_b128 v[222:225], v197 offset:34816
	ds_read_b128 v[226:229], v197 offset:35840
	ds_read_b128 v[230:233], v197 offset:36864
	ds_read_b128 v[234:237], v197 offset:37888
	ds_read_b128 v[238:241], v197 offset:38912
	ds_read_b128 v[242:245], v197 offset:39936
	global_load_lds_dwordx4 v[178:179], off
	v_lshl_add_u64 v[178:179], s[36:37], 0, v[166:167]
	s_mov_b32 m0, s44
	s_nop 0
	global_load_lds_dwordx4 v[178:179], off
	s_waitcnt vmcnt(8)
	s_waitcnt lgkmcnt(0)
	s_barrier
	s_setprio 0
	s_waitcnt lgkmcnt(0)
	v_mfma_f32_16x16x128_f8f6f4 v[160:163], v[26:33], v[202:209], v[160:163]
	v_mfma_f32_16x16x128_f8f6f4 v[156:159], v[18:25], v[202:209], v[156:159]
	v_mfma_f32_16x16x128_f8f6f4 v[148:151], v[18:25], v[222:229], v[148:151]
	v_mfma_f32_16x16x128_f8f6f4 v[152:155], v[26:33], v[222:229], v[152:155]
	v_mfma_f32_16x16x128_f8f6f4 v[144:147], v[26:33], v[230:237], v[144:147]
	v_mfma_f32_16x16x128_f8f6f4 v[140:143], v[18:25], v[230:237], v[140:143]
	v_mfma_f32_16x16x128_f8f6f4 v[132:135], v[18:25], v[238:245], v[132:135]
	v_mfma_f32_16x16x128_f8f6f4 v[136:139], v[26:33], v[238:245], v[136:139]
	s_setprio 3
	s_setprio 0
	v_mfma_f32_16x16x128_f8f6f4 v[128:131], v[10:17], v[202:209], v[128:131]
	v_mfma_f32_16x16x128_f8f6f4 v[124:127], v[2:9], v[202:209], v[124:127]
	v_mfma_f32_16x16x128_f8f6f4 v[116:119], v[2:9], v[222:229], v[116:119]
	v_mfma_f32_16x16x128_f8f6f4 v[120:123], v[10:17], v[222:229], v[120:123]
	v_mfma_f32_16x16x128_f8f6f4 v[112:115], v[10:17], v[230:237], v[112:115]
	v_mfma_f32_16x16x128_f8f6f4 v[108:111], v[2:9], v[230:237], v[108:111]
	v_mfma_f32_16x16x128_f8f6f4 v[100:103], v[2:9], v[238:245], v[100:103]
	v_mfma_f32_16x16x128_f8f6f4 v[104:107], v[10:17], v[238:245], v[104:107]
	s_setprio 3
	s_barrier
	s_mov_b32 m0, s64
	v_lshl_add_u64 v[174:175], v[174:175], 0, s[18:19]
	s_add_u32 s22, s22, 0x20080
	ds_read_b128 v[202:205], v197 offset:49152
	ds_read_b128 v[206:209], v197 offset:50176
	ds_read_b128 v[222:225], v197 offset:51200
	ds_read_b128 v[226:229], v197 offset:52224
	ds_read_b128 v[230:233], v197 offset:53248
	ds_read_b128 v[234:237], v197 offset:54272
	ds_read_b128 v[238:241], v197 offset:55296
	ds_read_b128 v[242:245], v197 offset:56320
	global_load_lds_dwordx4 v[174:175], off
	v_lshl_add_u64 v[174:175], v[190:191], 0, s[18:19]
	s_mov_b32 m0, s65
	s_addc_u32 s23, s23, 0
	global_load_lds_dwordx4 v[174:175], off
	v_lshl_add_u64 v[174:175], s[22:23], 0, v[34:35]
	s_mov_b32 m0, s66
	s_nop 0
	global_load_lds_dwordx4 v[174:175], off
	v_lshl_add_u64 v[174:175], s[22:23], 0, v[164:165]
	s_mov_b32 m0, s67
	s_nop 0
	global_load_lds_dwordx4 v[174:175], off
	v_lshl_add_u64 v[174:175], v[192:193], 0, s[18:19]
	s_mov_b32 m0, s47
	s_nop 0
	global_load_lds_dwordx4 v[174:175], off
	v_lshl_add_u64 v[174:175], v[194:195], 0, s[18:19]
	s_mov_b32 m0, s48
	s_nop 0
	global_load_lds_dwordx4 v[174:175], off
	s_waitcnt vmcnt(8)
	s_waitcnt lgkmcnt(0)
	s_barrier
	s_setprio 0
	s_waitcnt lgkmcnt(0)
	v_mfma_f32_16x16x128_f8f6f4 v[96:99], v[26:33], v[202:209], v[96:99]
	v_mfma_f32_16x16x128_f8f6f4 v[92:95], v[18:25], v[202:209], v[92:95]
	v_mfma_f32_16x16x128_f8f6f4 v[84:87], v[18:25], v[222:229], v[84:87]
	v_mfma_f32_16x16x128_f8f6f4 v[88:91], v[26:33], v[222:229], v[88:91]
	v_mfma_f32_16x16x128_f8f6f4 v[80:83], v[26:33], v[230:237], v[80:83]
	v_mfma_f32_16x16x128_f8f6f4 v[76:79], v[18:25], v[230:237], v[76:79]
	v_mfma_f32_16x16x128_f8f6f4 v[68:71], v[18:25], v[238:245], v[68:71]
	v_mfma_f32_16x16x128_f8f6f4 v[72:75], v[26:33], v[238:245], v[72:75]
	s_setprio 3
	s_setprio 0
	v_mfma_f32_16x16x128_f8f6f4 v[64:67], v[10:17], v[202:209], v[64:67]
	v_mfma_f32_16x16x128_f8f6f4 v[60:63], v[2:9], v[202:209], v[60:63]
	v_mfma_f32_16x16x128_f8f6f4 v[52:55], v[2:9], v[222:229], v[52:55]
	v_mfma_f32_16x16x128_f8f6f4 v[56:59], v[10:17], v[222:229], v[56:59]
	v_mfma_f32_16x16x128_f8f6f4 v[48:51], v[10:17], v[230:237], v[48:51]
	v_mfma_f32_16x16x128_f8f6f4 v[44:47], v[2:9], v[230:237], v[44:47]
	v_mfma_f32_16x16x128_f8f6f4 v[36:39], v[2:9], v[238:245], v[36:39]
	v_mfma_f32_16x16x128_f8f6f4 v[40:43], v[10:17], v[238:245], v[40:43]
	s_setprio 3
	s_barrier
	s_add_i32 s70, s70, 2
	s_add_u32 s30, s30, 0x100
	s_addc_u32 s31, s31, 0
	s_add_u32 s68, s68, 0x100
	s_addc_u32 s69, s69, 0
	s_cmp_gt_u32 s70, 5
	s_cbranch_scc0 .LBB0_1087

.LBB0_1160:
	s_add_u32 s22, s30, 0x100
	s_addc_u32 s23, s31, 0
	s_add_i32 s65, 0, 0x10000
	s_cmp_eq_u32 s64, 18
	s_cselect_b32 s41, s58, s23
	s_cselect_b32 s40, s59, s22
	s_cselect_b32 s37, s60, s63
	s_cselect_b32 s36, s61, s62
	s_add_i32 s66, 0, 0x14000
	v_add_u32_e32 v2, s65, v222
	v_add_u32_e32 v6, s66, v222
	ds_read_b128 v[26:29], v2
	ds_read_b128 v[30:33], v2 offset:1024
	ds_read_b128 v[18:21], v2 offset:2048
	ds_read_b128 v[22:25], v2 offset:3072
	ds_read_b128 v[10:13], v6
	ds_read_b128 v[14:17], v6 offset:1024
	ds_read_b128 v[2:5], v6 offset:2048
	ds_read_b128 v[6:9], v6 offset:3072
	v_lshl_add_u64 v[174:175], s[30:31], 0, v[170:171]
	s_add_i32 m0, s43, 0xc000
	ds_read_b128 v[190:193], v223
	ds_read_b128 v[194:197], v223 offset:1024
	ds_read_b128 v[198:201], v223 offset:2048
	ds_read_b128 v[202:205], v223 offset:3072
	ds_read_b128 v[224:227], v223 offset:4096
	ds_read_b128 v[228:231], v223 offset:5120
	ds_read_b128 v[232:235], v223 offset:6144
	ds_read_b128 v[236:239], v223 offset:7168
	global_load_lds_dwordx4 v[174:175], off
	v_lshl_add_u64 v[174:175], s[30:31], 0, v[172:173]
	s_add_i32 m0, s43, 0xe000
	s_nop 0
	global_load_lds_dwordx4 v[174:175], off
	s_waitcnt vmcnt(8)
	s_waitcnt lgkmcnt(0)
	s_barrier
	s_setprio 0
	s_waitcnt lgkmcnt(0)
	v_mfma_f32_16x16x128_f8f6f4 v[160:163], v[26:33], v[190:197], v[160:163]
	v_mfma_f32_16x16x128_f8f6f4 v[156:159], v[18:25], v[190:197], v[156:159]
	v_mfma_f32_16x16x128_f8f6f4 v[140:143], v[18:25], v[198:205], v[140:143]
	v_mfma_f32_16x16x128_f8f6f4 v[144:147], v[26:33], v[198:205], v[144:147]
	v_mfma_f32_16x16x128_f8f6f4 v[132:135], v[26:33], v[224:231], v[132:135]
	v_mfma_f32_16x16x128_f8f6f4 v[124:127], v[18:25], v[224:231], v[124:127]
	v_mfma_f32_16x16x128_f8f6f4 v[108:111], v[18:25], v[232:239], v[108:111]
	v_mfma_f32_16x16x128_f8f6f4 v[116:119], v[26:33], v[232:239], v[116:119]
	s_setprio 3
	s_setprio 0
	v_mfma_f32_16x16x128_f8f6f4 v[152:155], v[10:17], v[190:197], v[152:155]
	v_mfma_f32_16x16x128_f8f6f4 v[148:151], v[2:9], v[190:197], v[148:151]
	v_mfma_f32_16x16x128_f8f6f4 v[128:131], v[2:9], v[198:205], v[128:131]
	v_mfma_f32_16x16x128_f8f6f4 v[136:139], v[10:17], v[198:205], v[136:139]
	v_mfma_f32_16x16x128_f8f6f4 v[120:123], v[10:17], v[224:231], v[120:123]
	v_mfma_f32_16x16x128_f8f6f4 v[112:115], v[2:9], v[224:231], v[112:115]
	v_mfma_f32_16x16x128_f8f6f4 v[100:103], v[2:9], v[232:239], v[100:103]
	v_mfma_f32_16x16x128_f8f6f4 v[104:107], v[10:17], v[232:239], v[104:107]
	s_setprio 3
	s_barrier
	s_add_i32 s14, s65, s42
	v_lshl_add_u64 v[174:175], s[36:37], 0, v[34:35]
	s_mov_b32 m0, s14
	ds_read_b128 v[196:199], v223 offset:16384
	ds_read_b128 v[200:203], v223 offset:17408
	ds_read_b128 v[204:207], v223 offset:18432
	ds_read_b128 v[208:211], v223 offset:19456
	ds_read_b128 v[224:227], v223 offset:20480
	ds_read_b128 v[228:231], v223 offset:21504
	ds_read_b128 v[232:235], v223 offset:22528
	ds_read_b128 v[236:239], v223 offset:23552
	global_load_lds_dwordx4 v[174:175], off
	s_add_i32 m0, s14, 0x2000
	s_add_u32 s30, s36, 0x58000
	v_lshl_add_u64 v[190:191], s[36:37], 0, v[164:165]
	s_addc_u32 s31, s37, 0
	s_add_i32 s14, s66, s42
	global_load_lds_dwordx4 v[190:191], off
	v_lshl_add_u64 v[178:179], s[30:31], 0, v[34:35]
	s_mov_b32 m0, s14
	v_lshl_add_u64 v[192:193], s[40:41], 0, v[168:169]
	global_load_lds_dwordx4 v[178:179], off
	v_lshl_add_u64 v[178:179], s[30:31], 0, v[164:165]
	s_add_i32 m0, s14, 0x2000
	v_lshl_add_u64 v[194:195], s[40:41], 0, v[166:167]
	global_load_lds_dwordx4 v[178:179], off
	s_mov_b32 m0, s43
	s_nop 0
	global_load_lds_dwordx4 v[192:193], off
	s_mov_b32 m0, s44
	s_nop 0
	global_load_lds_dwordx4 v[194:195], off
	s_waitcnt vmcnt(8)
	s_waitcnt lgkmcnt(0)
	s_barrier
	s_setprio 0
	s_waitcnt lgkmcnt(0)
	v_mfma_f32_16x16x128_f8f6f4 v[96:99], v[26:33], v[196:203], v[96:99]
	v_mfma_f32_16x16x128_f8f6f4 v[92:95], v[18:25], v[196:203], v[92:95]
	v_mfma_f32_16x16x128_f8f6f4 v[76:79], v[18:25], v[204:211], v[76:79]
	v_mfma_f32_16x16x128_f8f6f4 v[84:87], v[26:33], v[204:211], v[84:87]
	v_mfma_f32_16x16x128_f8f6f4 v[68:71], v[26:33], v[224:231], v[68:71]
	v_mfma_f32_16x16x128_f8f6f4 v[60:63], v[18:25], v[224:231], v[60:63]
	v_mfma_f32_16x16x128_f8f6f4 v[44:47], v[18:25], v[232:239], v[44:47]
	v_mfma_f32_16x16x128_f8f6f4 v[52:55], v[26:33], v[232:239], v[52:55]
	s_setprio 3
	s_setprio 0
	v_mfma_f32_16x16x128_f8f6f4 v[88:91], v[10:17], v[196:203], v[88:91]
	v_mfma_f32_16x16x128_f8f6f4 v[80:83], v[2:9], v[196:203], v[80:83]
	v_mfma_f32_16x16x128_f8f6f4 v[64:67], v[2:9], v[204:211], v[64:67]
	v_mfma_f32_16x16x128_f8f6f4 v[72:75], v[10:17], v[204:211], v[72:75]
	v_mfma_f32_16x16x128_f8f6f4 v[56:59], v[10:17], v[224:231], v[56:59]
	v_mfma_f32_16x16x128_f8f6f4 v[48:51], v[2:9], v[224:231], v[48:51]
	v_mfma_f32_16x16x128_f8f6f4 v[36:39], v[2:9], v[232:239], v[36:39]
	v_mfma_f32_16x16x128_f8f6f4 v[40:43], v[10:17], v[232:239], v[40:43]
	s_setprio 3
	s_barrier
	s_add_i32 s14, 0, 0x18000
	s_add_i32 s65, 0, 0x1c000
	v_add_u32_e32 v14, s14, v222
	v_add_u32_e32 v30, s65, v222
	ds_read_b128 v[2:5], v14
	ds_read_b128 v[6:9], v14 offset:1024
	ds_read_b128 v[10:13], v14 offset:2048
	ds_read_b128 v[14:17], v14 offset:3072
	ds_read_b128 v[18:21], v30
	ds_read_b128 v[22:25], v30 offset:1024
	ds_read_b128 v[26:29], v30 offset:2048
	ds_read_b128 v[30:33], v30 offset:3072
	s_add_u32 s30, s40, 0x58000
	s_addc_u32 s31, s41, 0
	s_mov_b32 m0, s45
	v_lshl_add_u64 v[178:179], s[30:31], 0, v[168:169]
	ds_read_b128 v[196:199], v223 offset:32768
	ds_read_b128 v[200:203], v223 offset:33792
	ds_read_b128 v[204:207], v223 offset:34816
	ds_read_b128 v[208:211], v223 offset:35840
	ds_read_b128 v[224:227], v223 offset:36864
	ds_read_b128 v[228:231], v223 offset:37888
	ds_read_b128 v[232:235], v223 offset:38912
	ds_read_b128 v[236:239], v223 offset:39936
	global_load_lds_dwordx4 v[178:179], off
	v_lshl_add_u64 v[178:179], s[30:31], 0, v[166:167]
	s_mov_b32 m0, s46
	s_nop 0
	global_load_lds_dwordx4 v[178:179], off
	s_waitcnt vmcnt(8)
	s_waitcnt lgkmcnt(0)
	s_barrier
	s_setprio 0
	s_waitcnt lgkmcnt(0)
	v_mfma_f32_16x16x128_f8f6f4 v[160:163], v[2:9], v[196:203], v[160:163]
	v_mfma_f32_16x16x128_f8f6f4 v[156:159], v[10:17], v[196:203], v[156:159]
	v_mfma_f32_16x16x128_f8f6f4 v[140:143], v[10:17], v[204:211], v[140:143]
	v_mfma_f32_16x16x128_f8f6f4 v[144:147], v[2:9], v[204:211], v[144:147]
	v_mfma_f32_16x16x128_f8f6f4 v[132:135], v[2:9], v[224:231], v[132:135]
	v_mfma_f32_16x16x128_f8f6f4 v[124:127], v[10:17], v[224:231], v[124:127]
	v_mfma_f32_16x16x128_f8f6f4 v[108:111], v[10:17], v[232:239], v[108:111]
	v_mfma_f32_16x16x128_f8f6f4 v[116:119], v[2:9], v[232:239], v[116:119]
	s_setprio 3
	s_setprio 0
	v_mfma_f32_16x16x128_f8f6f4 v[152:155], v[18:25], v[196:203], v[152:155]
	v_mfma_f32_16x16x128_f8f6f4 v[148:151], v[26:33], v[196:203], v[148:151]
	v_mfma_f32_16x16x128_f8f6f4 v[128:131], v[26:33], v[204:211], v[128:131]
	v_mfma_f32_16x16x128_f8f6f4 v[136:139], v[18:25], v[204:211], v[136:139]
	v_mfma_f32_16x16x128_f8f6f4 v[120:123], v[18:25], v[224:231], v[120:123]
	v_mfma_f32_16x16x128_f8f6f4 v[112:115], v[26:33], v[224:231], v[112:115]
	v_mfma_f32_16x16x128_f8f6f4 v[100:103], v[26:33], v[232:239], v[100:103]
	v_mfma_f32_16x16x128_f8f6f4 v[104:107], v[18:25], v[232:239], v[104:107]
	s_setprio 3
	s_barrier
	s_add_i32 s14, s14, s42
	v_lshl_add_u64 v[174:175], v[174:175], 0, s[18:19]
	s_mov_b32 m0, s14
	ds_read_b128 v[196:199], v223 offset:49152
	ds_read_b128 v[200:203], v223 offset:50176
	ds_read_b128 v[204:207], v223 offset:51200
	ds_read_b128 v[208:211], v223 offset:52224
	ds_read_b128 v[224:227], v223 offset:53248
	ds_read_b128 v[228:231], v223 offset:54272
	ds_read_b128 v[232:235], v223 offset:55296
	ds_read_b128 v[236:239], v223 offset:56320
	global_load_lds_dwordx4 v[174:175], off
	s_add_i32 m0, s14, 0x2000
	s_add_u32 s30, s36, 0x58080
	v_lshl_add_u64 v[174:175], v[190:191], 0, s[18:19]
	s_addc_u32 s31, s37, 0
	s_add_i32 s14, s65, s42
	global_load_lds_dwordx4 v[174:175], off
	v_lshl_add_u64 v[174:175], s[30:31], 0, v[34:35]
	s_mov_b32 m0, s14
	s_nop 0
	global_load_lds_dwordx4 v[174:175], off
	v_lshl_add_u64 v[174:175], s[30:31], 0, v[164:165]
	s_add_i32 m0, s14, 0x2000
	s_nop 0
	global_load_lds_dwordx4 v[174:175], off
	v_lshl_add_u64 v[174:175], v[192:193], 0, s[18:19]
	s_mov_b32 m0, s51
	s_nop 0
	global_load_lds_dwordx4 v[174:175], off
	v_lshl_add_u64 v[174:175], v[194:195], 0, s[18:19]
	s_mov_b32 m0, s52
	s_nop 0
	global_load_lds_dwordx4 v[174:175], off
	s_waitcnt vmcnt(8)
	s_waitcnt lgkmcnt(0)
	s_barrier
	s_setprio 0
	s_waitcnt lgkmcnt(0)
	v_mfma_f32_16x16x128_f8f6f4 v[96:99], v[2:9], v[196:203], v[96:99]
	v_mfma_f32_16x16x128_f8f6f4 v[92:95], v[10:17], v[196:203], v[92:95]
	v_mfma_f32_16x16x128_f8f6f4 v[76:79], v[10:17], v[204:211], v[76:79]
	v_mfma_f32_16x16x128_f8f6f4 v[84:87], v[2:9], v[204:211], v[84:87]
	v_mfma_f32_16x16x128_f8f6f4 v[68:71], v[2:9], v[224:231], v[68:71]
	v_mfma_f32_16x16x128_f8f6f4 v[60:63], v[10:17], v[224:231], v[60:63]
	v_mfma_f32_16x16x128_f8f6f4 v[44:47], v[10:17], v[232:239], v[44:47]
	v_mfma_f32_16x16x128_f8f6f4 v[52:55], v[2:9], v[232:239], v[52:55]
	s_setprio 3
	s_setprio 0
	v_mfma_f32_16x16x128_f8f6f4 v[88:91], v[18:25], v[196:203], v[88:91]
	v_mfma_f32_16x16x128_f8f6f4 v[80:83], v[26:33], v[196:203], v[80:83]
	v_mfma_f32_16x16x128_f8f6f4 v[64:67], v[26:33], v[204:211], v[64:67]
	v_mfma_f32_16x16x128_f8f6f4 v[72:75], v[18:25], v[204:211], v[72:75]
	v_mfma_f32_16x16x128_f8f6f4 v[56:59], v[18:25], v[224:231], v[56:59]
	v_mfma_f32_16x16x128_f8f6f4 v[48:51], v[26:33], v[224:231], v[48:51]
	v_mfma_f32_16x16x128_f8f6f4 v[36:39], v[26:33], v[232:239], v[36:39]
	v_mfma_f32_16x16x128_f8f6f4 v[40:43], v[18:25], v[232:239], v[40:43]
	s_setprio 3
	s_barrier
	s_add_i32 s64, s64, 2
	s_add_u32 s62, s62, 0x100
	s_addc_u32 s63, s63, 0
	s_cmp_gt_u32 s64, 19
	s_mov_b64 s[30:31], s[22:23]
	s_cbranch_scc0 .LBB0_1160
	s_and_b64 vcc, exec, s[8:9]
	s_mov_b32 s58, 0x19b00000
	v_readlane_b32 s59, v255, 10
	s_mov_b32 s60, 0xff61b1e6
	s_mov_b64 s[62:63], 0x800
	s_cbranch_vccz .LBB0_1163
	s_barrier
